# speedup vs baseline: 1.0063x; 1.0063x over previous
.LBB1_26:
	s_waitcnt vmcnt(35)
	v_and_b32_e32 v113, 3, v0
	s_and_b32 s18, s2, 15
	v_cmp_eq_u32_e32 vcc, 0, v113
	v_cmp_gt_u32_e64 s[4:5], 12, v92
	s_and_b64 s[12:13], vcc, s[4:5]
	s_lshl_b32 s4, s3, 12
	s_lshl_b32 s5, s18, 8
	s_or_b32 s4, s4, s5
	s_mul_hi_i32 s5, s4, 0x6000
	s_mulk_i32 s4, 0x6000
	s_lshl_b32 s3, s3, 8
	s_add_u32 s16, s24, s4
	s_addc_u32 s17, s25, s5
	s_ashr_i32 s4, s21, 31
	s_lshr_b32 s4, s4, 29
	s_add_i32 s4, s21, s4
	s_ashr_i32 s19, s4, 3
	v_and_b32_e32 v101, 1, v74
	v_lshl_or_b32 v74, v91, 1, v95
	s_min_i32 s4, s19, 0xff
	v_mul_u32_u24_e32 v74, 0x60, v74
	v_lshlrev_b32_e32 v75, 1, v92
	s_mul_hi_i32 s5, s4, 0x6000
	s_mulk_i32 s4, 0x6000
	v_or3_b32 v88, v74, v75, v101
	s_add_u32 s4, s16, s4
	s_addc_u32 s5, s17, s5
	v_lshlrev_b64 v[102:103], 4, v[88:89]
	v_lshl_add_u64 v[104:105], s[4:5], 0, v[102:103]
	global_load_dwordx4 v[82:85], v[104:105], off
	global_load_dwordx4 v[74:77], v[104:105], off offset:512
	global_load_dwordx4 v[78:81], v[104:105], off offset:1024
	s_waitcnt vmcnt(5)
	v_mul_f32_e32 v88, 0xbfb8aa3b, v97
	v_mul_f32_e32 v99, 0x3c91a2b4, v88
	s_waitcnt vmcnt(4)
	v_mul_f32_e32 v88, 0x4038aa3b, v96
	v_mul_f32_e32 v104, 0x3c91a2b4, v88
	v_lshrrev_b32_e32 v88, 2, v92
	v_and_b32_e32 v92, 4, v92
	v_cmp_lt_u32_e64 s[4:5], 1, v93
	v_mov_b32_e32 v93, 0xd0
	v_cmp_ne_u32_e32 vcc, 0, v92
	v_lshlrev_b32_e32 v107, 3, v88
	v_sub_u32_e32 v88, 0, v107
	v_cndmask_b32_e32 v92, 0, v93, vcc
	v_add_u32_e32 v106, v92, v86
	v_and_b32_e32 v92, 12, v0
	v_mul_u32_u24_e32 v86, 0xd0, v101
	v_mad_u32_u24 v91, v91, 24, v92
	v_mul_u32_u24_e32 v93, 12, v95
	v_lshlrev_b32_e32 v92, 20, v101
	v_add3_u32 v112, v91, v86, v93
	v_lshl_or_b32 v86, s18, 21, v90
	v_add3_u32 v86, v86, s3, v92
	v_mul_f32_e32 v1, 0xbfb8aa3b, v1
	v_and_b32_e32 v114, 24, v88
	v_or_b32_e32 v88, v86, v94
	s_min_i32 s3, s19, 0xfe
	v_mul_f32_e32 v1, 0x3c91a2b4, v1
	s_waitcnt vmcnt(3)
	v_mul_f32_e32 v105, 0x4038aa3b, v100
	v_add_u32_e32 v108, 16, v106
	v_add_u32_e32 v109, 0x70, v106
	v_add_u32_e32 v110, 0x1b0, v106
	v_add_u32_e32 v111, 0x210, v106
	v_mul_u32_u24_e32 v113, 6, v113
	s_add_i32 s19, s3, 1
	v_lshl_add_u64 v[100:101], s[16:17], 0, v[102:103]
	v_lshl_add_u64 v[102:103], v[88:89], 1, s[14:15]
	s_sub_i32 s3, 0x7ff, s21
	v_mov_b32_e32 v115, 0x7f7f7f7f
	s_mov_b32 s16, 0x42700000
	s_mov_b32 s17, 0x41f00000
	s_mov_b32 s18, 0x41700000
	v_mov_b32_e32 v116, 0x6000
	v_mov_b32_e32 v117, 0x4b400000
	v_mov_b32_e32 v118, 0x4b400008
	v_mov_b32_e32 v119, 0x4b400010
	v_mbcnt_lo_u32_b32 v200, -1, 0
	v_mbcnt_hi_u32_b32 v200, -1, v200
	v_and_b32_e32 v201, 3, v200
	v_and_b32_e32 v202, 15, v200
	v_cmp_gt_u32_e32 vcc, 8, v202
	s_nop 1
	v_cndmask_b32_e64 v178, 0, v115, vcc
	v_cndmask_b32_e64 v179, v115, 0, vcc
	v_lshlrev_b32_e32 v181, 1, v201
	v_sub_u32_e32 v202, 22, v181
	v_lshlrev_b32_e64 v180, v202, 1
	v_sub_u32_e32 v202, 16, v181
	v_lshlrev_b32_e64 v181, v202, 1
	v_readfirstlane_b32 s51, v112
	v_lshrrev_b32_e32 v202, 4, v200
	v_lshlrev_b32_e32 v192, 5, v202
	v_bfe_u32 v202, v200, 2, 1
	v_mul_u32_u24_e32 v202, 0x110, v202
	v_add_u32_e32 v192, v192, v202
	s_mul_i32 s46, s51, 0xaaab
	s_lshr_b32 s46, s46, 15
	v_bfe_u32 v202, v200, 4, 1
	v_mul_u32_u24_e32 v184, 0x110, v202
	v_lshrrev_b32_e32 v202, 5, v200
	v_mul_u32_u24_e32 v202, 12, v202
	v_add_u32_e32 v184, v184, v202
	v_bfe_u32 v202, v200, 2, 2
	v_mul_u32_u24_e32 v164, 3, v202
	v_add3_u32 v184, v184, v164, v201
	v_add_u32_e32 v184, s46, v184
	v_add_u32_e32 v202, 0x100, v202
	v_cmp_eq_u32_e32 vcc, 3, v201
	s_nop 1
	v_cndmask_b32_e32 v184, v184, v202, vcc
	v_subrev_u32_e32 v185, s14, v102
	s_mov_b32 s44, s21
	s_mov_b32 s45, s22
	s_lshr_b32 s46, s44, 3
	s_add_i32 s46, s46, 1
	s_mul_i32 s46, s46, 0x6000
	s_mov_b32 s47, 0
	v_lshl_add_u64 v[196:197], v[100:101], 0, s[46:47]
	s_mov_b32 s42, 0x6000
	s_mov_b32 s43, 0
	s_sub_i32 s46, s44, 1
	s_sub_i32 s47, 0x800, s44
	s_and_b64 s[40:41], s[6:7], exec
	s_cselect_b32 s46, s46, s47
	s_cselect_b32 s41, 0, -1
	s_xor_b32 s40, s41, 0x400
	s_sub_i32 s40, s40, s41
	s_ashr_i32 s47, s46, 31
	s_lshl_b64 s[46:47], s[46:47], 10
	s_add_u32 s48, s14, s46
	s_addc_u32 s49, s15, s47
	s_waitcnt vmcnt(0) lgkmcnt(0)
	v_mov_b32_e32 v176, v87
	v_add_f32_e32 v169, -1.0, v87
	v_rcp_f32_e32 v186, v104
	s_nop 1
	v_mul_f32_e32 v188, v105, v186
	v_mov_b32_e32 v189, 0
	v_mov_b32_e32 v190, 0
	v_mov_b32_e32 v191, 0
	s_nop 1
	s_cmp_lt_i32 s44, s45
	s_cbranch_scc0 .Lscan_exit_st
	ds_read_b128 v[122:125], v192
	ds_read_b64 v[126:127], v192 offset:16
	s_waitcnt lgkmcnt(0)
	s_cmp_lt_u32 s51, 96
	s_cbranch_scc0 .Lscan_entry_b_st
	s_branch .Lscan_enter_a_st
	.p2align 6

.Lscan_enter_a_st:
	ds_read_b128 v[128:131], v192 offset:128
	ds_read_b64 v[132:133], v192 offset:144
	s_waitcnt vmcnt(8)
	global_load_dwordx4 v[146:149], v[196:197], off
	global_load_dwordx4 v[150:153], v[196:197], off offset:512
	global_load_dwordx4 v[154:157], v[196:197], off offset:1024
	v_lshl_add_u64 v[196:197], v[196:197], 0, s[42:43]
	s_waitcnt lgkmcnt(2)
	v_mfma_f32_16x16x128_f8f6f4 v[134:137], v[122:127], v[2:7], 0 cbsz:2 blgp:2
	v_mfma_f32_16x16x128_f8f6f4 v[138:141], v[122:127], v[14:19], 0 cbsz:2 blgp:2
	v_mfma_f32_16x16x128_f8f6f4 v[142:145], v[122:127], v[26:31], v[188:191] cbsz:2 blgp:2
	v_mfma_f32_16x16x128_f8f6f4 v[204:207], v[122:127], v[38:43], 0 cbsz:2 blgp:2
	v_mfma_f32_16x16x128_f8f6f4 v[208:211], v[122:127], v[50:55], 0 cbsz:2 blgp:2
	v_mfma_f32_16x16x128_f8f6f4 v[212:215], v[122:127], v[62:67], v[188:191] cbsz:2 blgp:2
	s_waitcnt lgkmcnt(0)
	v_mfma_f32_16x16x128_f8f6f4 v[134:137], v[128:133], v[8:13], v[134:137] cbsz:2 blgp:2
	v_mfma_f32_16x16x128_f8f6f4 v[204:207], v[128:133], v[44:49], v[204:207] cbsz:2 blgp:2
	v_mfma_f32_16x16x128_f8f6f4 v[138:141], v[128:133], v[20:25], v[138:141] cbsz:2 blgp:2
	v_mfma_f32_16x16x128_f8f6f4 v[208:211], v[128:133], v[56:61], v[208:211] cbsz:2 blgp:2
	v_mfma_f32_16x16x128_f8f6f4 v[142:145], v[128:133], v[32:37], v[142:145] cbsz:2 blgp:2
	v_mfma_f32_16x16x128_f8f6f4 v[212:215], v[128:133], v[68:73], v[212:215] cbsz:2 blgp:2
	v_cndmask_b32_e64 v158, v134, v204, s[4:5]
	v_cndmask_b32_e64 v159, v138, v208, s[4:5]
	v_fma_mix_f32 v158, v158, v1, v82 op_sel_hi:[0,0,1]
	v_fma_mix_f32 v159, v159, v99, v74 op_sel_hi:[0,0,1]
	v_exp_f32_e32 v158, v158
	v_exp_f32_e32 v159, v159
	v_fma_f32 v158, v158, v186, v186
	v_add_f32_e32 v159, 1.0, v159
	v_rcp_f32_e32 v158, v158
	v_rcp_f32_e32 v159, v159
	v_cndmask_b32_e64 v160, v142, v212, s[4:5]
	v_fma_mix_f32 v161, v158, v160, v78 op_sel_hi:[0,0,1]
	v_exp_f32_e32 v161, v161
	s_add_u32 s48, s48, s40
	v_add_f32_e32 v161, 1.0, v161
	v_rcp_f32_e32 v161, v161
	s_addc_u32 s49, s49, s41
	v_fma_f32 v162, v161, -2.0, 1.0
	v_sub_f32_e32 v163, v176, v162
	v_fma_f32 v176, v159, v163, v162
	v_fma_f32 v164, |v176|, s16, v117
	v_fma_f32 v165, |v176|, s17, v118
	v_fma_f32 v166, |v176|, s18, v119
	v_lshrrev_b32_e32 v167, 26, v176
	v_min3_u32 v164, v164, v165, v166
	v_bfi_b32 v168, 31, v164, v167
	s_nop 1
	v_mul_u32_u24_dpp v170, v168, v180 quad_perm:[1,2,3,3] row_mask:0xf bank_mask:0xf bound_ctrl:1
	v_mad_u32_u24 v171, v168, v181, v170
	ds_write_b8_d16_hi v184, v171 offset:544
	global_store_short_d16_hi v185, v176, s[48:49]
	s_waitcnt lgkmcnt(0)
	s_barrier
	ds_read_b128 v[122:125], v192 offset:544
	ds_read_b64 v[126:127], v192 offset:560
	s_barrier
	ds_read_b128 v[128:131], v192 offset:672
	ds_read_b64 v[132:133], v192 offset:688
	s_waitcnt lgkmcnt(2)
	v_mfma_f32_16x16x128_f8f6f4 v[134:137], v[122:127], v[2:7], 0 cbsz:2 blgp:2
	v_mfma_f32_16x16x128_f8f6f4 v[138:141], v[122:127], v[14:19], 0 cbsz:2 blgp:2
	v_mfma_f32_16x16x128_f8f6f4 v[142:145], v[122:127], v[26:31], v[188:191] cbsz:2 blgp:2
	v_mfma_f32_16x16x128_f8f6f4 v[204:207], v[122:127], v[38:43], 0 cbsz:2 blgp:2
	v_mfma_f32_16x16x128_f8f6f4 v[208:211], v[122:127], v[50:55], 0 cbsz:2 blgp:2
	v_mfma_f32_16x16x128_f8f6f4 v[212:215], v[122:127], v[62:67], v[188:191] cbsz:2 blgp:2
	s_waitcnt lgkmcnt(0)
	v_mfma_f32_16x16x128_f8f6f4 v[134:137], v[128:133], v[8:13], v[134:137] cbsz:2 blgp:2
	v_mfma_f32_16x16x128_f8f6f4 v[204:207], v[128:133], v[44:49], v[204:207] cbsz:2 blgp:2
	v_mfma_f32_16x16x128_f8f6f4 v[138:141], v[128:133], v[20:25], v[138:141] cbsz:2 blgp:2
	v_mfma_f32_16x16x128_f8f6f4 v[208:211], v[128:133], v[56:61], v[208:211] cbsz:2 blgp:2
	v_mfma_f32_16x16x128_f8f6f4 v[142:145], v[128:133], v[32:37], v[142:145] cbsz:2 blgp:2
	v_mfma_f32_16x16x128_f8f6f4 v[212:215], v[128:133], v[68:73], v[212:215] cbsz:2 blgp:2
	v_cndmask_b32_e64 v158, v134, v204, s[4:5]
	v_cndmask_b32_e64 v159, v138, v208, s[4:5]
	v_fma_mix_f32 v158, v158, v1, v82 op_sel:[0,0,1] op_sel_hi:[0,0,1]
	v_fma_mix_f32 v159, v159, v99, v74 op_sel:[0,0,1] op_sel_hi:[0,0,1]
	v_exp_f32_e32 v158, v158
	v_exp_f32_e32 v159, v159
	v_fma_f32 v158, v158, v186, v186
	v_add_f32_e32 v159, 1.0, v159
	v_rcp_f32_e32 v158, v158
	v_rcp_f32_e32 v159, v159
	v_cndmask_b32_e64 v160, v142, v212, s[4:5]
	v_fma_mix_f32 v161, v158, v160, v78 op_sel:[0,0,1] op_sel_hi:[0,0,1]
	v_exp_f32_e32 v161, v161
	s_add_u32 s48, s48, s40
	v_add_f32_e32 v161, 1.0, v161
	v_rcp_f32_e32 v161, v161
	s_addc_u32 s49, s49, s41
	v_fma_f32 v162, v161, -2.0, 1.0
	v_sub_f32_e32 v163, v176, v162
	v_fma_f32 v176, v159, v163, v162
	v_fma_f32 v164, |v176|, s16, v117
	v_fma_f32 v165, |v176|, s17, v118
	v_fma_f32 v166, |v176|, s18, v119
	v_lshrrev_b32_e32 v167, 26, v176
	v_min3_u32 v164, v164, v165, v166
	v_bfi_b32 v168, 31, v164, v167
	s_nop 1
	v_mul_u32_u24_dpp v170, v168, v180 quad_perm:[1,2,3,3] row_mask:0xf bank_mask:0xf bound_ctrl:1
	v_mad_u32_u24 v171, v168, v181, v170
	ds_write_b8_d16_hi v184, v171
	global_store_short_d16_hi v185, v176, s[48:49]
	s_waitcnt lgkmcnt(0)
	s_barrier
	ds_read_b128 v[122:125], v192 offset:0
	ds_read_b64 v[126:127], v192 offset:16
	s_barrier
	ds_read_b128 v[128:131], v192 offset:128
	ds_read_b64 v[132:133], v192 offset:144
	s_waitcnt lgkmcnt(2)
	v_mfma_f32_16x16x128_f8f6f4 v[134:137], v[122:127], v[2:7], 0 cbsz:2 blgp:2
	v_mfma_f32_16x16x128_f8f6f4 v[138:141], v[122:127], v[14:19], 0 cbsz:2 blgp:2
	v_mfma_f32_16x16x128_f8f6f4 v[142:145], v[122:127], v[26:31], v[188:191] cbsz:2 blgp:2
	v_mfma_f32_16x16x128_f8f6f4 v[204:207], v[122:127], v[38:43], 0 cbsz:2 blgp:2
	v_mfma_f32_16x16x128_f8f6f4 v[208:211], v[122:127], v[50:55], 0 cbsz:2 blgp:2
	v_mfma_f32_16x16x128_f8f6f4 v[212:215], v[122:127], v[62:67], v[188:191] cbsz:2 blgp:2
	s_waitcnt lgkmcnt(0)
	v_mfma_f32_16x16x128_f8f6f4 v[134:137], v[128:133], v[8:13], v[134:137] cbsz:2 blgp:2
	v_mfma_f32_16x16x128_f8f6f4 v[204:207], v[128:133], v[44:49], v[204:207] cbsz:2 blgp:2
	v_mfma_f32_16x16x128_f8f6f4 v[138:141], v[128:133], v[20:25], v[138:141] cbsz:2 blgp:2
	v_mfma_f32_16x16x128_f8f6f4 v[208:211], v[128:133], v[56:61], v[208:211] cbsz:2 blgp:2
	v_mfma_f32_16x16x128_f8f6f4 v[142:145], v[128:133], v[32:37], v[142:145] cbsz:2 blgp:2
	v_mfma_f32_16x16x128_f8f6f4 v[212:215], v[128:133], v[68:73], v[212:215] cbsz:2 blgp:2
	v_cndmask_b32_e64 v158, v134, v204, s[4:5]
	v_cndmask_b32_e64 v159, v138, v208, s[4:5]
	v_fma_mix_f32 v158, v158, v1, v83 op_sel_hi:[0,0,1]
	v_fma_mix_f32 v159, v159, v99, v75 op_sel_hi:[0,0,1]
	v_exp_f32_e32 v158, v158
	v_exp_f32_e32 v159, v159
	v_fma_f32 v158, v158, v186, v186
	v_add_f32_e32 v159, 1.0, v159
	v_rcp_f32_e32 v158, v158
	v_rcp_f32_e32 v159, v159
	v_cndmask_b32_e64 v160, v142, v212, s[4:5]
	v_fma_mix_f32 v161, v158, v160, v79 op_sel_hi:[0,0,1]
	v_exp_f32_e32 v161, v161
	s_add_u32 s48, s48, s40
	v_add_f32_e32 v161, 1.0, v161
	v_rcp_f32_e32 v161, v161
	s_addc_u32 s49, s49, s41
	v_fma_f32 v162, v161, -2.0, 1.0
	v_sub_f32_e32 v163, v176, v162
	v_fma_f32 v176, v159, v163, v162
	v_fma_f32 v164, |v176|, s16, v117
	v_fma_f32 v165, |v176|, s17, v118
	v_fma_f32 v166, |v176|, s18, v119
	v_lshrrev_b32_e32 v167, 26, v176
	v_min3_u32 v164, v164, v165, v166
	v_bfi_b32 v168, 31, v164, v167
	s_nop 1
	v_mul_u32_u24_dpp v170, v168, v180 quad_perm:[1,2,3,3] row_mask:0xf bank_mask:0xf bound_ctrl:1
	v_mad_u32_u24 v171, v168, v181, v170
	ds_write_b8_d16_hi v184, v171 offset:544
	global_store_short_d16_hi v185, v176, s[48:49]
	s_waitcnt lgkmcnt(0)
	s_barrier
	ds_read_b128 v[122:125], v192 offset:544
	ds_read_b64 v[126:127], v192 offset:560
	s_barrier
	ds_read_b128 v[128:131], v192 offset:672
	ds_read_b64 v[132:133], v192 offset:688
	s_waitcnt lgkmcnt(2)
	v_mfma_f32_16x16x128_f8f6f4 v[134:137], v[122:127], v[2:7], 0 cbsz:2 blgp:2
	v_mfma_f32_16x16x128_f8f6f4 v[138:141], v[122:127], v[14:19], 0 cbsz:2 blgp:2
	v_mfma_f32_16x16x128_f8f6f4 v[142:145], v[122:127], v[26:31], v[188:191] cbsz:2 blgp:2
	v_mfma_f32_16x16x128_f8f6f4 v[204:207], v[122:127], v[38:43], 0 cbsz:2 blgp:2
	v_mfma_f32_16x16x128_f8f6f4 v[208:211], v[122:127], v[50:55], 0 cbsz:2 blgp:2
	v_mfma_f32_16x16x128_f8f6f4 v[212:215], v[122:127], v[62:67], v[188:191] cbsz:2 blgp:2
	s_waitcnt lgkmcnt(0)
	v_mfma_f32_16x16x128_f8f6f4 v[134:137], v[128:133], v[8:13], v[134:137] cbsz:2 blgp:2
	v_mfma_f32_16x16x128_f8f6f4 v[204:207], v[128:133], v[44:49], v[204:207] cbsz:2 blgp:2
	v_mfma_f32_16x16x128_f8f6f4 v[138:141], v[128:133], v[20:25], v[138:141] cbsz:2 blgp:2
	v_mfma_f32_16x16x128_f8f6f4 v[208:211], v[128:133], v[56:61], v[208:211] cbsz:2 blgp:2
	v_mfma_f32_16x16x128_f8f6f4 v[142:145], v[128:133], v[32:37], v[142:145] cbsz:2 blgp:2
	v_mfma_f32_16x16x128_f8f6f4 v[212:215], v[128:133], v[68:73], v[212:215] cbsz:2 blgp:2
	v_cndmask_b32_e64 v158, v134, v204, s[4:5]
	v_cndmask_b32_e64 v159, v138, v208, s[4:5]
	v_fma_mix_f32 v158, v158, v1, v83 op_sel:[0,0,1] op_sel_hi:[0,0,1]
	v_fma_mix_f32 v159, v159, v99, v75 op_sel:[0,0,1] op_sel_hi:[0,0,1]
	v_exp_f32_e32 v158, v158
	v_exp_f32_e32 v159, v159
	v_fma_f32 v158, v158, v186, v186
	v_add_f32_e32 v159, 1.0, v159
	v_rcp_f32_e32 v158, v158
	v_rcp_f32_e32 v159, v159
	v_cndmask_b32_e64 v160, v142, v212, s[4:5]
	v_fma_mix_f32 v161, v158, v160, v79 op_sel:[0,0,1] op_sel_hi:[0,0,1]
	v_exp_f32_e32 v161, v161
	s_add_u32 s48, s48, s40
	v_add_f32_e32 v161, 1.0, v161
	v_rcp_f32_e32 v161, v161
	s_addc_u32 s49, s49, s41
	v_fma_f32 v162, v161, -2.0, 1.0
	v_sub_f32_e32 v163, v176, v162
	v_fma_f32 v176, v159, v163, v162
	v_fma_f32 v164, |v176|, s16, v117
	v_fma_f32 v165, |v176|, s17, v118
	v_fma_f32 v166, |v176|, s18, v119
	v_lshrrev_b32_e32 v167, 26, v176
	v_min3_u32 v164, v164, v165, v166
	v_bfi_b32 v168, 31, v164, v167
	s_nop 1
	v_mul_u32_u24_dpp v170, v168, v180 quad_perm:[1,2,3,3] row_mask:0xf bank_mask:0xf bound_ctrl:1
	v_mad_u32_u24 v171, v168, v181, v170
	ds_write_b8_d16_hi v184, v171
	global_store_short_d16_hi v185, v176, s[48:49]
	s_waitcnt lgkmcnt(0)
	s_barrier
	ds_read_b128 v[122:125], v192 offset:0
	ds_read_b64 v[126:127], v192 offset:16
	s_barrier
	ds_read_b128 v[128:131], v192 offset:128
	ds_read_b64 v[132:133], v192 offset:144
	s_waitcnt lgkmcnt(2)
	v_mfma_f32_16x16x128_f8f6f4 v[134:137], v[122:127], v[2:7], 0 cbsz:2 blgp:2
	v_mfma_f32_16x16x128_f8f6f4 v[138:141], v[122:127], v[14:19], 0 cbsz:2 blgp:2
	v_mfma_f32_16x16x128_f8f6f4 v[142:145], v[122:127], v[26:31], v[188:191] cbsz:2 blgp:2
	v_mfma_f32_16x16x128_f8f6f4 v[204:207], v[122:127], v[38:43], 0 cbsz:2 blgp:2
	v_mfma_f32_16x16x128_f8f6f4 v[208:211], v[122:127], v[50:55], 0 cbsz:2 blgp:2
	v_mfma_f32_16x16x128_f8f6f4 v[212:215], v[122:127], v[62:67], v[188:191] cbsz:2 blgp:2
	s_waitcnt lgkmcnt(0)
	v_mfma_f32_16x16x128_f8f6f4 v[134:137], v[128:133], v[8:13], v[134:137] cbsz:2 blgp:2
	v_mfma_f32_16x16x128_f8f6f4 v[204:207], v[128:133], v[44:49], v[204:207] cbsz:2 blgp:2
	v_mfma_f32_16x16x128_f8f6f4 v[138:141], v[128:133], v[20:25], v[138:141] cbsz:2 blgp:2
	v_mfma_f32_16x16x128_f8f6f4 v[208:211], v[128:133], v[56:61], v[208:211] cbsz:2 blgp:2
	v_mfma_f32_16x16x128_f8f6f4 v[142:145], v[128:133], v[32:37], v[142:145] cbsz:2 blgp:2
	v_mfma_f32_16x16x128_f8f6f4 v[212:215], v[128:133], v[68:73], v[212:215] cbsz:2 blgp:2
	v_cndmask_b32_e64 v158, v134, v204, s[4:5]
	v_cndmask_b32_e64 v159, v138, v208, s[4:5]
	v_fma_mix_f32 v158, v158, v1, v84 op_sel_hi:[0,0,1]
	v_fma_mix_f32 v159, v159, v99, v76 op_sel_hi:[0,0,1]
	v_exp_f32_e32 v158, v158
	v_exp_f32_e32 v159, v159
	v_fma_f32 v158, v158, v186, v186
	v_add_f32_e32 v159, 1.0, v159
	v_rcp_f32_e32 v158, v158
	v_rcp_f32_e32 v159, v159
	v_cndmask_b32_e64 v160, v142, v212, s[4:5]
	v_fma_mix_f32 v161, v158, v160, v80 op_sel_hi:[0,0,1]
	v_exp_f32_e32 v161, v161
	s_add_u32 s48, s48, s40
	v_add_f32_e32 v161, 1.0, v161
	v_rcp_f32_e32 v161, v161
	s_addc_u32 s49, s49, s41
	v_fma_f32 v162, v161, -2.0, 1.0
	v_sub_f32_e32 v163, v176, v162
	v_fma_f32 v176, v159, v163, v162
	v_fma_f32 v164, |v176|, s16, v117
	v_fma_f32 v165, |v176|, s17, v118
	v_fma_f32 v166, |v176|, s18, v119
	v_lshrrev_b32_e32 v167, 26, v176
	v_min3_u32 v164, v164, v165, v166
	v_bfi_b32 v168, 31, v164, v167
	s_nop 1
	v_mul_u32_u24_dpp v170, v168, v180 quad_perm:[1,2,3,3] row_mask:0xf bank_mask:0xf bound_ctrl:1
	v_mad_u32_u24 v171, v168, v181, v170
	ds_write_b8_d16_hi v184, v171 offset:544
	global_store_short_d16_hi v185, v176, s[48:49]
	s_waitcnt lgkmcnt(0)
	s_barrier
	ds_read_b128 v[122:125], v192 offset:544
	ds_read_b64 v[126:127], v192 offset:560
	s_barrier
	ds_read_b128 v[128:131], v192 offset:672
	ds_read_b64 v[132:133], v192 offset:688
	s_waitcnt lgkmcnt(2)
	v_mfma_f32_16x16x128_f8f6f4 v[134:137], v[122:127], v[2:7], 0 cbsz:2 blgp:2
	v_mfma_f32_16x16x128_f8f6f4 v[138:141], v[122:127], v[14:19], 0 cbsz:2 blgp:2
	v_mfma_f32_16x16x128_f8f6f4 v[142:145], v[122:127], v[26:31], v[188:191] cbsz:2 blgp:2
	v_mfma_f32_16x16x128_f8f6f4 v[204:207], v[122:127], v[38:43], 0 cbsz:2 blgp:2
	v_mfma_f32_16x16x128_f8f6f4 v[208:211], v[122:127], v[50:55], 0 cbsz:2 blgp:2
	v_mfma_f32_16x16x128_f8f6f4 v[212:215], v[122:127], v[62:67], v[188:191] cbsz:2 blgp:2
	s_waitcnt lgkmcnt(0)
	v_mfma_f32_16x16x128_f8f6f4 v[134:137], v[128:133], v[8:13], v[134:137] cbsz:2 blgp:2
	v_mfma_f32_16x16x128_f8f6f4 v[204:207], v[128:133], v[44:49], v[204:207] cbsz:2 blgp:2
	v_mfma_f32_16x16x128_f8f6f4 v[138:141], v[128:133], v[20:25], v[138:141] cbsz:2 blgp:2
	v_mfma_f32_16x16x128_f8f6f4 v[208:211], v[128:133], v[56:61], v[208:211] cbsz:2 blgp:2
	v_mfma_f32_16x16x128_f8f6f4 v[142:145], v[128:133], v[32:37], v[142:145] cbsz:2 blgp:2
	v_mfma_f32_16x16x128_f8f6f4 v[212:215], v[128:133], v[68:73], v[212:215] cbsz:2 blgp:2
	v_cndmask_b32_e64 v158, v134, v204, s[4:5]
	v_cndmask_b32_e64 v159, v138, v208, s[4:5]
	v_fma_mix_f32 v158, v158, v1, v84 op_sel:[0,0,1] op_sel_hi:[0,0,1]
	v_fma_mix_f32 v159, v159, v99, v76 op_sel:[0,0,1] op_sel_hi:[0,0,1]
	v_exp_f32_e32 v158, v158
	v_exp_f32_e32 v159, v159
	v_fma_f32 v158, v158, v186, v186
	v_add_f32_e32 v159, 1.0, v159
	v_rcp_f32_e32 v158, v158
	v_rcp_f32_e32 v159, v159
	v_cndmask_b32_e64 v160, v142, v212, s[4:5]
	v_fma_mix_f32 v161, v158, v160, v80 op_sel:[0,0,1] op_sel_hi:[0,0,1]
	v_exp_f32_e32 v161, v161
	s_add_u32 s48, s48, s40
	v_add_f32_e32 v161, 1.0, v161
	v_rcp_f32_e32 v161, v161
	s_addc_u32 s49, s49, s41
	v_fma_f32 v162, v161, -2.0, 1.0
	v_sub_f32_e32 v163, v176, v162
	v_fma_f32 v176, v159, v163, v162
	v_fma_f32 v164, |v176|, s16, v117
	v_fma_f32 v165, |v176|, s17, v118
	v_fma_f32 v166, |v176|, s18, v119
	v_lshrrev_b32_e32 v167, 26, v176
	v_min3_u32 v164, v164, v165, v166
	v_bfi_b32 v168, 31, v164, v167
	s_nop 1
	v_mul_u32_u24_dpp v170, v168, v180 quad_perm:[1,2,3,3] row_mask:0xf bank_mask:0xf bound_ctrl:1
	v_mad_u32_u24 v171, v168, v181, v170
	ds_write_b8_d16_hi v184, v171
	global_store_short_d16_hi v185, v176, s[48:49]
	s_waitcnt lgkmcnt(0)
	s_barrier
	ds_read_b128 v[122:125], v192 offset:0
	ds_read_b64 v[126:127], v192 offset:16
	s_barrier
	ds_read_b128 v[128:131], v192 offset:128
	ds_read_b64 v[132:133], v192 offset:144
	s_waitcnt lgkmcnt(2)
	v_mfma_f32_16x16x128_f8f6f4 v[134:137], v[122:127], v[2:7], 0 cbsz:2 blgp:2
	v_mfma_f32_16x16x128_f8f6f4 v[138:141], v[122:127], v[14:19], 0 cbsz:2 blgp:2
	v_mfma_f32_16x16x128_f8f6f4 v[142:145], v[122:127], v[26:31], v[188:191] cbsz:2 blgp:2
	v_mfma_f32_16x16x128_f8f6f4 v[204:207], v[122:127], v[38:43], 0 cbsz:2 blgp:2
	v_mfma_f32_16x16x128_f8f6f4 v[208:211], v[122:127], v[50:55], 0 cbsz:2 blgp:2
	v_mfma_f32_16x16x128_f8f6f4 v[212:215], v[122:127], v[62:67], v[188:191] cbsz:2 blgp:2
	s_waitcnt lgkmcnt(0)
	v_mfma_f32_16x16x128_f8f6f4 v[134:137], v[128:133], v[8:13], v[134:137] cbsz:2 blgp:2
	v_mfma_f32_16x16x128_f8f6f4 v[204:207], v[128:133], v[44:49], v[204:207] cbsz:2 blgp:2
	v_mfma_f32_16x16x128_f8f6f4 v[138:141], v[128:133], v[20:25], v[138:141] cbsz:2 blgp:2
	v_mfma_f32_16x16x128_f8f6f4 v[208:211], v[128:133], v[56:61], v[208:211] cbsz:2 blgp:2
	v_mfma_f32_16x16x128_f8f6f4 v[142:145], v[128:133], v[32:37], v[142:145] cbsz:2 blgp:2
	v_mfma_f32_16x16x128_f8f6f4 v[212:215], v[128:133], v[68:73], v[212:215] cbsz:2 blgp:2
	v_cndmask_b32_e64 v158, v134, v204, s[4:5]
	v_cndmask_b32_e64 v159, v138, v208, s[4:5]
	v_fma_mix_f32 v158, v158, v1, v85 op_sel_hi:[0,0,1]
	v_fma_mix_f32 v159, v159, v99, v77 op_sel_hi:[0,0,1]
	v_exp_f32_e32 v158, v158
	v_exp_f32_e32 v159, v159
	v_fma_f32 v158, v158, v186, v186
	v_add_f32_e32 v159, 1.0, v159
	v_rcp_f32_e32 v158, v158
	v_rcp_f32_e32 v159, v159
	v_cndmask_b32_e64 v160, v142, v212, s[4:5]
	v_fma_mix_f32 v161, v158, v160, v81 op_sel_hi:[0,0,1]
	v_exp_f32_e32 v161, v161
	s_add_u32 s48, s48, s40
	v_add_f32_e32 v161, 1.0, v161
	v_rcp_f32_e32 v161, v161
	s_addc_u32 s49, s49, s41
	v_fma_f32 v162, v161, -2.0, 1.0
	v_sub_f32_e32 v163, v176, v162
	v_fma_f32 v176, v159, v163, v162
	v_fma_f32 v164, |v176|, s16, v117
	v_fma_f32 v165, |v176|, s17, v118
	v_fma_f32 v166, |v176|, s18, v119
	v_lshrrev_b32_e32 v167, 26, v176
	v_min3_u32 v164, v164, v165, v166
	v_bfi_b32 v168, 31, v164, v167
	s_nop 1
	v_mul_u32_u24_dpp v170, v168, v180 quad_perm:[1,2,3,3] row_mask:0xf bank_mask:0xf bound_ctrl:1
	v_mad_u32_u24 v171, v168, v181, v170
	ds_write_b8_d16_hi v184, v171 offset:544
	global_store_short_d16_hi v185, v176, s[48:49]
	s_waitcnt lgkmcnt(0)
	s_barrier
	ds_read_b128 v[122:125], v192 offset:544
	ds_read_b64 v[126:127], v192 offset:560
	s_barrier
	ds_read_b128 v[128:131], v192 offset:672
	ds_read_b64 v[132:133], v192 offset:688
	s_waitcnt lgkmcnt(2)
	v_mfma_f32_16x16x128_f8f6f4 v[134:137], v[122:127], v[2:7], 0 cbsz:2 blgp:2
	v_mfma_f32_16x16x128_f8f6f4 v[138:141], v[122:127], v[14:19], 0 cbsz:2 blgp:2
	v_mfma_f32_16x16x128_f8f6f4 v[142:145], v[122:127], v[26:31], v[188:191] cbsz:2 blgp:2
	v_mfma_f32_16x16x128_f8f6f4 v[204:207], v[122:127], v[38:43], 0 cbsz:2 blgp:2
	v_mfma_f32_16x16x128_f8f6f4 v[208:211], v[122:127], v[50:55], 0 cbsz:2 blgp:2
	v_mfma_f32_16x16x128_f8f6f4 v[212:215], v[122:127], v[62:67], v[188:191] cbsz:2 blgp:2
	s_waitcnt lgkmcnt(0)
	v_mfma_f32_16x16x128_f8f6f4 v[134:137], v[128:133], v[8:13], v[134:137] cbsz:2 blgp:2
	v_mfma_f32_16x16x128_f8f6f4 v[204:207], v[128:133], v[44:49], v[204:207] cbsz:2 blgp:2
	v_mfma_f32_16x16x128_f8f6f4 v[138:141], v[128:133], v[20:25], v[138:141] cbsz:2 blgp:2
	v_mfma_f32_16x16x128_f8f6f4 v[208:211], v[128:133], v[56:61], v[208:211] cbsz:2 blgp:2
	v_mfma_f32_16x16x128_f8f6f4 v[142:145], v[128:133], v[32:37], v[142:145] cbsz:2 blgp:2
	v_mfma_f32_16x16x128_f8f6f4 v[212:215], v[128:133], v[68:73], v[212:215] cbsz:2 blgp:2
	v_cndmask_b32_e64 v158, v134, v204, s[4:5]
	v_cndmask_b32_e64 v159, v138, v208, s[4:5]
	v_fma_mix_f32 v158, v158, v1, v85 op_sel:[0,0,1] op_sel_hi:[0,0,1]
	v_fma_mix_f32 v159, v159, v99, v77 op_sel:[0,0,1] op_sel_hi:[0,0,1]
	v_exp_f32_e32 v158, v158
	v_exp_f32_e32 v159, v159
	v_fma_f32 v158, v158, v186, v186
	v_add_f32_e32 v159, 1.0, v159
	v_rcp_f32_e32 v158, v158
	v_rcp_f32_e32 v159, v159
	v_cndmask_b32_e64 v160, v142, v212, s[4:5]
	v_fma_mix_f32 v161, v158, v160, v81 op_sel:[0,0,1] op_sel_hi:[0,0,1]
	v_exp_f32_e32 v161, v161
	s_add_u32 s48, s48, s40
	v_add_f32_e32 v161, 1.0, v161
	v_rcp_f32_e32 v161, v161
	s_addc_u32 s49, s49, s41
	v_fma_f32 v162, v161, -2.0, 1.0
	v_sub_f32_e32 v163, v176, v162
	v_fma_f32 v176, v159, v163, v162
	v_fma_f32 v164, |v176|, s16, v117
	v_fma_f32 v165, |v176|, s17, v118
	v_fma_f32 v166, |v176|, s18, v119
	v_lshrrev_b32_e32 v167, 26, v176
	v_min3_u32 v164, v164, v165, v166
	v_bfi_b32 v168, 31, v164, v167
	s_nop 1
	v_mul_u32_u24_dpp v170, v168, v180 quad_perm:[1,2,3,3] row_mask:0xf bank_mask:0xf bound_ctrl:1
	v_mad_u32_u24 v171, v168, v181, v170
	ds_write_b8_d16_hi v184, v171
	global_store_short_d16_hi v185, v176, s[48:49]
	s_waitcnt lgkmcnt(0)
	s_barrier
	ds_read_b128 v[122:125], v192 offset:0
	ds_read_b64 v[126:127], v192 offset:16
	s_barrier
	ds_read_b128 v[128:131], v192 offset:128
	ds_read_b64 v[132:133], v192 offset:144
	s_waitcnt vmcnt(8)
	global_load_dwordx4 v[82:85], v[196:197], off
	global_load_dwordx4 v[74:77], v[196:197], off offset:512
	global_load_dwordx4 v[78:81], v[196:197], off offset:1024
	v_lshl_add_u64 v[196:197], v[196:197], 0, s[42:43]
	s_waitcnt lgkmcnt(2)
	v_mfma_f32_16x16x128_f8f6f4 v[134:137], v[122:127], v[2:7], 0 cbsz:2 blgp:2
	v_mfma_f32_16x16x128_f8f6f4 v[138:141], v[122:127], v[14:19], 0 cbsz:2 blgp:2
	v_mfma_f32_16x16x128_f8f6f4 v[142:145], v[122:127], v[26:31], v[188:191] cbsz:2 blgp:2
	v_mfma_f32_16x16x128_f8f6f4 v[204:207], v[122:127], v[38:43], 0 cbsz:2 blgp:2
	v_mfma_f32_16x16x128_f8f6f4 v[208:211], v[122:127], v[50:55], 0 cbsz:2 blgp:2
	v_mfma_f32_16x16x128_f8f6f4 v[212:215], v[122:127], v[62:67], v[188:191] cbsz:2 blgp:2
	s_waitcnt lgkmcnt(0)
	v_mfma_f32_16x16x128_f8f6f4 v[134:137], v[128:133], v[8:13], v[134:137] cbsz:2 blgp:2
	v_mfma_f32_16x16x128_f8f6f4 v[204:207], v[128:133], v[44:49], v[204:207] cbsz:2 blgp:2
	v_mfma_f32_16x16x128_f8f6f4 v[138:141], v[128:133], v[20:25], v[138:141] cbsz:2 blgp:2
	v_mfma_f32_16x16x128_f8f6f4 v[208:211], v[128:133], v[56:61], v[208:211] cbsz:2 blgp:2
	v_mfma_f32_16x16x128_f8f6f4 v[142:145], v[128:133], v[32:37], v[142:145] cbsz:2 blgp:2
	v_mfma_f32_16x16x128_f8f6f4 v[212:215], v[128:133], v[68:73], v[212:215] cbsz:2 blgp:2
	v_cndmask_b32_e64 v158, v134, v204, s[4:5]
	v_cndmask_b32_e64 v159, v138, v208, s[4:5]
	v_fma_mix_f32 v158, v158, v1, v146 op_sel_hi:[0,0,1]
	v_fma_mix_f32 v159, v159, v99, v150 op_sel_hi:[0,0,1]
	v_exp_f32_e32 v158, v158
	v_exp_f32_e32 v159, v159
	v_fma_f32 v158, v158, v186, v186
	v_add_f32_e32 v159, 1.0, v159
	v_rcp_f32_e32 v158, v158
	v_rcp_f32_e32 v159, v159
	v_cndmask_b32_e64 v160, v142, v212, s[4:5]
	v_fma_mix_f32 v161, v158, v160, v154 op_sel_hi:[0,0,1]
	v_exp_f32_e32 v161, v161
	s_add_u32 s48, s48, s40
	v_add_f32_e32 v161, 1.0, v161
	v_rcp_f32_e32 v161, v161
	s_addc_u32 s49, s49, s41
	v_fma_f32 v162, v161, -2.0, 1.0
	v_sub_f32_e32 v163, v176, v162
	v_fma_f32 v176, v159, v163, v162
	v_fma_f32 v164, |v176|, s16, v117
	v_fma_f32 v165, |v176|, s17, v118
	v_fma_f32 v166, |v176|, s18, v119
	v_lshrrev_b32_e32 v167, 26, v176
	v_min3_u32 v164, v164, v165, v166
	v_bfi_b32 v168, 31, v164, v167
	s_nop 1
	v_mul_u32_u24_dpp v170, v168, v180 quad_perm:[1,2,3,3] row_mask:0xf bank_mask:0xf bound_ctrl:1
	v_mad_u32_u24 v171, v168, v181, v170
	ds_write_b8_d16_hi v184, v171 offset:544
	global_store_short_d16_hi v185, v176, s[48:49]
	s_waitcnt lgkmcnt(0)
	s_barrier
	ds_read_b128 v[122:125], v192 offset:544
	ds_read_b64 v[126:127], v192 offset:560
	s_barrier
	ds_read_b128 v[128:131], v192 offset:672
	ds_read_b64 v[132:133], v192 offset:688
	s_waitcnt lgkmcnt(2)
	v_mfma_f32_16x16x128_f8f6f4 v[134:137], v[122:127], v[2:7], 0 cbsz:2 blgp:2
	v_mfma_f32_16x16x128_f8f6f4 v[138:141], v[122:127], v[14:19], 0 cbsz:2 blgp:2
	v_mfma_f32_16x16x128_f8f6f4 v[142:145], v[122:127], v[26:31], v[188:191] cbsz:2 blgp:2
	v_mfma_f32_16x16x128_f8f6f4 v[204:207], v[122:127], v[38:43], 0 cbsz:2 blgp:2
	v_mfma_f32_16x16x128_f8f6f4 v[208:211], v[122:127], v[50:55], 0 cbsz:2 blgp:2
	v_mfma_f32_16x16x128_f8f6f4 v[212:215], v[122:127], v[62:67], v[188:191] cbsz:2 blgp:2
	s_waitcnt lgkmcnt(0)
	v_mfma_f32_16x16x128_f8f6f4 v[134:137], v[128:133], v[8:13], v[134:137] cbsz:2 blgp:2
	v_mfma_f32_16x16x128_f8f6f4 v[204:207], v[128:133], v[44:49], v[204:207] cbsz:2 blgp:2
	v_mfma_f32_16x16x128_f8f6f4 v[138:141], v[128:133], v[20:25], v[138:141] cbsz:2 blgp:2
	v_mfma_f32_16x16x128_f8f6f4 v[208:211], v[128:133], v[56:61], v[208:211] cbsz:2 blgp:2
	v_mfma_f32_16x16x128_f8f6f4 v[142:145], v[128:133], v[32:37], v[142:145] cbsz:2 blgp:2
	v_mfma_f32_16x16x128_f8f6f4 v[212:215], v[128:133], v[68:73], v[212:215] cbsz:2 blgp:2
	v_cndmask_b32_e64 v158, v134, v204, s[4:5]
	v_cndmask_b32_e64 v159, v138, v208, s[4:5]
	v_fma_mix_f32 v158, v158, v1, v146 op_sel:[0,0,1] op_sel_hi:[0,0,1]
	v_fma_mix_f32 v159, v159, v99, v150 op_sel:[0,0,1] op_sel_hi:[0,0,1]
	v_exp_f32_e32 v158, v158
	v_exp_f32_e32 v159, v159
	v_fma_f32 v158, v158, v186, v186
	v_add_f32_e32 v159, 1.0, v159
	v_rcp_f32_e32 v158, v158
	v_rcp_f32_e32 v159, v159
	v_cndmask_b32_e64 v160, v142, v212, s[4:5]
	v_fma_mix_f32 v161, v158, v160, v154 op_sel:[0,0,1] op_sel_hi:[0,0,1]
	v_exp_f32_e32 v161, v161
	s_add_u32 s48, s48, s40
	v_add_f32_e32 v161, 1.0, v161
	v_rcp_f32_e32 v161, v161
	s_addc_u32 s49, s49, s41
	v_fma_f32 v162, v161, -2.0, 1.0
	v_sub_f32_e32 v163, v176, v162
	v_fma_f32 v176, v159, v163, v162
	v_fma_f32 v164, |v176|, s16, v117
	v_fma_f32 v165, |v176|, s17, v118
	v_fma_f32 v166, |v176|, s18, v119
	v_lshrrev_b32_e32 v167, 26, v176
	v_min3_u32 v164, v164, v165, v166
	v_bfi_b32 v168, 31, v164, v167
	s_nop 1
	v_mul_u32_u24_dpp v170, v168, v180 quad_perm:[1,2,3,3] row_mask:0xf bank_mask:0xf bound_ctrl:1
	v_mad_u32_u24 v171, v168, v181, v170
	ds_write_b8_d16_hi v184, v171
	global_store_short_d16_hi v185, v176, s[48:49]
	s_waitcnt lgkmcnt(0)
	s_barrier
	ds_read_b128 v[122:125], v192 offset:0
	ds_read_b64 v[126:127], v192 offset:16
	s_barrier
	ds_read_b128 v[128:131], v192 offset:128
	ds_read_b64 v[132:133], v192 offset:144
	s_waitcnt lgkmcnt(2)
	v_mfma_f32_16x16x128_f8f6f4 v[134:137], v[122:127], v[2:7], 0 cbsz:2 blgp:2
	v_mfma_f32_16x16x128_f8f6f4 v[138:141], v[122:127], v[14:19], 0 cbsz:2 blgp:2
	v_mfma_f32_16x16x128_f8f6f4 v[142:145], v[122:127], v[26:31], v[188:191] cbsz:2 blgp:2
	v_mfma_f32_16x16x128_f8f6f4 v[204:207], v[122:127], v[38:43], 0 cbsz:2 blgp:2
	v_mfma_f32_16x16x128_f8f6f4 v[208:211], v[122:127], v[50:55], 0 cbsz:2 blgp:2
	v_mfma_f32_16x16x128_f8f6f4 v[212:215], v[122:127], v[62:67], v[188:191] cbsz:2 blgp:2
	s_waitcnt lgkmcnt(0)
	v_mfma_f32_16x16x128_f8f6f4 v[134:137], v[128:133], v[8:13], v[134:137] cbsz:2 blgp:2
	v_mfma_f32_16x16x128_f8f6f4 v[204:207], v[128:133], v[44:49], v[204:207] cbsz:2 blgp:2
	v_mfma_f32_16x16x128_f8f6f4 v[138:141], v[128:133], v[20:25], v[138:141] cbsz:2 blgp:2
	v_mfma_f32_16x16x128_f8f6f4 v[208:211], v[128:133], v[56:61], v[208:211] cbsz:2 blgp:2
	v_mfma_f32_16x16x128_f8f6f4 v[142:145], v[128:133], v[32:37], v[142:145] cbsz:2 blgp:2
	v_mfma_f32_16x16x128_f8f6f4 v[212:215], v[128:133], v[68:73], v[212:215] cbsz:2 blgp:2
	v_cndmask_b32_e64 v158, v134, v204, s[4:5]
	v_cndmask_b32_e64 v159, v138, v208, s[4:5]
	v_fma_mix_f32 v158, v158, v1, v147 op_sel_hi:[0,0,1]
	v_fma_mix_f32 v159, v159, v99, v151 op_sel_hi:[0,0,1]
	v_exp_f32_e32 v158, v158
	v_exp_f32_e32 v159, v159
	v_fma_f32 v158, v158, v186, v186
	v_add_f32_e32 v159, 1.0, v159
	v_rcp_f32_e32 v158, v158
	v_rcp_f32_e32 v159, v159
	v_cndmask_b32_e64 v160, v142, v212, s[4:5]
	v_fma_mix_f32 v161, v158, v160, v155 op_sel_hi:[0,0,1]
	v_exp_f32_e32 v161, v161
	s_add_u32 s48, s48, s40
	v_add_f32_e32 v161, 1.0, v161
	v_rcp_f32_e32 v161, v161
	s_addc_u32 s49, s49, s41
	v_fma_f32 v162, v161, -2.0, 1.0
	v_sub_f32_e32 v163, v176, v162
	v_fma_f32 v176, v159, v163, v162
	v_fma_f32 v164, |v176|, s16, v117
	v_fma_f32 v165, |v176|, s17, v118
	v_fma_f32 v166, |v176|, s18, v119
	v_lshrrev_b32_e32 v167, 26, v176
	v_min3_u32 v164, v164, v165, v166
	v_bfi_b32 v168, 31, v164, v167
	s_nop 1
	v_mul_u32_u24_dpp v170, v168, v180 quad_perm:[1,2,3,3] row_mask:0xf bank_mask:0xf bound_ctrl:1
	v_mad_u32_u24 v171, v168, v181, v170
	ds_write_b8_d16_hi v184, v171 offset:544
	global_store_short_d16_hi v185, v176, s[48:49]
	s_waitcnt lgkmcnt(0)
	s_barrier
	ds_read_b128 v[122:125], v192 offset:544
	ds_read_b64 v[126:127], v192 offset:560
	s_barrier
	ds_read_b128 v[128:131], v192 offset:672
	ds_read_b64 v[132:133], v192 offset:688
	s_waitcnt lgkmcnt(2)
	v_mfma_f32_16x16x128_f8f6f4 v[134:137], v[122:127], v[2:7], 0 cbsz:2 blgp:2
	v_mfma_f32_16x16x128_f8f6f4 v[138:141], v[122:127], v[14:19], 0 cbsz:2 blgp:2
	v_mfma_f32_16x16x128_f8f6f4 v[142:145], v[122:127], v[26:31], v[188:191] cbsz:2 blgp:2
	v_mfma_f32_16x16x128_f8f6f4 v[204:207], v[122:127], v[38:43], 0 cbsz:2 blgp:2
	v_mfma_f32_16x16x128_f8f6f4 v[208:211], v[122:127], v[50:55], 0 cbsz:2 blgp:2
	v_mfma_f32_16x16x128_f8f6f4 v[212:215], v[122:127], v[62:67], v[188:191] cbsz:2 blgp:2
	s_waitcnt lgkmcnt(0)
	v_mfma_f32_16x16x128_f8f6f4 v[134:137], v[128:133], v[8:13], v[134:137] cbsz:2 blgp:2
	v_mfma_f32_16x16x128_f8f6f4 v[204:207], v[128:133], v[44:49], v[204:207] cbsz:2 blgp:2
	v_mfma_f32_16x16x128_f8f6f4 v[138:141], v[128:133], v[20:25], v[138:141] cbsz:2 blgp:2
	v_mfma_f32_16x16x128_f8f6f4 v[208:211], v[128:133], v[56:61], v[208:211] cbsz:2 blgp:2
	v_mfma_f32_16x16x128_f8f6f4 v[142:145], v[128:133], v[32:37], v[142:145] cbsz:2 blgp:2
	v_mfma_f32_16x16x128_f8f6f4 v[212:215], v[128:133], v[68:73], v[212:215] cbsz:2 blgp:2
	v_cndmask_b32_e64 v158, v134, v204, s[4:5]
	v_cndmask_b32_e64 v159, v138, v208, s[4:5]
	v_fma_mix_f32 v158, v158, v1, v147 op_sel:[0,0,1] op_sel_hi:[0,0,1]
	v_fma_mix_f32 v159, v159, v99, v151 op_sel:[0,0,1] op_sel_hi:[0,0,1]
	v_exp_f32_e32 v158, v158
	v_exp_f32_e32 v159, v159
	v_fma_f32 v158, v158, v186, v186
	v_add_f32_e32 v159, 1.0, v159
	v_rcp_f32_e32 v158, v158
	v_rcp_f32_e32 v159, v159
	v_cndmask_b32_e64 v160, v142, v212, s[4:5]
	v_fma_mix_f32 v161, v158, v160, v155 op_sel:[0,0,1] op_sel_hi:[0,0,1]
	v_exp_f32_e32 v161, v161
	s_add_u32 s48, s48, s40
	v_add_f32_e32 v161, 1.0, v161
	v_rcp_f32_e32 v161, v161
	s_addc_u32 s49, s49, s41
	v_fma_f32 v162, v161, -2.0, 1.0
	v_sub_f32_e32 v163, v176, v162
	v_fma_f32 v176, v159, v163, v162
	v_fma_f32 v164, |v176|, s16, v117
	v_fma_f32 v165, |v176|, s17, v118
	v_fma_f32 v166, |v176|, s18, v119
	v_lshrrev_b32_e32 v167, 26, v176
	v_min3_u32 v164, v164, v165, v166
	v_bfi_b32 v168, 31, v164, v167
	s_nop 1
	v_mul_u32_u24_dpp v170, v168, v180 quad_perm:[1,2,3,3] row_mask:0xf bank_mask:0xf bound_ctrl:1
	v_mad_u32_u24 v171, v168, v181, v170
	ds_write_b8_d16_hi v184, v171
	global_store_short_d16_hi v185, v176, s[48:49]
	s_waitcnt lgkmcnt(0)
	s_barrier
	ds_read_b128 v[122:125], v192 offset:0
	ds_read_b64 v[126:127], v192 offset:16
	s_barrier
	ds_read_b128 v[128:131], v192 offset:128
	ds_read_b64 v[132:133], v192 offset:144
	s_waitcnt lgkmcnt(2)
	v_mfma_f32_16x16x128_f8f6f4 v[134:137], v[122:127], v[2:7], 0 cbsz:2 blgp:2
	v_mfma_f32_16x16x128_f8f6f4 v[138:141], v[122:127], v[14:19], 0 cbsz:2 blgp:2
	v_mfma_f32_16x16x128_f8f6f4 v[142:145], v[122:127], v[26:31], v[188:191] cbsz:2 blgp:2
	v_mfma_f32_16x16x128_f8f6f4 v[204:207], v[122:127], v[38:43], 0 cbsz:2 blgp:2
	v_mfma_f32_16x16x128_f8f6f4 v[208:211], v[122:127], v[50:55], 0 cbsz:2 blgp:2
	v_mfma_f32_16x16x128_f8f6f4 v[212:215], v[122:127], v[62:67], v[188:191] cbsz:2 blgp:2
	s_waitcnt lgkmcnt(0)
	v_mfma_f32_16x16x128_f8f6f4 v[134:137], v[128:133], v[8:13], v[134:137] cbsz:2 blgp:2
	v_mfma_f32_16x16x128_f8f6f4 v[204:207], v[128:133], v[44:49], v[204:207] cbsz:2 blgp:2
	v_mfma_f32_16x16x128_f8f6f4 v[138:141], v[128:133], v[20:25], v[138:141] cbsz:2 blgp:2
	v_mfma_f32_16x16x128_f8f6f4 v[208:211], v[128:133], v[56:61], v[208:211] cbsz:2 blgp:2
	v_mfma_f32_16x16x128_f8f6f4 v[142:145], v[128:133], v[32:37], v[142:145] cbsz:2 blgp:2
	v_mfma_f32_16x16x128_f8f6f4 v[212:215], v[128:133], v[68:73], v[212:215] cbsz:2 blgp:2
	v_cndmask_b32_e64 v158, v134, v204, s[4:5]
	v_cndmask_b32_e64 v159, v138, v208, s[4:5]
	v_fma_mix_f32 v158, v158, v1, v148 op_sel_hi:[0,0,1]
	v_fma_mix_f32 v159, v159, v99, v152 op_sel_hi:[0,0,1]
	v_exp_f32_e32 v158, v158
	v_exp_f32_e32 v159, v159
	v_fma_f32 v158, v158, v186, v186
	v_add_f32_e32 v159, 1.0, v159
	v_rcp_f32_e32 v158, v158
	v_rcp_f32_e32 v159, v159
	v_cndmask_b32_e64 v160, v142, v212, s[4:5]
	v_fma_mix_f32 v161, v158, v160, v156 op_sel_hi:[0,0,1]
	v_exp_f32_e32 v161, v161
	s_add_u32 s48, s48, s40
	v_add_f32_e32 v161, 1.0, v161
	v_rcp_f32_e32 v161, v161
	s_addc_u32 s49, s49, s41
	v_fma_f32 v162, v161, -2.0, 1.0
	v_sub_f32_e32 v163, v176, v162
	v_fma_f32 v176, v159, v163, v162
	v_fma_f32 v164, |v176|, s16, v117
	v_fma_f32 v165, |v176|, s17, v118
	v_fma_f32 v166, |v176|, s18, v119
	v_lshrrev_b32_e32 v167, 26, v176
	v_min3_u32 v164, v164, v165, v166
	v_bfi_b32 v168, 31, v164, v167
	s_nop 1
	v_mul_u32_u24_dpp v170, v168, v180 quad_perm:[1,2,3,3] row_mask:0xf bank_mask:0xf bound_ctrl:1
	v_mad_u32_u24 v171, v168, v181, v170
	ds_write_b8_d16_hi v184, v171 offset:544
	global_store_short_d16_hi v185, v176, s[48:49]
	s_waitcnt lgkmcnt(0)
	s_barrier
	ds_read_b128 v[122:125], v192 offset:544
	ds_read_b64 v[126:127], v192 offset:560
	s_barrier
	ds_read_b128 v[128:131], v192 offset:672
	ds_read_b64 v[132:133], v192 offset:688
	s_waitcnt lgkmcnt(2)
	v_mfma_f32_16x16x128_f8f6f4 v[134:137], v[122:127], v[2:7], 0 cbsz:2 blgp:2
	v_mfma_f32_16x16x128_f8f6f4 v[138:141], v[122:127], v[14:19], 0 cbsz:2 blgp:2
	v_mfma_f32_16x16x128_f8f6f4 v[142:145], v[122:127], v[26:31], v[188:191] cbsz:2 blgp:2
	v_mfma_f32_16x16x128_f8f6f4 v[204:207], v[122:127], v[38:43], 0 cbsz:2 blgp:2
	v_mfma_f32_16x16x128_f8f6f4 v[208:211], v[122:127], v[50:55], 0 cbsz:2 blgp:2
	v_mfma_f32_16x16x128_f8f6f4 v[212:215], v[122:127], v[62:67], v[188:191] cbsz:2 blgp:2
	s_waitcnt lgkmcnt(0)
	v_mfma_f32_16x16x128_f8f6f4 v[134:137], v[128:133], v[8:13], v[134:137] cbsz:2 blgp:2
	v_mfma_f32_16x16x128_f8f6f4 v[204:207], v[128:133], v[44:49], v[204:207] cbsz:2 blgp:2
	v_mfma_f32_16x16x128_f8f6f4 v[138:141], v[128:133], v[20:25], v[138:141] cbsz:2 blgp:2
	v_mfma_f32_16x16x128_f8f6f4 v[208:211], v[128:133], v[56:61], v[208:211] cbsz:2 blgp:2
	v_mfma_f32_16x16x128_f8f6f4 v[142:145], v[128:133], v[32:37], v[142:145] cbsz:2 blgp:2
	v_mfma_f32_16x16x128_f8f6f4 v[212:215], v[128:133], v[68:73], v[212:215] cbsz:2 blgp:2
	v_cndmask_b32_e64 v158, v134, v204, s[4:5]
	v_cndmask_b32_e64 v159, v138, v208, s[4:5]
	v_fma_mix_f32 v158, v158, v1, v148 op_sel:[0,0,1] op_sel_hi:[0,0,1]
	v_fma_mix_f32 v159, v159, v99, v152 op_sel:[0,0,1] op_sel_hi:[0,0,1]
	v_exp_f32_e32 v158, v158
	v_exp_f32_e32 v159, v159
	v_fma_f32 v158, v158, v186, v186
	v_add_f32_e32 v159, 1.0, v159
	v_rcp_f32_e32 v158, v158
	v_rcp_f32_e32 v159, v159
	v_cndmask_b32_e64 v160, v142, v212, s[4:5]
	v_fma_mix_f32 v161, v158, v160, v156 op_sel:[0,0,1] op_sel_hi:[0,0,1]
	v_exp_f32_e32 v161, v161
	s_add_u32 s48, s48, s40
	v_add_f32_e32 v161, 1.0, v161
	v_rcp_f32_e32 v161, v161
	s_addc_u32 s49, s49, s41
	v_fma_f32 v162, v161, -2.0, 1.0
	v_sub_f32_e32 v163, v176, v162
	v_fma_f32 v176, v159, v163, v162
	v_fma_f32 v164, |v176|, s16, v117
	v_fma_f32 v165, |v176|, s17, v118
	v_fma_f32 v166, |v176|, s18, v119
	v_lshrrev_b32_e32 v167, 26, v176
	v_min3_u32 v164, v164, v165, v166
	v_bfi_b32 v168, 31, v164, v167
	s_nop 1
	v_mul_u32_u24_dpp v170, v168, v180 quad_perm:[1,2,3,3] row_mask:0xf bank_mask:0xf bound_ctrl:1
	v_mad_u32_u24 v171, v168, v181, v170
	ds_write_b8_d16_hi v184, v171
	global_store_short_d16_hi v185, v176, s[48:49]
	s_waitcnt lgkmcnt(0)
	s_barrier
	ds_read_b128 v[122:125], v192 offset:0
	ds_read_b64 v[126:127], v192 offset:16
	s_barrier
	ds_read_b128 v[128:131], v192 offset:128
	ds_read_b64 v[132:133], v192 offset:144
	s_waitcnt lgkmcnt(2)
	v_mfma_f32_16x16x128_f8f6f4 v[134:137], v[122:127], v[2:7], 0 cbsz:2 blgp:2
	v_mfma_f32_16x16x128_f8f6f4 v[138:141], v[122:127], v[14:19], 0 cbsz:2 blgp:2
	v_mfma_f32_16x16x128_f8f6f4 v[142:145], v[122:127], v[26:31], v[188:191] cbsz:2 blgp:2
	v_mfma_f32_16x16x128_f8f6f4 v[204:207], v[122:127], v[38:43], 0 cbsz:2 blgp:2
	v_mfma_f32_16x16x128_f8f6f4 v[208:211], v[122:127], v[50:55], 0 cbsz:2 blgp:2
	v_mfma_f32_16x16x128_f8f6f4 v[212:215], v[122:127], v[62:67], v[188:191] cbsz:2 blgp:2
	s_waitcnt lgkmcnt(0)
	v_mfma_f32_16x16x128_f8f6f4 v[134:137], v[128:133], v[8:13], v[134:137] cbsz:2 blgp:2
	v_mfma_f32_16x16x128_f8f6f4 v[204:207], v[128:133], v[44:49], v[204:207] cbsz:2 blgp:2
	v_mfma_f32_16x16x128_f8f6f4 v[138:141], v[128:133], v[20:25], v[138:141] cbsz:2 blgp:2
	v_mfma_f32_16x16x128_f8f6f4 v[208:211], v[128:133], v[56:61], v[208:211] cbsz:2 blgp:2
	v_mfma_f32_16x16x128_f8f6f4 v[142:145], v[128:133], v[32:37], v[142:145] cbsz:2 blgp:2
	v_mfma_f32_16x16x128_f8f6f4 v[212:215], v[128:133], v[68:73], v[212:215] cbsz:2 blgp:2
	v_cndmask_b32_e64 v158, v134, v204, s[4:5]
	v_cndmask_b32_e64 v159, v138, v208, s[4:5]
	v_fma_mix_f32 v158, v158, v1, v149 op_sel_hi:[0,0,1]
	v_fma_mix_f32 v159, v159, v99, v153 op_sel_hi:[0,0,1]
	v_exp_f32_e32 v158, v158
	v_exp_f32_e32 v159, v159
	v_fma_f32 v158, v158, v186, v186
	v_add_f32_e32 v159, 1.0, v159
	v_rcp_f32_e32 v158, v158
	v_rcp_f32_e32 v159, v159
	v_cndmask_b32_e64 v160, v142, v212, s[4:5]
	v_fma_mix_f32 v161, v158, v160, v157 op_sel_hi:[0,0,1]
	v_exp_f32_e32 v161, v161
	s_add_u32 s48, s48, s40
	v_add_f32_e32 v161, 1.0, v161
	v_rcp_f32_e32 v161, v161
	s_addc_u32 s49, s49, s41
	v_fma_f32 v162, v161, -2.0, 1.0
	v_sub_f32_e32 v163, v176, v162
	v_fma_f32 v176, v159, v163, v162
	v_fma_f32 v164, |v176|, s16, v117
	v_fma_f32 v165, |v176|, s17, v118
	v_fma_f32 v166, |v176|, s18, v119
	v_lshrrev_b32_e32 v167, 26, v176
	v_min3_u32 v164, v164, v165, v166
	v_bfi_b32 v168, 31, v164, v167
	s_nop 1
	v_mul_u32_u24_dpp v170, v168, v180 quad_perm:[1,2,3,3] row_mask:0xf bank_mask:0xf bound_ctrl:1
	v_mad_u32_u24 v171, v168, v181, v170
	ds_write_b8_d16_hi v184, v171 offset:544
	global_store_short_d16_hi v185, v176, s[48:49]
	s_waitcnt lgkmcnt(0)
	s_barrier
	ds_read_b128 v[122:125], v192 offset:544
	ds_read_b64 v[126:127], v192 offset:560
	s_barrier
	ds_read_b128 v[128:131], v192 offset:672
	ds_read_b64 v[132:133], v192 offset:688
	s_add_i32 s44, s44, 16
	s_waitcnt lgkmcnt(2)
	v_mfma_f32_16x16x128_f8f6f4 v[134:137], v[122:127], v[2:7], 0 cbsz:2 blgp:2
	v_mfma_f32_16x16x128_f8f6f4 v[138:141], v[122:127], v[14:19], 0 cbsz:2 blgp:2
	v_mfma_f32_16x16x128_f8f6f4 v[142:145], v[122:127], v[26:31], v[188:191] cbsz:2 blgp:2
	v_mfma_f32_16x16x128_f8f6f4 v[204:207], v[122:127], v[38:43], 0 cbsz:2 blgp:2
	v_mfma_f32_16x16x128_f8f6f4 v[208:211], v[122:127], v[50:55], 0 cbsz:2 blgp:2
	v_mfma_f32_16x16x128_f8f6f4 v[212:215], v[122:127], v[62:67], v[188:191] cbsz:2 blgp:2
	s_waitcnt lgkmcnt(0)
	v_mfma_f32_16x16x128_f8f6f4 v[134:137], v[128:133], v[8:13], v[134:137] cbsz:2 blgp:2
	v_mfma_f32_16x16x128_f8f6f4 v[204:207], v[128:133], v[44:49], v[204:207] cbsz:2 blgp:2
	v_mfma_f32_16x16x128_f8f6f4 v[138:141], v[128:133], v[20:25], v[138:141] cbsz:2 blgp:2
	v_mfma_f32_16x16x128_f8f6f4 v[208:211], v[128:133], v[56:61], v[208:211] cbsz:2 blgp:2
	v_mfma_f32_16x16x128_f8f6f4 v[142:145], v[128:133], v[32:37], v[142:145] cbsz:2 blgp:2
	v_mfma_f32_16x16x128_f8f6f4 v[212:215], v[128:133], v[68:73], v[212:215] cbsz:2 blgp:2
	v_cndmask_b32_e64 v158, v134, v204, s[4:5]
	v_cndmask_b32_e64 v159, v138, v208, s[4:5]
	v_fma_mix_f32 v158, v158, v1, v149 op_sel:[0,0,1] op_sel_hi:[0,0,1]
	v_fma_mix_f32 v159, v159, v99, v153 op_sel:[0,0,1] op_sel_hi:[0,0,1]
	v_exp_f32_e32 v158, v158
	v_exp_f32_e32 v159, v159
	v_fma_f32 v158, v158, v186, v186
	v_add_f32_e32 v159, 1.0, v159
	v_rcp_f32_e32 v158, v158
	v_rcp_f32_e32 v159, v159
	v_cndmask_b32_e64 v160, v142, v212, s[4:5]
	v_fma_mix_f32 v161, v158, v160, v157 op_sel:[0,0,1] op_sel_hi:[0,0,1]
	v_exp_f32_e32 v161, v161
	s_add_u32 s48, s48, s40
	v_add_f32_e32 v161, 1.0, v161
	v_rcp_f32_e32 v161, v161
	s_addc_u32 s49, s49, s41
	v_fma_f32 v162, v161, -2.0, 1.0
	v_sub_f32_e32 v163, v176, v162
	v_fma_f32 v176, v159, v163, v162
	v_fma_f32 v164, |v176|, s16, v117
	v_fma_f32 v165, |v176|, s17, v118
	v_fma_f32 v166, |v176|, s18, v119
	v_lshrrev_b32_e32 v167, 26, v176
	v_min3_u32 v164, v164, v165, v166
	v_bfi_b32 v168, 31, v164, v167
	s_nop 1
	v_mul_u32_u24_dpp v170, v168, v180 quad_perm:[1,2,3,3] row_mask:0xf bank_mask:0xf bound_ctrl:1
	v_mad_u32_u24 v171, v168, v181, v170
	ds_write_b8_d16_hi v184, v171
	global_store_short_d16_hi v185, v176, s[48:49]
	s_waitcnt lgkmcnt(0)
	s_barrier
	ds_read_b128 v[122:125], v192 offset:0
	ds_read_b64 v[126:127], v192 offset:16
	s_cmp_lt_i32 s44, s45
	s_cbranch_scc1 .Lscan_loop_a_st
	s_barrier
	s_branch .Lscan_exit_st

.Lscan_enter_b_st:
	ds_read_b128 v[122:125], v192 offset:0
	ds_read_b64 v[126:127], v192 offset:16
	ds_read_b128 v[128:131], v192 offset:128
	ds_read_b64 v[132:133], v192 offset:144
	s_waitcnt vmcnt(8)
	global_load_dwordx4 v[146:149], v[196:197], off
	global_load_dwordx4 v[150:153], v[196:197], off offset:512
	global_load_dwordx4 v[154:157], v[196:197], off offset:1024
	v_lshl_add_u64 v[196:197], v[196:197], 0, s[42:43]
	s_waitcnt lgkmcnt(2)
	v_mfma_f32_16x16x128_f8f6f4 v[134:137], v[122:127], v[2:7], 0 cbsz:2 blgp:2
	v_mfma_f32_16x16x128_f8f6f4 v[138:141], v[122:127], v[14:19], 0 cbsz:2 blgp:2
	v_mfma_f32_16x16x128_f8f6f4 v[142:145], v[122:127], v[26:31], v[188:191] cbsz:2 blgp:2
	v_mfma_f32_16x16x128_f8f6f4 v[204:207], v[122:127], v[38:43], 0 cbsz:2 blgp:2
	v_mfma_f32_16x16x128_f8f6f4 v[208:211], v[122:127], v[50:55], 0 cbsz:2 blgp:2
	v_mfma_f32_16x16x128_f8f6f4 v[212:215], v[122:127], v[62:67], v[188:191] cbsz:2 blgp:2
	s_waitcnt lgkmcnt(0)
	v_mfma_f32_16x16x128_f8f6f4 v[134:137], v[128:133], v[8:13], v[134:137] cbsz:2 blgp:2
	v_mfma_f32_16x16x128_f8f6f4 v[204:207], v[128:133], v[44:49], v[204:207] cbsz:2 blgp:2
	v_mfma_f32_16x16x128_f8f6f4 v[138:141], v[128:133], v[20:25], v[138:141] cbsz:2 blgp:2
	v_mfma_f32_16x16x128_f8f6f4 v[208:211], v[128:133], v[56:61], v[208:211] cbsz:2 blgp:2
	v_mfma_f32_16x16x128_f8f6f4 v[142:145], v[128:133], v[32:37], v[142:145] cbsz:2 blgp:2
	v_mfma_f32_16x16x128_f8f6f4 v[212:215], v[128:133], v[68:73], v[212:215] cbsz:2 blgp:2
	v_cndmask_b32_e64 v158, v134, v204, s[4:5]
	v_cndmask_b32_e64 v159, v138, v208, s[4:5]
	v_fma_mix_f32 v158, v158, v1, v82 op_sel_hi:[0,0,1]
	v_fma_mix_f32 v159, v159, v99, v74 op_sel_hi:[0,0,1]
	v_exp_f32_e32 v158, v158
	v_exp_f32_e32 v159, v159
	v_fma_f32 v158, v158, v186, v186
	v_add_f32_e32 v159, 1.0, v159
	v_rcp_f32_e32 v158, v158
	v_rcp_f32_e32 v159, v159
	v_cndmask_b32_e64 v160, v142, v212, s[4:5]
	v_fma_mix_f32 v161, v158, v160, v78 op_sel_hi:[0,0,1]
	v_exp_f32_e32 v161, v161
	s_add_u32 s48, s48, s40
	v_add_f32_e32 v161, 1.0, v161
	v_rcp_f32_e32 v161, v161
	s_addc_u32 s49, s49, s41
	v_fma_f32 v162, v161, -2.0, 1.0
	v_sub_f32_e32 v163, v176, v162
	v_fma_f32 v176, v159, v163, v162
	v_fma_f32 v164, |v176|, s16, v117
	v_fma_f32 v165, |v176|, s17, v118
	v_fma_f32 v166, |v176|, s18, v119
	v_lshrrev_b32_e32 v167, 26, v176
	v_min3_u32 v164, v164, v165, v166
	v_bfi_b32 v168, 31, v164, v167
	s_nop 1
	v_mul_u32_u24_dpp v170, v168, v180 quad_perm:[1,2,3,3] row_mask:0xf bank_mask:0xf bound_ctrl:1
	v_mad_u32_u24 v171, v168, v181, v170
	ds_write_b8_d16_hi v184, v171 offset:544
	s_barrier
	global_store_short_d16_hi v185, v176, s[48:49]
	s_waitcnt lgkmcnt(0)
	s_barrier
	ds_read_b128 v[122:125], v192 offset:544
	ds_read_b64 v[126:127], v192 offset:560
	ds_read_b128 v[128:131], v192 offset:672
	ds_read_b64 v[132:133], v192 offset:688
	s_waitcnt lgkmcnt(2)
	v_mfma_f32_16x16x128_f8f6f4 v[134:137], v[122:127], v[2:7], 0 cbsz:2 blgp:2
	v_mfma_f32_16x16x128_f8f6f4 v[138:141], v[122:127], v[14:19], 0 cbsz:2 blgp:2
	v_mfma_f32_16x16x128_f8f6f4 v[142:145], v[122:127], v[26:31], v[188:191] cbsz:2 blgp:2
	v_mfma_f32_16x16x128_f8f6f4 v[204:207], v[122:127], v[38:43], 0 cbsz:2 blgp:2
	v_mfma_f32_16x16x128_f8f6f4 v[208:211], v[122:127], v[50:55], 0 cbsz:2 blgp:2
	v_mfma_f32_16x16x128_f8f6f4 v[212:215], v[122:127], v[62:67], v[188:191] cbsz:2 blgp:2
	s_waitcnt lgkmcnt(0)
	v_mfma_f32_16x16x128_f8f6f4 v[134:137], v[128:133], v[8:13], v[134:137] cbsz:2 blgp:2
	v_mfma_f32_16x16x128_f8f6f4 v[204:207], v[128:133], v[44:49], v[204:207] cbsz:2 blgp:2
	v_mfma_f32_16x16x128_f8f6f4 v[138:141], v[128:133], v[20:25], v[138:141] cbsz:2 blgp:2
	v_mfma_f32_16x16x128_f8f6f4 v[208:211], v[128:133], v[56:61], v[208:211] cbsz:2 blgp:2
	v_mfma_f32_16x16x128_f8f6f4 v[142:145], v[128:133], v[32:37], v[142:145] cbsz:2 blgp:2
	v_mfma_f32_16x16x128_f8f6f4 v[212:215], v[128:133], v[68:73], v[212:215] cbsz:2 blgp:2
	v_cndmask_b32_e64 v158, v134, v204, s[4:5]
	v_cndmask_b32_e64 v159, v138, v208, s[4:5]
	v_fma_mix_f32 v158, v158, v1, v82 op_sel:[0,0,1] op_sel_hi:[0,0,1]
	v_fma_mix_f32 v159, v159, v99, v74 op_sel:[0,0,1] op_sel_hi:[0,0,1]
	v_exp_f32_e32 v158, v158
	v_exp_f32_e32 v159, v159
	v_fma_f32 v158, v158, v186, v186
	v_add_f32_e32 v159, 1.0, v159
	v_rcp_f32_e32 v158, v158
	v_rcp_f32_e32 v159, v159
	v_cndmask_b32_e64 v160, v142, v212, s[4:5]
	v_fma_mix_f32 v161, v158, v160, v78 op_sel:[0,0,1] op_sel_hi:[0,0,1]
	v_exp_f32_e32 v161, v161
	s_add_u32 s48, s48, s40
	v_add_f32_e32 v161, 1.0, v161
	v_rcp_f32_e32 v161, v161
	s_addc_u32 s49, s49, s41
	v_fma_f32 v162, v161, -2.0, 1.0
	v_sub_f32_e32 v163, v176, v162
	v_fma_f32 v176, v159, v163, v162
	v_fma_f32 v164, |v176|, s16, v117
	v_fma_f32 v165, |v176|, s17, v118
	v_fma_f32 v166, |v176|, s18, v119
	v_lshrrev_b32_e32 v167, 26, v176
	v_min3_u32 v164, v164, v165, v166
	v_bfi_b32 v168, 31, v164, v167
	s_nop 1
	v_mul_u32_u24_dpp v170, v168, v180 quad_perm:[1,2,3,3] row_mask:0xf bank_mask:0xf bound_ctrl:1
	v_mad_u32_u24 v171, v168, v181, v170
	ds_write_b8_d16_hi v184, v171
	s_barrier
	global_store_short_d16_hi v185, v176, s[48:49]
	s_waitcnt lgkmcnt(0)
	s_barrier
	ds_read_b128 v[122:125], v192 offset:0
	ds_read_b64 v[126:127], v192 offset:16
	ds_read_b128 v[128:131], v192 offset:128
	ds_read_b64 v[132:133], v192 offset:144
	s_waitcnt lgkmcnt(2)
	v_mfma_f32_16x16x128_f8f6f4 v[134:137], v[122:127], v[2:7], 0 cbsz:2 blgp:2
	v_mfma_f32_16x16x128_f8f6f4 v[138:141], v[122:127], v[14:19], 0 cbsz:2 blgp:2
	v_mfma_f32_16x16x128_f8f6f4 v[142:145], v[122:127], v[26:31], v[188:191] cbsz:2 blgp:2
	v_mfma_f32_16x16x128_f8f6f4 v[204:207], v[122:127], v[38:43], 0 cbsz:2 blgp:2
	v_mfma_f32_16x16x128_f8f6f4 v[208:211], v[122:127], v[50:55], 0 cbsz:2 blgp:2
	v_mfma_f32_16x16x128_f8f6f4 v[212:215], v[122:127], v[62:67], v[188:191] cbsz:2 blgp:2
	s_waitcnt lgkmcnt(0)
	v_mfma_f32_16x16x128_f8f6f4 v[134:137], v[128:133], v[8:13], v[134:137] cbsz:2 blgp:2
	v_mfma_f32_16x16x128_f8f6f4 v[204:207], v[128:133], v[44:49], v[204:207] cbsz:2 blgp:2
	v_mfma_f32_16x16x128_f8f6f4 v[138:141], v[128:133], v[20:25], v[138:141] cbsz:2 blgp:2
	v_mfma_f32_16x16x128_f8f6f4 v[208:211], v[128:133], v[56:61], v[208:211] cbsz:2 blgp:2
	v_mfma_f32_16x16x128_f8f6f4 v[142:145], v[128:133], v[32:37], v[142:145] cbsz:2 blgp:2
	v_mfma_f32_16x16x128_f8f6f4 v[212:215], v[128:133], v[68:73], v[212:215] cbsz:2 blgp:2
	v_cndmask_b32_e64 v158, v134, v204, s[4:5]
	v_cndmask_b32_e64 v159, v138, v208, s[4:5]
	v_fma_mix_f32 v158, v158, v1, v83 op_sel_hi:[0,0,1]
	v_fma_mix_f32 v159, v159, v99, v75 op_sel_hi:[0,0,1]
	v_exp_f32_e32 v158, v158
	v_exp_f32_e32 v159, v159
	v_fma_f32 v158, v158, v186, v186
	v_add_f32_e32 v159, 1.0, v159
	v_rcp_f32_e32 v158, v158
	v_rcp_f32_e32 v159, v159
	v_cndmask_b32_e64 v160, v142, v212, s[4:5]
	v_fma_mix_f32 v161, v158, v160, v79 op_sel_hi:[0,0,1]
	v_exp_f32_e32 v161, v161
	s_add_u32 s48, s48, s40
	v_add_f32_e32 v161, 1.0, v161
	v_rcp_f32_e32 v161, v161
	s_addc_u32 s49, s49, s41
	v_fma_f32 v162, v161, -2.0, 1.0
	v_sub_f32_e32 v163, v176, v162
	v_fma_f32 v176, v159, v163, v162
	v_fma_f32 v164, |v176|, s16, v117
	v_fma_f32 v165, |v176|, s17, v118
	v_fma_f32 v166, |v176|, s18, v119
	v_lshrrev_b32_e32 v167, 26, v176
	v_min3_u32 v164, v164, v165, v166
	v_bfi_b32 v168, 31, v164, v167
	s_nop 1
	v_mul_u32_u24_dpp v170, v168, v180 quad_perm:[1,2,3,3] row_mask:0xf bank_mask:0xf bound_ctrl:1
	v_mad_u32_u24 v171, v168, v181, v170
	ds_write_b8_d16_hi v184, v171 offset:544
	s_barrier
	global_store_short_d16_hi v185, v176, s[48:49]
	s_waitcnt lgkmcnt(0)
	s_barrier
	ds_read_b128 v[122:125], v192 offset:544
	ds_read_b64 v[126:127], v192 offset:560
	ds_read_b128 v[128:131], v192 offset:672
	ds_read_b64 v[132:133], v192 offset:688
	s_waitcnt lgkmcnt(2)
	v_mfma_f32_16x16x128_f8f6f4 v[134:137], v[122:127], v[2:7], 0 cbsz:2 blgp:2
	v_mfma_f32_16x16x128_f8f6f4 v[138:141], v[122:127], v[14:19], 0 cbsz:2 blgp:2
	v_mfma_f32_16x16x128_f8f6f4 v[142:145], v[122:127], v[26:31], v[188:191] cbsz:2 blgp:2
	v_mfma_f32_16x16x128_f8f6f4 v[204:207], v[122:127], v[38:43], 0 cbsz:2 blgp:2
	v_mfma_f32_16x16x128_f8f6f4 v[208:211], v[122:127], v[50:55], 0 cbsz:2 blgp:2
	v_mfma_f32_16x16x128_f8f6f4 v[212:215], v[122:127], v[62:67], v[188:191] cbsz:2 blgp:2
	s_waitcnt lgkmcnt(0)
	v_mfma_f32_16x16x128_f8f6f4 v[134:137], v[128:133], v[8:13], v[134:137] cbsz:2 blgp:2
	v_mfma_f32_16x16x128_f8f6f4 v[204:207], v[128:133], v[44:49], v[204:207] cbsz:2 blgp:2
	v_mfma_f32_16x16x128_f8f6f4 v[138:141], v[128:133], v[20:25], v[138:141] cbsz:2 blgp:2
	v_mfma_f32_16x16x128_f8f6f4 v[208:211], v[128:133], v[56:61], v[208:211] cbsz:2 blgp:2
	v_mfma_f32_16x16x128_f8f6f4 v[142:145], v[128:133], v[32:37], v[142:145] cbsz:2 blgp:2
	v_mfma_f32_16x16x128_f8f6f4 v[212:215], v[128:133], v[68:73], v[212:215] cbsz:2 blgp:2
	v_cndmask_b32_e64 v158, v134, v204, s[4:5]
	v_cndmask_b32_e64 v159, v138, v208, s[4:5]
	v_fma_mix_f32 v158, v158, v1, v83 op_sel:[0,0,1] op_sel_hi:[0,0,1]
	v_fma_mix_f32 v159, v159, v99, v75 op_sel:[0,0,1] op_sel_hi:[0,0,1]
	v_exp_f32_e32 v158, v158
	v_exp_f32_e32 v159, v159
	v_fma_f32 v158, v158, v186, v186
	v_add_f32_e32 v159, 1.0, v159
	v_rcp_f32_e32 v158, v158
	v_rcp_f32_e32 v159, v159
	v_cndmask_b32_e64 v160, v142, v212, s[4:5]
	v_fma_mix_f32 v161, v158, v160, v79 op_sel:[0,0,1] op_sel_hi:[0,0,1]
	v_exp_f32_e32 v161, v161
	s_add_u32 s48, s48, s40
	v_add_f32_e32 v161, 1.0, v161
	v_rcp_f32_e32 v161, v161
	s_addc_u32 s49, s49, s41
	v_fma_f32 v162, v161, -2.0, 1.0
	v_sub_f32_e32 v163, v176, v162
	v_fma_f32 v176, v159, v163, v162
	v_fma_f32 v164, |v176|, s16, v117
	v_fma_f32 v165, |v176|, s17, v118
	v_fma_f32 v166, |v176|, s18, v119
	v_lshrrev_b32_e32 v167, 26, v176
	v_min3_u32 v164, v164, v165, v166
	v_bfi_b32 v168, 31, v164, v167
	s_nop 1
	v_mul_u32_u24_dpp v170, v168, v180 quad_perm:[1,2,3,3] row_mask:0xf bank_mask:0xf bound_ctrl:1
	v_mad_u32_u24 v171, v168, v181, v170
	ds_write_b8_d16_hi v184, v171
	s_barrier
	global_store_short_d16_hi v185, v176, s[48:49]
	s_waitcnt lgkmcnt(0)
	s_barrier
	ds_read_b128 v[122:125], v192 offset:0
	ds_read_b64 v[126:127], v192 offset:16
	ds_read_b128 v[128:131], v192 offset:128
	ds_read_b64 v[132:133], v192 offset:144
	s_waitcnt lgkmcnt(2)
	v_mfma_f32_16x16x128_f8f6f4 v[134:137], v[122:127], v[2:7], 0 cbsz:2 blgp:2
	v_mfma_f32_16x16x128_f8f6f4 v[138:141], v[122:127], v[14:19], 0 cbsz:2 blgp:2
	v_mfma_f32_16x16x128_f8f6f4 v[142:145], v[122:127], v[26:31], v[188:191] cbsz:2 blgp:2
	v_mfma_f32_16x16x128_f8f6f4 v[204:207], v[122:127], v[38:43], 0 cbsz:2 blgp:2
	v_mfma_f32_16x16x128_f8f6f4 v[208:211], v[122:127], v[50:55], 0 cbsz:2 blgp:2
	v_mfma_f32_16x16x128_f8f6f4 v[212:215], v[122:127], v[62:67], v[188:191] cbsz:2 blgp:2
	s_waitcnt lgkmcnt(0)
	v_mfma_f32_16x16x128_f8f6f4 v[134:137], v[128:133], v[8:13], v[134:137] cbsz:2 blgp:2
	v_mfma_f32_16x16x128_f8f6f4 v[204:207], v[128:133], v[44:49], v[204:207] cbsz:2 blgp:2
	v_mfma_f32_16x16x128_f8f6f4 v[138:141], v[128:133], v[20:25], v[138:141] cbsz:2 blgp:2
	v_mfma_f32_16x16x128_f8f6f4 v[208:211], v[128:133], v[56:61], v[208:211] cbsz:2 blgp:2
	v_mfma_f32_16x16x128_f8f6f4 v[142:145], v[128:133], v[32:37], v[142:145] cbsz:2 blgp:2
	v_mfma_f32_16x16x128_f8f6f4 v[212:215], v[128:133], v[68:73], v[212:215] cbsz:2 blgp:2
	v_cndmask_b32_e64 v158, v134, v204, s[4:5]
	v_cndmask_b32_e64 v159, v138, v208, s[4:5]
	v_fma_mix_f32 v158, v158, v1, v84 op_sel_hi:[0,0,1]
	v_fma_mix_f32 v159, v159, v99, v76 op_sel_hi:[0,0,1]
	v_exp_f32_e32 v158, v158
	v_exp_f32_e32 v159, v159
	v_fma_f32 v158, v158, v186, v186
	v_add_f32_e32 v159, 1.0, v159
	v_rcp_f32_e32 v158, v158
	v_rcp_f32_e32 v159, v159
	v_cndmask_b32_e64 v160, v142, v212, s[4:5]
	v_fma_mix_f32 v161, v158, v160, v80 op_sel_hi:[0,0,1]
	v_exp_f32_e32 v161, v161
	s_add_u32 s48, s48, s40
	v_add_f32_e32 v161, 1.0, v161
	v_rcp_f32_e32 v161, v161
	s_addc_u32 s49, s49, s41
	v_fma_f32 v162, v161, -2.0, 1.0
	v_sub_f32_e32 v163, v176, v162
	v_fma_f32 v176, v159, v163, v162
	v_fma_f32 v164, |v176|, s16, v117
	v_fma_f32 v165, |v176|, s17, v118
	v_fma_f32 v166, |v176|, s18, v119
	v_lshrrev_b32_e32 v167, 26, v176
	v_min3_u32 v164, v164, v165, v166
	v_bfi_b32 v168, 31, v164, v167
	s_nop 1
	v_mul_u32_u24_dpp v170, v168, v180 quad_perm:[1,2,3,3] row_mask:0xf bank_mask:0xf bound_ctrl:1
	v_mad_u32_u24 v171, v168, v181, v170
	ds_write_b8_d16_hi v184, v171 offset:544
	s_barrier
	global_store_short_d16_hi v185, v176, s[48:49]
	s_waitcnt lgkmcnt(0)
	s_barrier
	ds_read_b128 v[122:125], v192 offset:544
	ds_read_b64 v[126:127], v192 offset:560
	ds_read_b128 v[128:131], v192 offset:672
	ds_read_b64 v[132:133], v192 offset:688
	s_waitcnt lgkmcnt(2)
	v_mfma_f32_16x16x128_f8f6f4 v[134:137], v[122:127], v[2:7], 0 cbsz:2 blgp:2
	v_mfma_f32_16x16x128_f8f6f4 v[138:141], v[122:127], v[14:19], 0 cbsz:2 blgp:2
	v_mfma_f32_16x16x128_f8f6f4 v[142:145], v[122:127], v[26:31], v[188:191] cbsz:2 blgp:2
	v_mfma_f32_16x16x128_f8f6f4 v[204:207], v[122:127], v[38:43], 0 cbsz:2 blgp:2
	v_mfma_f32_16x16x128_f8f6f4 v[208:211], v[122:127], v[50:55], 0 cbsz:2 blgp:2
	v_mfma_f32_16x16x128_f8f6f4 v[212:215], v[122:127], v[62:67], v[188:191] cbsz:2 blgp:2
	s_waitcnt lgkmcnt(0)
	v_mfma_f32_16x16x128_f8f6f4 v[134:137], v[128:133], v[8:13], v[134:137] cbsz:2 blgp:2
	v_mfma_f32_16x16x128_f8f6f4 v[204:207], v[128:133], v[44:49], v[204:207] cbsz:2 blgp:2
	v_mfma_f32_16x16x128_f8f6f4 v[138:141], v[128:133], v[20:25], v[138:141] cbsz:2 blgp:2
	v_mfma_f32_16x16x128_f8f6f4 v[208:211], v[128:133], v[56:61], v[208:211] cbsz:2 blgp:2
	v_mfma_f32_16x16x128_f8f6f4 v[142:145], v[128:133], v[32:37], v[142:145] cbsz:2 blgp:2
	v_mfma_f32_16x16x128_f8f6f4 v[212:215], v[128:133], v[68:73], v[212:215] cbsz:2 blgp:2
	v_cndmask_b32_e64 v158, v134, v204, s[4:5]
	v_cndmask_b32_e64 v159, v138, v208, s[4:5]
	v_fma_mix_f32 v158, v158, v1, v84 op_sel:[0,0,1] op_sel_hi:[0,0,1]
	v_fma_mix_f32 v159, v159, v99, v76 op_sel:[0,0,1] op_sel_hi:[0,0,1]
	v_exp_f32_e32 v158, v158
	v_exp_f32_e32 v159, v159
	v_fma_f32 v158, v158, v186, v186
	v_add_f32_e32 v159, 1.0, v159
	v_rcp_f32_e32 v158, v158
	v_rcp_f32_e32 v159, v159
	v_cndmask_b32_e64 v160, v142, v212, s[4:5]
	v_fma_mix_f32 v161, v158, v160, v80 op_sel:[0,0,1] op_sel_hi:[0,0,1]
	v_exp_f32_e32 v161, v161
	s_add_u32 s48, s48, s40
	v_add_f32_e32 v161, 1.0, v161
	v_rcp_f32_e32 v161, v161
	s_addc_u32 s49, s49, s41
	v_fma_f32 v162, v161, -2.0, 1.0
	v_sub_f32_e32 v163, v176, v162
	v_fma_f32 v176, v159, v163, v162
	v_fma_f32 v164, |v176|, s16, v117
	v_fma_f32 v165, |v176|, s17, v118
	v_fma_f32 v166, |v176|, s18, v119
	v_lshrrev_b32_e32 v167, 26, v176
	v_min3_u32 v164, v164, v165, v166
	v_bfi_b32 v168, 31, v164, v167
	s_nop 1
	v_mul_u32_u24_dpp v170, v168, v180 quad_perm:[1,2,3,3] row_mask:0xf bank_mask:0xf bound_ctrl:1
	v_mad_u32_u24 v171, v168, v181, v170
	ds_write_b8_d16_hi v184, v171
	s_barrier
	global_store_short_d16_hi v185, v176, s[48:49]
	s_waitcnt lgkmcnt(0)
	s_barrier
	ds_read_b128 v[122:125], v192 offset:0
	ds_read_b64 v[126:127], v192 offset:16
	ds_read_b128 v[128:131], v192 offset:128
	ds_read_b64 v[132:133], v192 offset:144
	s_waitcnt lgkmcnt(2)
	v_mfma_f32_16x16x128_f8f6f4 v[134:137], v[122:127], v[2:7], 0 cbsz:2 blgp:2
	v_mfma_f32_16x16x128_f8f6f4 v[138:141], v[122:127], v[14:19], 0 cbsz:2 blgp:2
	v_mfma_f32_16x16x128_f8f6f4 v[142:145], v[122:127], v[26:31], v[188:191] cbsz:2 blgp:2
	v_mfma_f32_16x16x128_f8f6f4 v[204:207], v[122:127], v[38:43], 0 cbsz:2 blgp:2
	v_mfma_f32_16x16x128_f8f6f4 v[208:211], v[122:127], v[50:55], 0 cbsz:2 blgp:2
	v_mfma_f32_16x16x128_f8f6f4 v[212:215], v[122:127], v[62:67], v[188:191] cbsz:2 blgp:2
	s_waitcnt lgkmcnt(0)
	v_mfma_f32_16x16x128_f8f6f4 v[134:137], v[128:133], v[8:13], v[134:137] cbsz:2 blgp:2
	v_mfma_f32_16x16x128_f8f6f4 v[204:207], v[128:133], v[44:49], v[204:207] cbsz:2 blgp:2
	v_mfma_f32_16x16x128_f8f6f4 v[138:141], v[128:133], v[20:25], v[138:141] cbsz:2 blgp:2
	v_mfma_f32_16x16x128_f8f6f4 v[208:211], v[128:133], v[56:61], v[208:211] cbsz:2 blgp:2
	v_mfma_f32_16x16x128_f8f6f4 v[142:145], v[128:133], v[32:37], v[142:145] cbsz:2 blgp:2
	v_mfma_f32_16x16x128_f8f6f4 v[212:215], v[128:133], v[68:73], v[212:215] cbsz:2 blgp:2
	v_cndmask_b32_e64 v158, v134, v204, s[4:5]
	v_cndmask_b32_e64 v159, v138, v208, s[4:5]
	v_fma_mix_f32 v158, v158, v1, v85 op_sel_hi:[0,0,1]
	v_fma_mix_f32 v159, v159, v99, v77 op_sel_hi:[0,0,1]
	v_exp_f32_e32 v158, v158
	v_exp_f32_e32 v159, v159
	v_fma_f32 v158, v158, v186, v186
	v_add_f32_e32 v159, 1.0, v159
	v_rcp_f32_e32 v158, v158
	v_rcp_f32_e32 v159, v159
	v_cndmask_b32_e64 v160, v142, v212, s[4:5]
	v_fma_mix_f32 v161, v158, v160, v81 op_sel_hi:[0,0,1]
	v_exp_f32_e32 v161, v161
	s_add_u32 s48, s48, s40
	v_add_f32_e32 v161, 1.0, v161
	v_rcp_f32_e32 v161, v161
	s_addc_u32 s49, s49, s41
	v_fma_f32 v162, v161, -2.0, 1.0
	v_sub_f32_e32 v163, v176, v162
	v_fma_f32 v176, v159, v163, v162
	v_fma_f32 v164, |v176|, s16, v117
	v_fma_f32 v165, |v176|, s17, v118
	v_fma_f32 v166, |v176|, s18, v119
	v_lshrrev_b32_e32 v167, 26, v176
	v_min3_u32 v164, v164, v165, v166
	v_bfi_b32 v168, 31, v164, v167
	s_nop 1
	v_mul_u32_u24_dpp v170, v168, v180 quad_perm:[1,2,3,3] row_mask:0xf bank_mask:0xf bound_ctrl:1
	v_mad_u32_u24 v171, v168, v181, v170
	ds_write_b8_d16_hi v184, v171 offset:544
	s_barrier
	global_store_short_d16_hi v185, v176, s[48:49]
	s_waitcnt lgkmcnt(0)
	s_barrier
	ds_read_b128 v[122:125], v192 offset:544
	ds_read_b64 v[126:127], v192 offset:560
	ds_read_b128 v[128:131], v192 offset:672
	ds_read_b64 v[132:133], v192 offset:688
	s_waitcnt lgkmcnt(2)
	v_mfma_f32_16x16x128_f8f6f4 v[134:137], v[122:127], v[2:7], 0 cbsz:2 blgp:2
	v_mfma_f32_16x16x128_f8f6f4 v[138:141], v[122:127], v[14:19], 0 cbsz:2 blgp:2
	v_mfma_f32_16x16x128_f8f6f4 v[142:145], v[122:127], v[26:31], v[188:191] cbsz:2 blgp:2
	v_mfma_f32_16x16x128_f8f6f4 v[204:207], v[122:127], v[38:43], 0 cbsz:2 blgp:2
	v_mfma_f32_16x16x128_f8f6f4 v[208:211], v[122:127], v[50:55], 0 cbsz:2 blgp:2
	v_mfma_f32_16x16x128_f8f6f4 v[212:215], v[122:127], v[62:67], v[188:191] cbsz:2 blgp:2
	s_waitcnt lgkmcnt(0)
	v_mfma_f32_16x16x128_f8f6f4 v[134:137], v[128:133], v[8:13], v[134:137] cbsz:2 blgp:2
	v_mfma_f32_16x16x128_f8f6f4 v[204:207], v[128:133], v[44:49], v[204:207] cbsz:2 blgp:2
	v_mfma_f32_16x16x128_f8f6f4 v[138:141], v[128:133], v[20:25], v[138:141] cbsz:2 blgp:2
	v_mfma_f32_16x16x128_f8f6f4 v[208:211], v[128:133], v[56:61], v[208:211] cbsz:2 blgp:2
	v_mfma_f32_16x16x128_f8f6f4 v[142:145], v[128:133], v[32:37], v[142:145] cbsz:2 blgp:2
	v_mfma_f32_16x16x128_f8f6f4 v[212:215], v[128:133], v[68:73], v[212:215] cbsz:2 blgp:2
	v_cndmask_b32_e64 v158, v134, v204, s[4:5]
	v_cndmask_b32_e64 v159, v138, v208, s[4:5]
	v_fma_mix_f32 v158, v158, v1, v85 op_sel:[0,0,1] op_sel_hi:[0,0,1]
	v_fma_mix_f32 v159, v159, v99, v77 op_sel:[0,0,1] op_sel_hi:[0,0,1]
	v_exp_f32_e32 v158, v158
	v_exp_f32_e32 v159, v159
	v_fma_f32 v158, v158, v186, v186
	v_add_f32_e32 v159, 1.0, v159
	v_rcp_f32_e32 v158, v158
	v_rcp_f32_e32 v159, v159
	v_cndmask_b32_e64 v160, v142, v212, s[4:5]
	v_fma_mix_f32 v161, v158, v160, v81 op_sel:[0,0,1] op_sel_hi:[0,0,1]
	v_exp_f32_e32 v161, v161
	s_add_u32 s48, s48, s40
	v_add_f32_e32 v161, 1.0, v161
	v_rcp_f32_e32 v161, v161
	s_addc_u32 s49, s49, s41
	v_fma_f32 v162, v161, -2.0, 1.0
	v_sub_f32_e32 v163, v176, v162
	v_fma_f32 v176, v159, v163, v162
	v_fma_f32 v164, |v176|, s16, v117
	v_fma_f32 v165, |v176|, s17, v118
	v_fma_f32 v166, |v176|, s18, v119
	v_lshrrev_b32_e32 v167, 26, v176
	v_min3_u32 v164, v164, v165, v166
	v_bfi_b32 v168, 31, v164, v167
	s_nop 1
	v_mul_u32_u24_dpp v170, v168, v180 quad_perm:[1,2,3,3] row_mask:0xf bank_mask:0xf bound_ctrl:1
	v_mad_u32_u24 v171, v168, v181, v170
	ds_write_b8_d16_hi v184, v171
	s_barrier
	global_store_short_d16_hi v185, v176, s[48:49]
	s_waitcnt lgkmcnt(0)
	s_barrier
	ds_read_b128 v[122:125], v192 offset:0
	ds_read_b64 v[126:127], v192 offset:16
	ds_read_b128 v[128:131], v192 offset:128
	ds_read_b64 v[132:133], v192 offset:144
	s_waitcnt vmcnt(8)
	global_load_dwordx4 v[82:85], v[196:197], off
	global_load_dwordx4 v[74:77], v[196:197], off offset:512
	global_load_dwordx4 v[78:81], v[196:197], off offset:1024
	v_lshl_add_u64 v[196:197], v[196:197], 0, s[42:43]
	s_waitcnt lgkmcnt(2)
	v_mfma_f32_16x16x128_f8f6f4 v[134:137], v[122:127], v[2:7], 0 cbsz:2 blgp:2
	v_mfma_f32_16x16x128_f8f6f4 v[138:141], v[122:127], v[14:19], 0 cbsz:2 blgp:2
	v_mfma_f32_16x16x128_f8f6f4 v[142:145], v[122:127], v[26:31], v[188:191] cbsz:2 blgp:2
	v_mfma_f32_16x16x128_f8f6f4 v[204:207], v[122:127], v[38:43], 0 cbsz:2 blgp:2
	v_mfma_f32_16x16x128_f8f6f4 v[208:211], v[122:127], v[50:55], 0 cbsz:2 blgp:2
	v_mfma_f32_16x16x128_f8f6f4 v[212:215], v[122:127], v[62:67], v[188:191] cbsz:2 blgp:2
	s_waitcnt lgkmcnt(0)
	v_mfma_f32_16x16x128_f8f6f4 v[134:137], v[128:133], v[8:13], v[134:137] cbsz:2 blgp:2
	v_mfma_f32_16x16x128_f8f6f4 v[204:207], v[128:133], v[44:49], v[204:207] cbsz:2 blgp:2
	v_mfma_f32_16x16x128_f8f6f4 v[138:141], v[128:133], v[20:25], v[138:141] cbsz:2 blgp:2
	v_mfma_f32_16x16x128_f8f6f4 v[208:211], v[128:133], v[56:61], v[208:211] cbsz:2 blgp:2
	v_mfma_f32_16x16x128_f8f6f4 v[142:145], v[128:133], v[32:37], v[142:145] cbsz:2 blgp:2
	v_mfma_f32_16x16x128_f8f6f4 v[212:215], v[128:133], v[68:73], v[212:215] cbsz:2 blgp:2
	v_cndmask_b32_e64 v158, v134, v204, s[4:5]
	v_cndmask_b32_e64 v159, v138, v208, s[4:5]
	v_fma_mix_f32 v158, v158, v1, v146 op_sel_hi:[0,0,1]
	v_fma_mix_f32 v159, v159, v99, v150 op_sel_hi:[0,0,1]
	v_exp_f32_e32 v158, v158
	v_exp_f32_e32 v159, v159
	v_fma_f32 v158, v158, v186, v186
	v_add_f32_e32 v159, 1.0, v159
	v_rcp_f32_e32 v158, v158
	v_rcp_f32_e32 v159, v159
	v_cndmask_b32_e64 v160, v142, v212, s[4:5]
	v_fma_mix_f32 v161, v158, v160, v154 op_sel_hi:[0,0,1]
	v_exp_f32_e32 v161, v161
	s_add_u32 s48, s48, s40
	v_add_f32_e32 v161, 1.0, v161
	v_rcp_f32_e32 v161, v161
	s_addc_u32 s49, s49, s41
	v_fma_f32 v162, v161, -2.0, 1.0
	v_sub_f32_e32 v163, v176, v162
	v_fma_f32 v176, v159, v163, v162
	v_fma_f32 v164, |v176|, s16, v117
	v_fma_f32 v165, |v176|, s17, v118
	v_fma_f32 v166, |v176|, s18, v119
	v_lshrrev_b32_e32 v167, 26, v176
	v_min3_u32 v164, v164, v165, v166
	v_bfi_b32 v168, 31, v164, v167
	s_nop 1
	v_mul_u32_u24_dpp v170, v168, v180 quad_perm:[1,2,3,3] row_mask:0xf bank_mask:0xf bound_ctrl:1
	v_mad_u32_u24 v171, v168, v181, v170
	ds_write_b8_d16_hi v184, v171 offset:544
	s_barrier
	global_store_short_d16_hi v185, v176, s[48:49]
	s_waitcnt lgkmcnt(0)
	s_barrier
	ds_read_b128 v[122:125], v192 offset:544
	ds_read_b64 v[126:127], v192 offset:560
	ds_read_b128 v[128:131], v192 offset:672
	ds_read_b64 v[132:133], v192 offset:688
	s_waitcnt lgkmcnt(2)
	v_mfma_f32_16x16x128_f8f6f4 v[134:137], v[122:127], v[2:7], 0 cbsz:2 blgp:2
	v_mfma_f32_16x16x128_f8f6f4 v[138:141], v[122:127], v[14:19], 0 cbsz:2 blgp:2
	v_mfma_f32_16x16x128_f8f6f4 v[142:145], v[122:127], v[26:31], v[188:191] cbsz:2 blgp:2
	v_mfma_f32_16x16x128_f8f6f4 v[204:207], v[122:127], v[38:43], 0 cbsz:2 blgp:2
	v_mfma_f32_16x16x128_f8f6f4 v[208:211], v[122:127], v[50:55], 0 cbsz:2 blgp:2
	v_mfma_f32_16x16x128_f8f6f4 v[212:215], v[122:127], v[62:67], v[188:191] cbsz:2 blgp:2
	s_waitcnt lgkmcnt(0)
	v_mfma_f32_16x16x128_f8f6f4 v[134:137], v[128:133], v[8:13], v[134:137] cbsz:2 blgp:2
	v_mfma_f32_16x16x128_f8f6f4 v[204:207], v[128:133], v[44:49], v[204:207] cbsz:2 blgp:2
	v_mfma_f32_16x16x128_f8f6f4 v[138:141], v[128:133], v[20:25], v[138:141] cbsz:2 blgp:2
	v_mfma_f32_16x16x128_f8f6f4 v[208:211], v[128:133], v[56:61], v[208:211] cbsz:2 blgp:2
	v_mfma_f32_16x16x128_f8f6f4 v[142:145], v[128:133], v[32:37], v[142:145] cbsz:2 blgp:2
	v_mfma_f32_16x16x128_f8f6f4 v[212:215], v[128:133], v[68:73], v[212:215] cbsz:2 blgp:2
	v_cndmask_b32_e64 v158, v134, v204, s[4:5]
	v_cndmask_b32_e64 v159, v138, v208, s[4:5]
	v_fma_mix_f32 v158, v158, v1, v146 op_sel:[0,0,1] op_sel_hi:[0,0,1]
	v_fma_mix_f32 v159, v159, v99, v150 op_sel:[0,0,1] op_sel_hi:[0,0,1]
	v_exp_f32_e32 v158, v158
	v_exp_f32_e32 v159, v159
	v_fma_f32 v158, v158, v186, v186
	v_add_f32_e32 v159, 1.0, v159
	v_rcp_f32_e32 v158, v158
	v_rcp_f32_e32 v159, v159
	v_cndmask_b32_e64 v160, v142, v212, s[4:5]
	v_fma_mix_f32 v161, v158, v160, v154 op_sel:[0,0,1] op_sel_hi:[0,0,1]
	v_exp_f32_e32 v161, v161
	s_add_u32 s48, s48, s40
	v_add_f32_e32 v161, 1.0, v161
	v_rcp_f32_e32 v161, v161
	s_addc_u32 s49, s49, s41
	v_fma_f32 v162, v161, -2.0, 1.0
	v_sub_f32_e32 v163, v176, v162
	v_fma_f32 v176, v159, v163, v162
	v_fma_f32 v164, |v176|, s16, v117
	v_fma_f32 v165, |v176|, s17, v118
	v_fma_f32 v166, |v176|, s18, v119
	v_lshrrev_b32_e32 v167, 26, v176
	v_min3_u32 v164, v164, v165, v166
	v_bfi_b32 v168, 31, v164, v167
	s_nop 1
	v_mul_u32_u24_dpp v170, v168, v180 quad_perm:[1,2,3,3] row_mask:0xf bank_mask:0xf bound_ctrl:1
	v_mad_u32_u24 v171, v168, v181, v170
	ds_write_b8_d16_hi v184, v171
	s_barrier
	global_store_short_d16_hi v185, v176, s[48:49]
	s_waitcnt lgkmcnt(0)
	s_barrier
	ds_read_b128 v[122:125], v192 offset:0
	ds_read_b64 v[126:127], v192 offset:16
	ds_read_b128 v[128:131], v192 offset:128
	ds_read_b64 v[132:133], v192 offset:144
	s_waitcnt lgkmcnt(2)
	v_mfma_f32_16x16x128_f8f6f4 v[134:137], v[122:127], v[2:7], 0 cbsz:2 blgp:2
	v_mfma_f32_16x16x128_f8f6f4 v[138:141], v[122:127], v[14:19], 0 cbsz:2 blgp:2
	v_mfma_f32_16x16x128_f8f6f4 v[142:145], v[122:127], v[26:31], v[188:191] cbsz:2 blgp:2
	v_mfma_f32_16x16x128_f8f6f4 v[204:207], v[122:127], v[38:43], 0 cbsz:2 blgp:2
	v_mfma_f32_16x16x128_f8f6f4 v[208:211], v[122:127], v[50:55], 0 cbsz:2 blgp:2
	v_mfma_f32_16x16x128_f8f6f4 v[212:215], v[122:127], v[62:67], v[188:191] cbsz:2 blgp:2
	s_waitcnt lgkmcnt(0)
	v_mfma_f32_16x16x128_f8f6f4 v[134:137], v[128:133], v[8:13], v[134:137] cbsz:2 blgp:2
	v_mfma_f32_16x16x128_f8f6f4 v[204:207], v[128:133], v[44:49], v[204:207] cbsz:2 blgp:2
	v_mfma_f32_16x16x128_f8f6f4 v[138:141], v[128:133], v[20:25], v[138:141] cbsz:2 blgp:2
	v_mfma_f32_16x16x128_f8f6f4 v[208:211], v[128:133], v[56:61], v[208:211] cbsz:2 blgp:2
	v_mfma_f32_16x16x128_f8f6f4 v[142:145], v[128:133], v[32:37], v[142:145] cbsz:2 blgp:2
	v_mfma_f32_16x16x128_f8f6f4 v[212:215], v[128:133], v[68:73], v[212:215] cbsz:2 blgp:2
	v_cndmask_b32_e64 v158, v134, v204, s[4:5]
	v_cndmask_b32_e64 v159, v138, v208, s[4:5]
	v_fma_mix_f32 v158, v158, v1, v147 op_sel_hi:[0,0,1]
	v_fma_mix_f32 v159, v159, v99, v151 op_sel_hi:[0,0,1]
	v_exp_f32_e32 v158, v158
	v_exp_f32_e32 v159, v159
	v_fma_f32 v158, v158, v186, v186
	v_add_f32_e32 v159, 1.0, v159
	v_rcp_f32_e32 v158, v158
	v_rcp_f32_e32 v159, v159
	v_cndmask_b32_e64 v160, v142, v212, s[4:5]
	v_fma_mix_f32 v161, v158, v160, v155 op_sel_hi:[0,0,1]
	v_exp_f32_e32 v161, v161
	s_add_u32 s48, s48, s40
	v_add_f32_e32 v161, 1.0, v161
	v_rcp_f32_e32 v161, v161
	s_addc_u32 s49, s49, s41
	v_fma_f32 v162, v161, -2.0, 1.0
	v_sub_f32_e32 v163, v176, v162
	v_fma_f32 v176, v159, v163, v162
	v_fma_f32 v164, |v176|, s16, v117
	v_fma_f32 v165, |v176|, s17, v118
	v_fma_f32 v166, |v176|, s18, v119
	v_lshrrev_b32_e32 v167, 26, v176
	v_min3_u32 v164, v164, v165, v166
	v_bfi_b32 v168, 31, v164, v167
	s_nop 1
	v_mul_u32_u24_dpp v170, v168, v180 quad_perm:[1,2,3,3] row_mask:0xf bank_mask:0xf bound_ctrl:1
	v_mad_u32_u24 v171, v168, v181, v170
	ds_write_b8_d16_hi v184, v171 offset:544
	s_barrier
	global_store_short_d16_hi v185, v176, s[48:49]
	s_waitcnt lgkmcnt(0)
	s_barrier
	ds_read_b128 v[122:125], v192 offset:544
	ds_read_b64 v[126:127], v192 offset:560
	ds_read_b128 v[128:131], v192 offset:672
	ds_read_b64 v[132:133], v192 offset:688
	s_waitcnt lgkmcnt(2)
	v_mfma_f32_16x16x128_f8f6f4 v[134:137], v[122:127], v[2:7], 0 cbsz:2 blgp:2
	v_mfma_f32_16x16x128_f8f6f4 v[138:141], v[122:127], v[14:19], 0 cbsz:2 blgp:2
	v_mfma_f32_16x16x128_f8f6f4 v[142:145], v[122:127], v[26:31], v[188:191] cbsz:2 blgp:2
	v_mfma_f32_16x16x128_f8f6f4 v[204:207], v[122:127], v[38:43], 0 cbsz:2 blgp:2
	v_mfma_f32_16x16x128_f8f6f4 v[208:211], v[122:127], v[50:55], 0 cbsz:2 blgp:2
	v_mfma_f32_16x16x128_f8f6f4 v[212:215], v[122:127], v[62:67], v[188:191] cbsz:2 blgp:2
	s_waitcnt lgkmcnt(0)
	v_mfma_f32_16x16x128_f8f6f4 v[134:137], v[128:133], v[8:13], v[134:137] cbsz:2 blgp:2
	v_mfma_f32_16x16x128_f8f6f4 v[204:207], v[128:133], v[44:49], v[204:207] cbsz:2 blgp:2
	v_mfma_f32_16x16x128_f8f6f4 v[138:141], v[128:133], v[20:25], v[138:141] cbsz:2 blgp:2
	v_mfma_f32_16x16x128_f8f6f4 v[208:211], v[128:133], v[56:61], v[208:211] cbsz:2 blgp:2
	v_mfma_f32_16x16x128_f8f6f4 v[142:145], v[128:133], v[32:37], v[142:145] cbsz:2 blgp:2
	v_mfma_f32_16x16x128_f8f6f4 v[212:215], v[128:133], v[68:73], v[212:215] cbsz:2 blgp:2
	v_cndmask_b32_e64 v158, v134, v204, s[4:5]
	v_cndmask_b32_e64 v159, v138, v208, s[4:5]
	v_fma_mix_f32 v158, v158, v1, v147 op_sel:[0,0,1] op_sel_hi:[0,0,1]
	v_fma_mix_f32 v159, v159, v99, v151 op_sel:[0,0,1] op_sel_hi:[0,0,1]
	v_exp_f32_e32 v158, v158
	v_exp_f32_e32 v159, v159
	v_fma_f32 v158, v158, v186, v186
	v_add_f32_e32 v159, 1.0, v159
	v_rcp_f32_e32 v158, v158
	v_rcp_f32_e32 v159, v159
	v_cndmask_b32_e64 v160, v142, v212, s[4:5]
	v_fma_mix_f32 v161, v158, v160, v155 op_sel:[0,0,1] op_sel_hi:[0,0,1]
	v_exp_f32_e32 v161, v161
	s_add_u32 s48, s48, s40
	v_add_f32_e32 v161, 1.0, v161
	v_rcp_f32_e32 v161, v161
	s_addc_u32 s49, s49, s41
	v_fma_f32 v162, v161, -2.0, 1.0
	v_sub_f32_e32 v163, v176, v162
	v_fma_f32 v176, v159, v163, v162
	v_fma_f32 v164, |v176|, s16, v117
	v_fma_f32 v165, |v176|, s17, v118
	v_fma_f32 v166, |v176|, s18, v119
	v_lshrrev_b32_e32 v167, 26, v176
	v_min3_u32 v164, v164, v165, v166
	v_bfi_b32 v168, 31, v164, v167
	s_nop 1
	v_mul_u32_u24_dpp v170, v168, v180 quad_perm:[1,2,3,3] row_mask:0xf bank_mask:0xf bound_ctrl:1
	v_mad_u32_u24 v171, v168, v181, v170
	ds_write_b8_d16_hi v184, v171
	s_barrier
	global_store_short_d16_hi v185, v176, s[48:49]
	s_waitcnt lgkmcnt(0)
	s_barrier
	ds_read_b128 v[122:125], v192 offset:0
	ds_read_b64 v[126:127], v192 offset:16
	ds_read_b128 v[128:131], v192 offset:128
	ds_read_b64 v[132:133], v192 offset:144
	s_waitcnt lgkmcnt(2)
	v_mfma_f32_16x16x128_f8f6f4 v[134:137], v[122:127], v[2:7], 0 cbsz:2 blgp:2
	v_mfma_f32_16x16x128_f8f6f4 v[138:141], v[122:127], v[14:19], 0 cbsz:2 blgp:2
	v_mfma_f32_16x16x128_f8f6f4 v[142:145], v[122:127], v[26:31], v[188:191] cbsz:2 blgp:2
	v_mfma_f32_16x16x128_f8f6f4 v[204:207], v[122:127], v[38:43], 0 cbsz:2 blgp:2
	v_mfma_f32_16x16x128_f8f6f4 v[208:211], v[122:127], v[50:55], 0 cbsz:2 blgp:2
	v_mfma_f32_16x16x128_f8f6f4 v[212:215], v[122:127], v[62:67], v[188:191] cbsz:2 blgp:2
	s_waitcnt lgkmcnt(0)
	v_mfma_f32_16x16x128_f8f6f4 v[134:137], v[128:133], v[8:13], v[134:137] cbsz:2 blgp:2
	v_mfma_f32_16x16x128_f8f6f4 v[204:207], v[128:133], v[44:49], v[204:207] cbsz:2 blgp:2
	v_mfma_f32_16x16x128_f8f6f4 v[138:141], v[128:133], v[20:25], v[138:141] cbsz:2 blgp:2
	v_mfma_f32_16x16x128_f8f6f4 v[208:211], v[128:133], v[56:61], v[208:211] cbsz:2 blgp:2
	v_mfma_f32_16x16x128_f8f6f4 v[142:145], v[128:133], v[32:37], v[142:145] cbsz:2 blgp:2
	v_mfma_f32_16x16x128_f8f6f4 v[212:215], v[128:133], v[68:73], v[212:215] cbsz:2 blgp:2
	v_cndmask_b32_e64 v158, v134, v204, s[4:5]
	v_cndmask_b32_e64 v159, v138, v208, s[4:5]
	v_fma_mix_f32 v158, v158, v1, v148 op_sel_hi:[0,0,1]
	v_fma_mix_f32 v159, v159, v99, v152 op_sel_hi:[0,0,1]
	v_exp_f32_e32 v158, v158
	v_exp_f32_e32 v159, v159
	v_fma_f32 v158, v158, v186, v186
	v_add_f32_e32 v159, 1.0, v159
	v_rcp_f32_e32 v158, v158
	v_rcp_f32_e32 v159, v159
	v_cndmask_b32_e64 v160, v142, v212, s[4:5]
	v_fma_mix_f32 v161, v158, v160, v156 op_sel_hi:[0,0,1]
	v_exp_f32_e32 v161, v161
	s_add_u32 s48, s48, s40
	v_add_f32_e32 v161, 1.0, v161
	v_rcp_f32_e32 v161, v161
	s_addc_u32 s49, s49, s41
	v_fma_f32 v162, v161, -2.0, 1.0
	v_sub_f32_e32 v163, v176, v162
	v_fma_f32 v176, v159, v163, v162
	v_fma_f32 v164, |v176|, s16, v117
	v_fma_f32 v165, |v176|, s17, v118
	v_fma_f32 v166, |v176|, s18, v119
	v_lshrrev_b32_e32 v167, 26, v176
	v_min3_u32 v164, v164, v165, v166
	v_bfi_b32 v168, 31, v164, v167
	s_nop 1
	v_mul_u32_u24_dpp v170, v168, v180 quad_perm:[1,2,3,3] row_mask:0xf bank_mask:0xf bound_ctrl:1
	v_mad_u32_u24 v171, v168, v181, v170
	ds_write_b8_d16_hi v184, v171 offset:544
	s_barrier
	global_store_short_d16_hi v185, v176, s[48:49]
	s_waitcnt lgkmcnt(0)
	s_barrier
	ds_read_b128 v[122:125], v192 offset:544
	ds_read_b64 v[126:127], v192 offset:560
	ds_read_b128 v[128:131], v192 offset:672
	ds_read_b64 v[132:133], v192 offset:688
	s_waitcnt lgkmcnt(2)
	v_mfma_f32_16x16x128_f8f6f4 v[134:137], v[122:127], v[2:7], 0 cbsz:2 blgp:2
	v_mfma_f32_16x16x128_f8f6f4 v[138:141], v[122:127], v[14:19], 0 cbsz:2 blgp:2
	v_mfma_f32_16x16x128_f8f6f4 v[142:145], v[122:127], v[26:31], v[188:191] cbsz:2 blgp:2
	v_mfma_f32_16x16x128_f8f6f4 v[204:207], v[122:127], v[38:43], 0 cbsz:2 blgp:2
	v_mfma_f32_16x16x128_f8f6f4 v[208:211], v[122:127], v[50:55], 0 cbsz:2 blgp:2
	v_mfma_f32_16x16x128_f8f6f4 v[212:215], v[122:127], v[62:67], v[188:191] cbsz:2 blgp:2
	s_waitcnt lgkmcnt(0)
	v_mfma_f32_16x16x128_f8f6f4 v[134:137], v[128:133], v[8:13], v[134:137] cbsz:2 blgp:2
	v_mfma_f32_16x16x128_f8f6f4 v[204:207], v[128:133], v[44:49], v[204:207] cbsz:2 blgp:2
	v_mfma_f32_16x16x128_f8f6f4 v[138:141], v[128:133], v[20:25], v[138:141] cbsz:2 blgp:2
	v_mfma_f32_16x16x128_f8f6f4 v[208:211], v[128:133], v[56:61], v[208:211] cbsz:2 blgp:2
	v_mfma_f32_16x16x128_f8f6f4 v[142:145], v[128:133], v[32:37], v[142:145] cbsz:2 blgp:2
	v_mfma_f32_16x16x128_f8f6f4 v[212:215], v[128:133], v[68:73], v[212:215] cbsz:2 blgp:2
	v_cndmask_b32_e64 v158, v134, v204, s[4:5]
	v_cndmask_b32_e64 v159, v138, v208, s[4:5]
	v_fma_mix_f32 v158, v158, v1, v148 op_sel:[0,0,1] op_sel_hi:[0,0,1]
	v_fma_mix_f32 v159, v159, v99, v152 op_sel:[0,0,1] op_sel_hi:[0,0,1]
	v_exp_f32_e32 v158, v158
	v_exp_f32_e32 v159, v159
	v_fma_f32 v158, v158, v186, v186
	v_add_f32_e32 v159, 1.0, v159
	v_rcp_f32_e32 v158, v158
	v_rcp_f32_e32 v159, v159
	v_cndmask_b32_e64 v160, v142, v212, s[4:5]
	v_fma_mix_f32 v161, v158, v160, v156 op_sel:[0,0,1] op_sel_hi:[0,0,1]
	v_exp_f32_e32 v161, v161
	s_add_u32 s48, s48, s40
	v_add_f32_e32 v161, 1.0, v161
	v_rcp_f32_e32 v161, v161
	s_addc_u32 s49, s49, s41
	v_fma_f32 v162, v161, -2.0, 1.0
	v_sub_f32_e32 v163, v176, v162
	v_fma_f32 v176, v159, v163, v162
	v_fma_f32 v164, |v176|, s16, v117
	v_fma_f32 v165, |v176|, s17, v118
	v_fma_f32 v166, |v176|, s18, v119
	v_lshrrev_b32_e32 v167, 26, v176
	v_min3_u32 v164, v164, v165, v166
	v_bfi_b32 v168, 31, v164, v167
	s_nop 1
	v_mul_u32_u24_dpp v170, v168, v180 quad_perm:[1,2,3,3] row_mask:0xf bank_mask:0xf bound_ctrl:1
	v_mad_u32_u24 v171, v168, v181, v170
	ds_write_b8_d16_hi v184, v171
	s_barrier
	global_store_short_d16_hi v185, v176, s[48:49]
	s_waitcnt lgkmcnt(0)
	s_barrier
	ds_read_b128 v[122:125], v192 offset:0
	ds_read_b64 v[126:127], v192 offset:16
	ds_read_b128 v[128:131], v192 offset:128
	ds_read_b64 v[132:133], v192 offset:144
	s_waitcnt lgkmcnt(2)
	v_mfma_f32_16x16x128_f8f6f4 v[134:137], v[122:127], v[2:7], 0 cbsz:2 blgp:2
	v_mfma_f32_16x16x128_f8f6f4 v[138:141], v[122:127], v[14:19], 0 cbsz:2 blgp:2
	v_mfma_f32_16x16x128_f8f6f4 v[142:145], v[122:127], v[26:31], v[188:191] cbsz:2 blgp:2
	v_mfma_f32_16x16x128_f8f6f4 v[204:207], v[122:127], v[38:43], 0 cbsz:2 blgp:2
	v_mfma_f32_16x16x128_f8f6f4 v[208:211], v[122:127], v[50:55], 0 cbsz:2 blgp:2
	v_mfma_f32_16x16x128_f8f6f4 v[212:215], v[122:127], v[62:67], v[188:191] cbsz:2 blgp:2
	s_waitcnt lgkmcnt(0)
	v_mfma_f32_16x16x128_f8f6f4 v[134:137], v[128:133], v[8:13], v[134:137] cbsz:2 blgp:2
	v_mfma_f32_16x16x128_f8f6f4 v[204:207], v[128:133], v[44:49], v[204:207] cbsz:2 blgp:2
	v_mfma_f32_16x16x128_f8f6f4 v[138:141], v[128:133], v[20:25], v[138:141] cbsz:2 blgp:2
	v_mfma_f32_16x16x128_f8f6f4 v[208:211], v[128:133], v[56:61], v[208:211] cbsz:2 blgp:2
	v_mfma_f32_16x16x128_f8f6f4 v[142:145], v[128:133], v[32:37], v[142:145] cbsz:2 blgp:2
	v_mfma_f32_16x16x128_f8f6f4 v[212:215], v[128:133], v[68:73], v[212:215] cbsz:2 blgp:2
	v_cndmask_b32_e64 v158, v134, v204, s[4:5]
	v_cndmask_b32_e64 v159, v138, v208, s[4:5]
	v_fma_mix_f32 v158, v158, v1, v149 op_sel_hi:[0,0,1]
	v_fma_mix_f32 v159, v159, v99, v153 op_sel_hi:[0,0,1]
	v_exp_f32_e32 v158, v158
	v_exp_f32_e32 v159, v159
	v_fma_f32 v158, v158, v186, v186
	v_add_f32_e32 v159, 1.0, v159
	v_rcp_f32_e32 v158, v158
	v_rcp_f32_e32 v159, v159
	v_cndmask_b32_e64 v160, v142, v212, s[4:5]
	v_fma_mix_f32 v161, v158, v160, v157 op_sel_hi:[0,0,1]
	v_exp_f32_e32 v161, v161
	s_add_u32 s48, s48, s40
	v_add_f32_e32 v161, 1.0, v161
	v_rcp_f32_e32 v161, v161
	s_addc_u32 s49, s49, s41
	v_fma_f32 v162, v161, -2.0, 1.0
	v_sub_f32_e32 v163, v176, v162
	v_fma_f32 v176, v159, v163, v162
	v_fma_f32 v164, |v176|, s16, v117
	v_fma_f32 v165, |v176|, s17, v118
	v_fma_f32 v166, |v176|, s18, v119
	v_lshrrev_b32_e32 v167, 26, v176
	v_min3_u32 v164, v164, v165, v166
	v_bfi_b32 v168, 31, v164, v167
	s_nop 1
	v_mul_u32_u24_dpp v170, v168, v180 quad_perm:[1,2,3,3] row_mask:0xf bank_mask:0xf bound_ctrl:1
	v_mad_u32_u24 v171, v168, v181, v170
	ds_write_b8_d16_hi v184, v171 offset:544
	s_barrier
	global_store_short_d16_hi v185, v176, s[48:49]
	s_waitcnt lgkmcnt(0)
	s_barrier
	ds_read_b128 v[122:125], v192 offset:544
	ds_read_b64 v[126:127], v192 offset:560
	ds_read_b128 v[128:131], v192 offset:672
	ds_read_b64 v[132:133], v192 offset:688
	s_add_i32 s44, s44, 16
	s_waitcnt lgkmcnt(2)
	v_mfma_f32_16x16x128_f8f6f4 v[134:137], v[122:127], v[2:7], 0 cbsz:2 blgp:2
	v_mfma_f32_16x16x128_f8f6f4 v[138:141], v[122:127], v[14:19], 0 cbsz:2 blgp:2
	v_mfma_f32_16x16x128_f8f6f4 v[142:145], v[122:127], v[26:31], v[188:191] cbsz:2 blgp:2
	v_mfma_f32_16x16x128_f8f6f4 v[204:207], v[122:127], v[38:43], 0 cbsz:2 blgp:2
	v_mfma_f32_16x16x128_f8f6f4 v[208:211], v[122:127], v[50:55], 0 cbsz:2 blgp:2
	v_mfma_f32_16x16x128_f8f6f4 v[212:215], v[122:127], v[62:67], v[188:191] cbsz:2 blgp:2
	s_waitcnt lgkmcnt(0)
	v_mfma_f32_16x16x128_f8f6f4 v[134:137], v[128:133], v[8:13], v[134:137] cbsz:2 blgp:2
	v_mfma_f32_16x16x128_f8f6f4 v[204:207], v[128:133], v[44:49], v[204:207] cbsz:2 blgp:2
	v_mfma_f32_16x16x128_f8f6f4 v[138:141], v[128:133], v[20:25], v[138:141] cbsz:2 blgp:2
	v_mfma_f32_16x16x128_f8f6f4 v[208:211], v[128:133], v[56:61], v[208:211] cbsz:2 blgp:2
	v_mfma_f32_16x16x128_f8f6f4 v[142:145], v[128:133], v[32:37], v[142:145] cbsz:2 blgp:2
	v_mfma_f32_16x16x128_f8f6f4 v[212:215], v[128:133], v[68:73], v[212:215] cbsz:2 blgp:2
	v_cndmask_b32_e64 v158, v134, v204, s[4:5]
	v_cndmask_b32_e64 v159, v138, v208, s[4:5]
	v_fma_mix_f32 v158, v158, v1, v149 op_sel:[0,0,1] op_sel_hi:[0,0,1]
	v_fma_mix_f32 v159, v159, v99, v153 op_sel:[0,0,1] op_sel_hi:[0,0,1]
	v_exp_f32_e32 v158, v158
	v_exp_f32_e32 v159, v159
	v_fma_f32 v158, v158, v186, v186
	v_add_f32_e32 v159, 1.0, v159
	v_rcp_f32_e32 v158, v158
	v_rcp_f32_e32 v159, v159
	v_cndmask_b32_e64 v160, v142, v212, s[4:5]
	v_fma_mix_f32 v161, v158, v160, v157 op_sel:[0,0,1] op_sel_hi:[0,0,1]
	v_exp_f32_e32 v161, v161
	s_add_u32 s48, s48, s40
	v_add_f32_e32 v161, 1.0, v161
	v_rcp_f32_e32 v161, v161
	s_addc_u32 s49, s49, s41
	v_fma_f32 v162, v161, -2.0, 1.0
	v_sub_f32_e32 v163, v176, v162
	v_fma_f32 v176, v159, v163, v162
	v_fma_f32 v164, |v176|, s16, v117
	v_fma_f32 v165, |v176|, s17, v118
	v_fma_f32 v166, |v176|, s18, v119
	v_lshrrev_b32_e32 v167, 26, v176
	v_min3_u32 v164, v164, v165, v166
	v_bfi_b32 v168, 31, v164, v167
	s_nop 1
	v_mul_u32_u24_dpp v170, v168, v180 quad_perm:[1,2,3,3] row_mask:0xf bank_mask:0xf bound_ctrl:1
	v_mad_u32_u24 v171, v168, v181, v170
	ds_write_b8_d16_hi v184, v171
	s_barrier
	global_store_short_d16_hi v185, v176, s[48:49]
	s_cmp_lt_i32 s44, s45
	s_cbranch_scc1 .Lscan_loop_b_st
	s_waitcnt lgkmcnt(0)
	s_barrier

	.amdhsa_kernel _Z12stage_kerneliiiiiiPKfS0_S0_PKtS0_PjPKhS0_S0_S0_PtPfS3_
		.amdhsa_group_segment_fixed_size 29184
		.amdhsa_private_segment_fixed_size 0
		.amdhsa_kernarg_size 384
		.amdhsa_user_sgpr_count 2
		.amdhsa_user_sgpr_dispatch_ptr 0
		.amdhsa_user_sgpr_queue_ptr 0
		.amdhsa_user_sgpr_kernarg_segment_ptr 1
		.amdhsa_user_sgpr_dispatch_id 0
		.amdhsa_user_sgpr_kernarg_preload_length 0
		.amdhsa_user_sgpr_kernarg_preload_offset 0
		.amdhsa_user_sgpr_private_segment_size 0
		.amdhsa_uses_dynamic_stack 0
		.amdhsa_enable_private_segment 0
		.amdhsa_system_sgpr_workgroup_id_x 1
		.amdhsa_system_sgpr_workgroup_id_y 0
		.amdhsa_system_sgpr_workgroup_id_z 0
		.amdhsa_system_sgpr_workgroup_info 0
		.amdhsa_system_vgpr_workitem_id 0
		.amdhsa_next_free_vgpr 228
		.amdhsa_next_free_sgpr 54
		.amdhsa_accum_offset 228
		.amdhsa_reserve_vcc 1
		.amdhsa_float_round_mode_32 0
		.amdhsa_float_round_mode_16_64 0
		.amdhsa_float_denorm_mode_32 3
		.amdhsa_float_denorm_mode_16_64 3
		.amdhsa_dx10_clamp 1
		.amdhsa_ieee_mode 1
		.amdhsa_fp16_overflow 0
		.amdhsa_tg_split 0
		.amdhsa_exception_fp_ieee_invalid_op 0
		.amdhsa_exception_fp_denorm_src 0
		.amdhsa_exception_fp_ieee_div_zero 0
		.amdhsa_exception_fp_ieee_overflow 0
		.amdhsa_exception_fp_ieee_underflow 0
		.amdhsa_exception_fp_ieee_inexact 0
		.amdhsa_exception_int_div_zero 0
	.end_amdhsa_kernel

.LBB2_12:
	s_or_b64 exec, exec, s[0:1]
	v_and_b32_e32 v97, 1, v74
	v_mov_b32_e32 v74, s8
	v_mov_b32_e32 v75, s9
	v_lshl_or_b32 v76, s2, 9, v0
	v_mov_b32_e32 v77, v87
	v_lshl_add_u64 v[74:75], v[76:77], 2, v[74:75]
	s_waitcnt lgkmcnt(0)
	s_barrier
	global_load_dword v118, v[74:75], off
	v_and_b32_e32 v74, 4, v90
	v_mov_b32_e32 v75, 0xd0
	v_cmp_ne_u32_e32 vcc, 0, v74
	v_and_b32_e32 v110, 3, v0
	v_cmp_gt_u32_e64 s[0:1], 12, v90
	v_cndmask_b32_e32 v74, 0, v75, vcc
	v_cmp_eq_u32_e32 vcc, 0, v110
	s_and_b64 s[4:5], vcc, s[0:1]
	s_lshl_b32 s1, s2, 21
	v_add_u32_e32 v109, v74, v86
	s_mul_i32 s0, s2, 0x600000
	v_lshl_or_b32 v74, v89, 1, v88
	s_and_b32 s2, s1, 0x1e00000
	v_mul_u32_u24_e32 v74, 0x60, v74
	v_lshlrev_b32_e32 v75, 1, v90
	s_add_u32 s0, s14, s0
	s_addc_u32 s1, s15, 0
	v_or3_b32 v86, v74, v75, v97
	v_lshl_add_u64 v[98:99], v[86:87], 4, s[0:1]
	s_mov_b64 s[0:1], 0x5a0000
	v_lshl_add_u64 v[100:101], v[98:99], 0, s[0:1]
	s_mov_b32 s0, 0x5a0000
	v_add_co_u32_e32 v102, vcc, s0, v98
	s_waitcnt vmcnt(4)
	v_mul_f32_e32 v86, 0xbfb8aa3b, v95
	v_addc_co_u32_e32 v103, vcc, 0, v99, vcc
	global_load_dwordx4 v[82:85], v[102:103], off
	global_load_dwordx4 v[74:77], v[100:101], off offset:512
	global_load_dwordx4 v[78:81], v[100:101], off offset:1024
	v_mul_f32_e32 v100, 0x3c91a2b4, v86
	s_waitcnt vmcnt(6)
	v_mul_f32_e32 v86, 0xbfb8aa3b, v94
	v_mul_f32_e32 v101, 0x3c91a2b4, v86
	s_waitcnt vmcnt(5)
	v_mul_f32_e32 v86, 0x4038aa3b, v93
	v_and_b32_e32 v0, 12, v0
	v_mul_f32_e32 v102, 0x3c91a2b4, v86
	v_lshrrev_b32_e32 v86, 2, v90
	v_mul_u32_u24_e32 v90, 0xd0, v97
	v_mad_u32_u24 v0, v89, 24, v0
	v_mul_u32_u24_e32 v88, 12, v88
	v_add3_u32 v93, v0, v90, v88
	v_or_b32_e32 v0, s2, v1
	v_lshlrev_b32_e32 v104, 3, v86
	v_lshlrev_b32_e32 v89, 20, v97
	v_lshl_add_u32 v0, s22, 8, v0
	v_sub_u32_e32 v86, 0, v104
	v_or3_b32 v0, v0, v89, v92
	v_and_b32_e32 v111, 24, v86
	v_lshlrev_b32_e32 v86, 1, v0
	s_mov_b64 s[6:7], 0x5a6000
	v_lshl_add_u64 v[0:1], s[12:13], 0, v[86:87]
	v_lshl_add_u64 v[86:87], v[98:99], 0, s[6:7]
	s_mov_b64 s[6:7], 0x5a6200
	v_lshl_add_u64 v[88:89], v[98:99], 0, s[6:7]
	s_mov_b64 s[6:7], 0x5a6400
	v_cmp_lt_u32_e64 s[0:1], 1, v91
	s_waitcnt vmcnt(4)
	v_mul_f32_e32 v103, 0x4038aa3b, v96
	s_mov_b32 s3, 0
	v_or_b32_e32 v105, 0x1c400, v109
	v_add_u32_e32 v106, 0x1c410, v109
	v_add_u32_e32 v107, 0x1c470, v109
	v_add_u32_e32 v108, 0x1c5b0, v109
	v_add_u32_e32 v109, 0x1c610, v109
	v_mul_u32_u24_e32 v110, 6, v110
	v_lshl_add_u64 v[90:91], v[98:99], 0, s[6:7]
	s_movk_i32 s22, 0x780
	s_movk_i32 s14, 0x7f
	s_movk_i32 s15, 0xf0
	v_mov_b32_e32 v112, 0x7f7f7f7f
	s_mov_b32 s17, 0x42700000
	s_mov_b32 s18, 0x41f00000
	s_mov_b32 s19, 0x41700000
	s_mov_b64 s[6:7], 0x12000
	s_mov_b64 s[8:9], 0x12200
	s_mov_b64 s[10:11], 0x12400
	v_mov_b32_e32 v113, 0x4b400000
	v_mov_b32_e32 v114, 0x4b400008
	v_mov_b32_e32 v115, 0x4b400010
	v_add_u32_e32 v116, 0x1c5a0, v93
	v_add_u32_e32 v117, 0x1c400, v93
	v_mbcnt_lo_u32_b32 v200, -1, 0
	v_mbcnt_hi_u32_b32 v200, -1, v200
	v_and_b32_e32 v201, 3, v200
	v_and_b32_e32 v202, 15, v200
	v_cmp_gt_u32_e32 vcc, 8, v202
	s_nop 1
	v_cndmask_b32_e64 v178, 0, v112, vcc
	v_cndmask_b32_e64 v179, v112, 0, vcc
	v_lshlrev_b32_e32 v181, 1, v201
	v_sub_u32_e32 v202, 22, v181
	v_lshlrev_b32_e64 v180, v202, 1
	v_sub_u32_e32 v202, 16, v181
	v_lshlrev_b32_e64 v181, v202, 1
	v_readfirstlane_b32 s51, v117
	v_lshrrev_b32_e32 v202, 4, v200
	v_lshlrev_b32_e32 v192, 5, v202
	v_bfe_u32 v202, v200, 2, 1
	v_mul_u32_u24_e32 v202, 0x110, v202
	v_add_u32_e32 v192, v192, v202
	v_add_u32_e32 v192, 0x1c400, v192
	s_sub_u32 s51, s51, 0x1c400
	s_mul_i32 s46, s51, 0xaaab
	s_lshr_b32 s46, s46, 15
	v_bfe_u32 v202, v200, 4, 1
	v_mul_u32_u24_e32 v184, 0x110, v202
	v_lshrrev_b32_e32 v202, 5, v200
	v_mul_u32_u24_e32 v202, 12, v202
	v_add_u32_e32 v184, v184, v202
	v_bfe_u32 v202, v200, 2, 2
	v_mul_u32_u24_e32 v164, 3, v202
	v_add3_u32 v184, v184, v164, v201
	v_add_u32_e32 v184, s46, v184
	v_add_u32_e32 v202, 0x1c500, v202
	v_add_u32_e32 v184, 0x1c400, v184
	v_cmp_eq_u32_e32 vcc, 3, v201
	s_nop 1
	v_cndmask_b32_e32 v184, v184, v202, vcc
	v_subrev_u32_e32 v185, s12, v0
	s_movk_i32 s44, 0x780
	s_movk_i32 s45, 0x800
	s_lshr_b32 s46, s44, 3
	s_add_i32 s46, s46, 1
	s_mul_i32 s46, s46, 0x6000
	s_mov_b32 s47, 0
	v_lshl_add_u64 v[196:197], v[98:99], 0, s[46:47]
	s_mov_b32 s42, 0x6000
	s_mov_b32 s43, 0
	s_sub_i32 s46, s44, 1
	s_sub_i32 s47, 0x800, s44
	s_and_b64 s[40:41], s[20:21], exec
	s_cselect_b32 s46, s46, s47
	s_cselect_b32 s41, 0, -1
	s_xor_b32 s40, s41, 0x400
	s_sub_i32 s40, s40, s41
	s_ashr_i32 s47, s46, 31
	s_lshl_b64 s[46:47], s[46:47], 10
	s_add_u32 s48, s12, s46
	s_addc_u32 s49, s13, s47
	s_waitcnt vmcnt(0) lgkmcnt(0)
	v_mov_b32_e32 v176, v118
	v_add_f32_e32 v169, -1.0, v118
	v_rcp_f32_e32 v186, v102
	s_nop 1
	v_mul_f32_e32 v188, v103, v186
	v_mov_b32_e32 v189, 0
	v_mov_b32_e32 v190, 0
	v_mov_b32_e32 v191, 0
	s_nop 1
	s_cmp_lt_i32 s44, s45
	s_cbranch_scc0 .Lscan_exit_f2
	ds_read_b128 v[122:125], v192
	ds_read_b64 v[126:127], v192 offset:16
	s_waitcnt lgkmcnt(0)
	s_cmp_lt_u32 s51, 96
	s_cbranch_scc0 .Lscan_entry_b_f2
	s_branch .Lscan_enter_a_f2
	.p2align 6

.Lscan_enter_a_f2:
	ds_read_b128 v[128:131], v192 offset:128
	ds_read_b64 v[132:133], v192 offset:144
	s_waitcnt vmcnt(8)
	global_load_dwordx4 v[146:149], v[196:197], off
	global_load_dwordx4 v[150:153], v[196:197], off offset:512
	global_load_dwordx4 v[154:157], v[196:197], off offset:1024
	v_lshl_add_u64 v[196:197], v[196:197], 0, s[42:43]
	s_waitcnt lgkmcnt(2)
	v_mfma_f32_16x16x128_f8f6f4 v[134:137], v[122:127], v[2:7], 0 cbsz:2 blgp:2
	v_mfma_f32_16x16x128_f8f6f4 v[138:141], v[122:127], v[14:19], 0 cbsz:2 blgp:2
	v_mfma_f32_16x16x128_f8f6f4 v[142:145], v[122:127], v[26:31], v[188:191] cbsz:2 blgp:2
	v_mfma_f32_16x16x128_f8f6f4 v[204:207], v[122:127], v[38:43], 0 cbsz:2 blgp:2
	v_mfma_f32_16x16x128_f8f6f4 v[208:211], v[122:127], v[50:55], 0 cbsz:2 blgp:2
	v_mfma_f32_16x16x128_f8f6f4 v[212:215], v[122:127], v[62:67], v[188:191] cbsz:2 blgp:2
	s_waitcnt lgkmcnt(0)
	v_mfma_f32_16x16x128_f8f6f4 v[134:137], v[128:133], v[8:13], v[134:137] cbsz:2 blgp:2
	v_mfma_f32_16x16x128_f8f6f4 v[204:207], v[128:133], v[44:49], v[204:207] cbsz:2 blgp:2
	v_mfma_f32_16x16x128_f8f6f4 v[138:141], v[128:133], v[20:25], v[138:141] cbsz:2 blgp:2
	v_mfma_f32_16x16x128_f8f6f4 v[208:211], v[128:133], v[56:61], v[208:211] cbsz:2 blgp:2
	v_mfma_f32_16x16x128_f8f6f4 v[142:145], v[128:133], v[32:37], v[142:145] cbsz:2 blgp:2
	v_mfma_f32_16x16x128_f8f6f4 v[212:215], v[128:133], v[68:73], v[212:215] cbsz:2 blgp:2
	v_cndmask_b32_e64 v158, v134, v204, s[0:1]
	v_cndmask_b32_e64 v159, v138, v208, s[0:1]
	v_fma_mix_f32 v158, v158, v100, v82 op_sel_hi:[0,0,1]
	v_fma_mix_f32 v159, v159, v101, v74 op_sel_hi:[0,0,1]
	v_exp_f32_e32 v158, v158
	v_exp_f32_e32 v159, v159
	v_fma_f32 v158, v158, v186, v186
	v_add_f32_e32 v159, 1.0, v159
	v_rcp_f32_e32 v158, v158
	v_rcp_f32_e32 v159, v159
	v_cndmask_b32_e64 v160, v142, v212, s[0:1]
	v_fma_mix_f32 v161, v158, v160, v78 op_sel_hi:[0,0,1]
	v_exp_f32_e32 v161, v161
	s_add_u32 s48, s48, s40
	v_add_f32_e32 v161, 1.0, v161
	v_rcp_f32_e32 v161, v161
	s_addc_u32 s49, s49, s41
	v_fma_f32 v162, v161, -2.0, 1.0
	v_sub_f32_e32 v163, v176, v162
	v_fma_f32 v176, v159, v163, v162
	v_fma_f32 v164, |v176|, s17, v113
	v_fma_f32 v165, |v176|, s18, v114
	v_fma_f32 v166, |v176|, s19, v115
	v_lshrrev_b32_e32 v167, 26, v176
	v_min3_u32 v164, v164, v165, v166
	v_bfi_b32 v168, 31, v164, v167
	s_nop 1
	v_mul_u32_u24_dpp v170, v168, v180 quad_perm:[1,2,3,3] row_mask:0xf bank_mask:0xf bound_ctrl:1
	v_mad_u32_u24 v171, v168, v181, v170
	ds_write_b8_d16_hi v184, v171 offset:544
	global_store_short_d16_hi v185, v176, s[48:49]
	s_waitcnt lgkmcnt(0)
	s_barrier
	ds_read_b128 v[122:125], v192 offset:544
	ds_read_b64 v[126:127], v192 offset:560
	s_barrier
	ds_read_b128 v[128:131], v192 offset:672
	ds_read_b64 v[132:133], v192 offset:688
	s_waitcnt lgkmcnt(2)
	v_mfma_f32_16x16x128_f8f6f4 v[134:137], v[122:127], v[2:7], 0 cbsz:2 blgp:2
	v_mfma_f32_16x16x128_f8f6f4 v[138:141], v[122:127], v[14:19], 0 cbsz:2 blgp:2
	v_mfma_f32_16x16x128_f8f6f4 v[142:145], v[122:127], v[26:31], v[188:191] cbsz:2 blgp:2
	v_mfma_f32_16x16x128_f8f6f4 v[204:207], v[122:127], v[38:43], 0 cbsz:2 blgp:2
	v_mfma_f32_16x16x128_f8f6f4 v[208:211], v[122:127], v[50:55], 0 cbsz:2 blgp:2
	v_mfma_f32_16x16x128_f8f6f4 v[212:215], v[122:127], v[62:67], v[188:191] cbsz:2 blgp:2
	s_waitcnt lgkmcnt(0)
	v_mfma_f32_16x16x128_f8f6f4 v[134:137], v[128:133], v[8:13], v[134:137] cbsz:2 blgp:2
	v_mfma_f32_16x16x128_f8f6f4 v[204:207], v[128:133], v[44:49], v[204:207] cbsz:2 blgp:2
	v_mfma_f32_16x16x128_f8f6f4 v[138:141], v[128:133], v[20:25], v[138:141] cbsz:2 blgp:2
	v_mfma_f32_16x16x128_f8f6f4 v[208:211], v[128:133], v[56:61], v[208:211] cbsz:2 blgp:2
	v_mfma_f32_16x16x128_f8f6f4 v[142:145], v[128:133], v[32:37], v[142:145] cbsz:2 blgp:2
	v_mfma_f32_16x16x128_f8f6f4 v[212:215], v[128:133], v[68:73], v[212:215] cbsz:2 blgp:2
	v_cndmask_b32_e64 v158, v134, v204, s[0:1]
	v_cndmask_b32_e64 v159, v138, v208, s[0:1]
	v_fma_mix_f32 v158, v158, v100, v82 op_sel:[0,0,1] op_sel_hi:[0,0,1]
	v_fma_mix_f32 v159, v159, v101, v74 op_sel:[0,0,1] op_sel_hi:[0,0,1]
	v_exp_f32_e32 v158, v158
	v_exp_f32_e32 v159, v159
	v_fma_f32 v158, v158, v186, v186
	v_add_f32_e32 v159, 1.0, v159
	v_rcp_f32_e32 v158, v158
	v_rcp_f32_e32 v159, v159
	v_cndmask_b32_e64 v160, v142, v212, s[0:1]
	v_fma_mix_f32 v161, v158, v160, v78 op_sel:[0,0,1] op_sel_hi:[0,0,1]
	v_exp_f32_e32 v161, v161
	s_add_u32 s48, s48, s40
	v_add_f32_e32 v161, 1.0, v161
	v_rcp_f32_e32 v161, v161
	s_addc_u32 s49, s49, s41
	v_fma_f32 v162, v161, -2.0, 1.0
	v_sub_f32_e32 v163, v176, v162
	v_fma_f32 v176, v159, v163, v162
	v_fma_f32 v164, |v176|, s17, v113
	v_fma_f32 v165, |v176|, s18, v114
	v_fma_f32 v166, |v176|, s19, v115
	v_lshrrev_b32_e32 v167, 26, v176
	v_min3_u32 v164, v164, v165, v166
	v_bfi_b32 v168, 31, v164, v167
	s_nop 1
	v_mul_u32_u24_dpp v170, v168, v180 quad_perm:[1,2,3,3] row_mask:0xf bank_mask:0xf bound_ctrl:1
	v_mad_u32_u24 v171, v168, v181, v170
	ds_write_b8_d16_hi v184, v171
	global_store_short_d16_hi v185, v176, s[48:49]
	s_waitcnt lgkmcnt(0)
	s_barrier
	ds_read_b128 v[122:125], v192 offset:0
	ds_read_b64 v[126:127], v192 offset:16
	s_barrier
	ds_read_b128 v[128:131], v192 offset:128
	ds_read_b64 v[132:133], v192 offset:144
	s_waitcnt lgkmcnt(2)
	v_mfma_f32_16x16x128_f8f6f4 v[134:137], v[122:127], v[2:7], 0 cbsz:2 blgp:2
	v_mfma_f32_16x16x128_f8f6f4 v[138:141], v[122:127], v[14:19], 0 cbsz:2 blgp:2
	v_mfma_f32_16x16x128_f8f6f4 v[142:145], v[122:127], v[26:31], v[188:191] cbsz:2 blgp:2
	v_mfma_f32_16x16x128_f8f6f4 v[204:207], v[122:127], v[38:43], 0 cbsz:2 blgp:2
	v_mfma_f32_16x16x128_f8f6f4 v[208:211], v[122:127], v[50:55], 0 cbsz:2 blgp:2
	v_mfma_f32_16x16x128_f8f6f4 v[212:215], v[122:127], v[62:67], v[188:191] cbsz:2 blgp:2
	s_waitcnt lgkmcnt(0)
	v_mfma_f32_16x16x128_f8f6f4 v[134:137], v[128:133], v[8:13], v[134:137] cbsz:2 blgp:2
	v_mfma_f32_16x16x128_f8f6f4 v[204:207], v[128:133], v[44:49], v[204:207] cbsz:2 blgp:2
	v_mfma_f32_16x16x128_f8f6f4 v[138:141], v[128:133], v[20:25], v[138:141] cbsz:2 blgp:2
	v_mfma_f32_16x16x128_f8f6f4 v[208:211], v[128:133], v[56:61], v[208:211] cbsz:2 blgp:2
	v_mfma_f32_16x16x128_f8f6f4 v[142:145], v[128:133], v[32:37], v[142:145] cbsz:2 blgp:2
	v_mfma_f32_16x16x128_f8f6f4 v[212:215], v[128:133], v[68:73], v[212:215] cbsz:2 blgp:2
	v_cndmask_b32_e64 v158, v134, v204, s[0:1]
	v_cndmask_b32_e64 v159, v138, v208, s[0:1]
	v_fma_mix_f32 v158, v158, v100, v83 op_sel_hi:[0,0,1]
	v_fma_mix_f32 v159, v159, v101, v75 op_sel_hi:[0,0,1]
	v_exp_f32_e32 v158, v158
	v_exp_f32_e32 v159, v159
	v_fma_f32 v158, v158, v186, v186
	v_add_f32_e32 v159, 1.0, v159
	v_rcp_f32_e32 v158, v158
	v_rcp_f32_e32 v159, v159
	v_cndmask_b32_e64 v160, v142, v212, s[0:1]
	v_fma_mix_f32 v161, v158, v160, v79 op_sel_hi:[0,0,1]
	v_exp_f32_e32 v161, v161
	s_add_u32 s48, s48, s40
	v_add_f32_e32 v161, 1.0, v161
	v_rcp_f32_e32 v161, v161
	s_addc_u32 s49, s49, s41
	v_fma_f32 v162, v161, -2.0, 1.0
	v_sub_f32_e32 v163, v176, v162
	v_fma_f32 v176, v159, v163, v162
	v_fma_f32 v164, |v176|, s17, v113
	v_fma_f32 v165, |v176|, s18, v114
	v_fma_f32 v166, |v176|, s19, v115
	v_lshrrev_b32_e32 v167, 26, v176
	v_min3_u32 v164, v164, v165, v166
	v_bfi_b32 v168, 31, v164, v167
	s_nop 1
	v_mul_u32_u24_dpp v170, v168, v180 quad_perm:[1,2,3,3] row_mask:0xf bank_mask:0xf bound_ctrl:1
	v_mad_u32_u24 v171, v168, v181, v170
	ds_write_b8_d16_hi v184, v171 offset:544
	global_store_short_d16_hi v185, v176, s[48:49]
	s_waitcnt lgkmcnt(0)
	s_barrier
	ds_read_b128 v[122:125], v192 offset:544
	ds_read_b64 v[126:127], v192 offset:560
	s_barrier
	ds_read_b128 v[128:131], v192 offset:672
	ds_read_b64 v[132:133], v192 offset:688
	s_waitcnt lgkmcnt(2)
	v_mfma_f32_16x16x128_f8f6f4 v[134:137], v[122:127], v[2:7], 0 cbsz:2 blgp:2
	v_mfma_f32_16x16x128_f8f6f4 v[138:141], v[122:127], v[14:19], 0 cbsz:2 blgp:2
	v_mfma_f32_16x16x128_f8f6f4 v[142:145], v[122:127], v[26:31], v[188:191] cbsz:2 blgp:2
	v_mfma_f32_16x16x128_f8f6f4 v[204:207], v[122:127], v[38:43], 0 cbsz:2 blgp:2
	v_mfma_f32_16x16x128_f8f6f4 v[208:211], v[122:127], v[50:55], 0 cbsz:2 blgp:2
	v_mfma_f32_16x16x128_f8f6f4 v[212:215], v[122:127], v[62:67], v[188:191] cbsz:2 blgp:2
	s_waitcnt lgkmcnt(0)
	v_mfma_f32_16x16x128_f8f6f4 v[134:137], v[128:133], v[8:13], v[134:137] cbsz:2 blgp:2
	v_mfma_f32_16x16x128_f8f6f4 v[204:207], v[128:133], v[44:49], v[204:207] cbsz:2 blgp:2
	v_mfma_f32_16x16x128_f8f6f4 v[138:141], v[128:133], v[20:25], v[138:141] cbsz:2 blgp:2
	v_mfma_f32_16x16x128_f8f6f4 v[208:211], v[128:133], v[56:61], v[208:211] cbsz:2 blgp:2
	v_mfma_f32_16x16x128_f8f6f4 v[142:145], v[128:133], v[32:37], v[142:145] cbsz:2 blgp:2
	v_mfma_f32_16x16x128_f8f6f4 v[212:215], v[128:133], v[68:73], v[212:215] cbsz:2 blgp:2
	v_cndmask_b32_e64 v158, v134, v204, s[0:1]
	v_cndmask_b32_e64 v159, v138, v208, s[0:1]
	v_fma_mix_f32 v158, v158, v100, v83 op_sel:[0,0,1] op_sel_hi:[0,0,1]
	v_fma_mix_f32 v159, v159, v101, v75 op_sel:[0,0,1] op_sel_hi:[0,0,1]
	v_exp_f32_e32 v158, v158
	v_exp_f32_e32 v159, v159
	v_fma_f32 v158, v158, v186, v186
	v_add_f32_e32 v159, 1.0, v159
	v_rcp_f32_e32 v158, v158
	v_rcp_f32_e32 v159, v159
	v_cndmask_b32_e64 v160, v142, v212, s[0:1]
	v_fma_mix_f32 v161, v158, v160, v79 op_sel:[0,0,1] op_sel_hi:[0,0,1]
	v_exp_f32_e32 v161, v161
	s_add_u32 s48, s48, s40
	v_add_f32_e32 v161, 1.0, v161
	v_rcp_f32_e32 v161, v161
	s_addc_u32 s49, s49, s41
	v_fma_f32 v162, v161, -2.0, 1.0
	v_sub_f32_e32 v163, v176, v162
	v_fma_f32 v176, v159, v163, v162
	v_fma_f32 v164, |v176|, s17, v113
	v_fma_f32 v165, |v176|, s18, v114
	v_fma_f32 v166, |v176|, s19, v115
	v_lshrrev_b32_e32 v167, 26, v176
	v_min3_u32 v164, v164, v165, v166
	v_bfi_b32 v168, 31, v164, v167
	s_nop 1
	v_mul_u32_u24_dpp v170, v168, v180 quad_perm:[1,2,3,3] row_mask:0xf bank_mask:0xf bound_ctrl:1
	v_mad_u32_u24 v171, v168, v181, v170
	ds_write_b8_d16_hi v184, v171
	global_store_short_d16_hi v185, v176, s[48:49]
	s_waitcnt lgkmcnt(0)
	s_barrier
	ds_read_b128 v[122:125], v192 offset:0
	ds_read_b64 v[126:127], v192 offset:16
	s_barrier
	ds_read_b128 v[128:131], v192 offset:128
	ds_read_b64 v[132:133], v192 offset:144
	s_waitcnt lgkmcnt(2)
	v_mfma_f32_16x16x128_f8f6f4 v[134:137], v[122:127], v[2:7], 0 cbsz:2 blgp:2
	v_mfma_f32_16x16x128_f8f6f4 v[138:141], v[122:127], v[14:19], 0 cbsz:2 blgp:2
	v_mfma_f32_16x16x128_f8f6f4 v[142:145], v[122:127], v[26:31], v[188:191] cbsz:2 blgp:2
	v_mfma_f32_16x16x128_f8f6f4 v[204:207], v[122:127], v[38:43], 0 cbsz:2 blgp:2
	v_mfma_f32_16x16x128_f8f6f4 v[208:211], v[122:127], v[50:55], 0 cbsz:2 blgp:2
	v_mfma_f32_16x16x128_f8f6f4 v[212:215], v[122:127], v[62:67], v[188:191] cbsz:2 blgp:2
	s_waitcnt lgkmcnt(0)
	v_mfma_f32_16x16x128_f8f6f4 v[134:137], v[128:133], v[8:13], v[134:137] cbsz:2 blgp:2
	v_mfma_f32_16x16x128_f8f6f4 v[204:207], v[128:133], v[44:49], v[204:207] cbsz:2 blgp:2
	v_mfma_f32_16x16x128_f8f6f4 v[138:141], v[128:133], v[20:25], v[138:141] cbsz:2 blgp:2
	v_mfma_f32_16x16x128_f8f6f4 v[208:211], v[128:133], v[56:61], v[208:211] cbsz:2 blgp:2
	v_mfma_f32_16x16x128_f8f6f4 v[142:145], v[128:133], v[32:37], v[142:145] cbsz:2 blgp:2
	v_mfma_f32_16x16x128_f8f6f4 v[212:215], v[128:133], v[68:73], v[212:215] cbsz:2 blgp:2
	v_cndmask_b32_e64 v158, v134, v204, s[0:1]
	v_cndmask_b32_e64 v159, v138, v208, s[0:1]
	v_fma_mix_f32 v158, v158, v100, v84 op_sel_hi:[0,0,1]
	v_fma_mix_f32 v159, v159, v101, v76 op_sel_hi:[0,0,1]
	v_exp_f32_e32 v158, v158
	v_exp_f32_e32 v159, v159
	v_fma_f32 v158, v158, v186, v186
	v_add_f32_e32 v159, 1.0, v159
	v_rcp_f32_e32 v158, v158
	v_rcp_f32_e32 v159, v159
	v_cndmask_b32_e64 v160, v142, v212, s[0:1]
	v_fma_mix_f32 v161, v158, v160, v80 op_sel_hi:[0,0,1]
	v_exp_f32_e32 v161, v161
	s_add_u32 s48, s48, s40
	v_add_f32_e32 v161, 1.0, v161
	v_rcp_f32_e32 v161, v161
	s_addc_u32 s49, s49, s41
	v_fma_f32 v162, v161, -2.0, 1.0
	v_sub_f32_e32 v163, v176, v162
	v_fma_f32 v176, v159, v163, v162
	v_fma_f32 v164, |v176|, s17, v113
	v_fma_f32 v165, |v176|, s18, v114
	v_fma_f32 v166, |v176|, s19, v115
	v_lshrrev_b32_e32 v167, 26, v176
	v_min3_u32 v164, v164, v165, v166
	v_bfi_b32 v168, 31, v164, v167
	s_nop 1
	v_mul_u32_u24_dpp v170, v168, v180 quad_perm:[1,2,3,3] row_mask:0xf bank_mask:0xf bound_ctrl:1
	v_mad_u32_u24 v171, v168, v181, v170
	ds_write_b8_d16_hi v184, v171 offset:544
	global_store_short_d16_hi v185, v176, s[48:49]
	s_waitcnt lgkmcnt(0)
	s_barrier
	ds_read_b128 v[122:125], v192 offset:544
	ds_read_b64 v[126:127], v192 offset:560
	s_barrier
	ds_read_b128 v[128:131], v192 offset:672
	ds_read_b64 v[132:133], v192 offset:688
	s_waitcnt lgkmcnt(2)
	v_mfma_f32_16x16x128_f8f6f4 v[134:137], v[122:127], v[2:7], 0 cbsz:2 blgp:2
	v_mfma_f32_16x16x128_f8f6f4 v[138:141], v[122:127], v[14:19], 0 cbsz:2 blgp:2
	v_mfma_f32_16x16x128_f8f6f4 v[142:145], v[122:127], v[26:31], v[188:191] cbsz:2 blgp:2
	v_mfma_f32_16x16x128_f8f6f4 v[204:207], v[122:127], v[38:43], 0 cbsz:2 blgp:2
	v_mfma_f32_16x16x128_f8f6f4 v[208:211], v[122:127], v[50:55], 0 cbsz:2 blgp:2
	v_mfma_f32_16x16x128_f8f6f4 v[212:215], v[122:127], v[62:67], v[188:191] cbsz:2 blgp:2
	s_waitcnt lgkmcnt(0)
	v_mfma_f32_16x16x128_f8f6f4 v[134:137], v[128:133], v[8:13], v[134:137] cbsz:2 blgp:2
	v_mfma_f32_16x16x128_f8f6f4 v[204:207], v[128:133], v[44:49], v[204:207] cbsz:2 blgp:2
	v_mfma_f32_16x16x128_f8f6f4 v[138:141], v[128:133], v[20:25], v[138:141] cbsz:2 blgp:2
	v_mfma_f32_16x16x128_f8f6f4 v[208:211], v[128:133], v[56:61], v[208:211] cbsz:2 blgp:2
	v_mfma_f32_16x16x128_f8f6f4 v[142:145], v[128:133], v[32:37], v[142:145] cbsz:2 blgp:2
	v_mfma_f32_16x16x128_f8f6f4 v[212:215], v[128:133], v[68:73], v[212:215] cbsz:2 blgp:2
	v_cndmask_b32_e64 v158, v134, v204, s[0:1]
	v_cndmask_b32_e64 v159, v138, v208, s[0:1]
	v_fma_mix_f32 v158, v158, v100, v84 op_sel:[0,0,1] op_sel_hi:[0,0,1]
	v_fma_mix_f32 v159, v159, v101, v76 op_sel:[0,0,1] op_sel_hi:[0,0,1]
	v_exp_f32_e32 v158, v158
	v_exp_f32_e32 v159, v159
	v_fma_f32 v158, v158, v186, v186
	v_add_f32_e32 v159, 1.0, v159
	v_rcp_f32_e32 v158, v158
	v_rcp_f32_e32 v159, v159
	v_cndmask_b32_e64 v160, v142, v212, s[0:1]
	v_fma_mix_f32 v161, v158, v160, v80 op_sel:[0,0,1] op_sel_hi:[0,0,1]
	v_exp_f32_e32 v161, v161
	s_add_u32 s48, s48, s40
	v_add_f32_e32 v161, 1.0, v161
	v_rcp_f32_e32 v161, v161
	s_addc_u32 s49, s49, s41
	v_fma_f32 v162, v161, -2.0, 1.0
	v_sub_f32_e32 v163, v176, v162
	v_fma_f32 v176, v159, v163, v162
	v_fma_f32 v164, |v176|, s17, v113
	v_fma_f32 v165, |v176|, s18, v114
	v_fma_f32 v166, |v176|, s19, v115
	v_lshrrev_b32_e32 v167, 26, v176
	v_min3_u32 v164, v164, v165, v166
	v_bfi_b32 v168, 31, v164, v167
	s_nop 1
	v_mul_u32_u24_dpp v170, v168, v180 quad_perm:[1,2,3,3] row_mask:0xf bank_mask:0xf bound_ctrl:1
	v_mad_u32_u24 v171, v168, v181, v170
	ds_write_b8_d16_hi v184, v171
	global_store_short_d16_hi v185, v176, s[48:49]
	s_waitcnt lgkmcnt(0)
	s_barrier
	ds_read_b128 v[122:125], v192 offset:0
	ds_read_b64 v[126:127], v192 offset:16
	s_barrier
	ds_read_b128 v[128:131], v192 offset:128
	ds_read_b64 v[132:133], v192 offset:144
	s_waitcnt lgkmcnt(2)
	v_mfma_f32_16x16x128_f8f6f4 v[134:137], v[122:127], v[2:7], 0 cbsz:2 blgp:2
	v_mfma_f32_16x16x128_f8f6f4 v[138:141], v[122:127], v[14:19], 0 cbsz:2 blgp:2
	v_mfma_f32_16x16x128_f8f6f4 v[142:145], v[122:127], v[26:31], v[188:191] cbsz:2 blgp:2
	v_mfma_f32_16x16x128_f8f6f4 v[204:207], v[122:127], v[38:43], 0 cbsz:2 blgp:2
	v_mfma_f32_16x16x128_f8f6f4 v[208:211], v[122:127], v[50:55], 0 cbsz:2 blgp:2
	v_mfma_f32_16x16x128_f8f6f4 v[212:215], v[122:127], v[62:67], v[188:191] cbsz:2 blgp:2
	s_waitcnt lgkmcnt(0)
	v_mfma_f32_16x16x128_f8f6f4 v[134:137], v[128:133], v[8:13], v[134:137] cbsz:2 blgp:2
	v_mfma_f32_16x16x128_f8f6f4 v[204:207], v[128:133], v[44:49], v[204:207] cbsz:2 blgp:2
	v_mfma_f32_16x16x128_f8f6f4 v[138:141], v[128:133], v[20:25], v[138:141] cbsz:2 blgp:2
	v_mfma_f32_16x16x128_f8f6f4 v[208:211], v[128:133], v[56:61], v[208:211] cbsz:2 blgp:2
	v_mfma_f32_16x16x128_f8f6f4 v[142:145], v[128:133], v[32:37], v[142:145] cbsz:2 blgp:2
	v_mfma_f32_16x16x128_f8f6f4 v[212:215], v[128:133], v[68:73], v[212:215] cbsz:2 blgp:2
	v_cndmask_b32_e64 v158, v134, v204, s[0:1]
	v_cndmask_b32_e64 v159, v138, v208, s[0:1]
	v_fma_mix_f32 v158, v158, v100, v85 op_sel_hi:[0,0,1]
	v_fma_mix_f32 v159, v159, v101, v77 op_sel_hi:[0,0,1]
	v_exp_f32_e32 v158, v158
	v_exp_f32_e32 v159, v159
	v_fma_f32 v158, v158, v186, v186
	v_add_f32_e32 v159, 1.0, v159
	v_rcp_f32_e32 v158, v158
	v_rcp_f32_e32 v159, v159
	v_cndmask_b32_e64 v160, v142, v212, s[0:1]
	v_fma_mix_f32 v161, v158, v160, v81 op_sel_hi:[0,0,1]
	v_exp_f32_e32 v161, v161
	s_add_u32 s48, s48, s40
	v_add_f32_e32 v161, 1.0, v161
	v_rcp_f32_e32 v161, v161
	s_addc_u32 s49, s49, s41
	v_fma_f32 v162, v161, -2.0, 1.0
	v_sub_f32_e32 v163, v176, v162
	v_fma_f32 v176, v159, v163, v162
	v_fma_f32 v164, |v176|, s17, v113
	v_fma_f32 v165, |v176|, s18, v114
	v_fma_f32 v166, |v176|, s19, v115
	v_lshrrev_b32_e32 v167, 26, v176
	v_min3_u32 v164, v164, v165, v166
	v_bfi_b32 v168, 31, v164, v167
	s_nop 1
	v_mul_u32_u24_dpp v170, v168, v180 quad_perm:[1,2,3,3] row_mask:0xf bank_mask:0xf bound_ctrl:1
	v_mad_u32_u24 v171, v168, v181, v170
	ds_write_b8_d16_hi v184, v171 offset:544
	global_store_short_d16_hi v185, v176, s[48:49]
	s_waitcnt lgkmcnt(0)
	s_barrier
	ds_read_b128 v[122:125], v192 offset:544
	ds_read_b64 v[126:127], v192 offset:560
	s_barrier
	ds_read_b128 v[128:131], v192 offset:672
	ds_read_b64 v[132:133], v192 offset:688
	s_waitcnt lgkmcnt(2)
	v_mfma_f32_16x16x128_f8f6f4 v[134:137], v[122:127], v[2:7], 0 cbsz:2 blgp:2
	v_mfma_f32_16x16x128_f8f6f4 v[138:141], v[122:127], v[14:19], 0 cbsz:2 blgp:2
	v_mfma_f32_16x16x128_f8f6f4 v[142:145], v[122:127], v[26:31], v[188:191] cbsz:2 blgp:2
	v_mfma_f32_16x16x128_f8f6f4 v[204:207], v[122:127], v[38:43], 0 cbsz:2 blgp:2
	v_mfma_f32_16x16x128_f8f6f4 v[208:211], v[122:127], v[50:55], 0 cbsz:2 blgp:2
	v_mfma_f32_16x16x128_f8f6f4 v[212:215], v[122:127], v[62:67], v[188:191] cbsz:2 blgp:2
	s_waitcnt lgkmcnt(0)
	v_mfma_f32_16x16x128_f8f6f4 v[134:137], v[128:133], v[8:13], v[134:137] cbsz:2 blgp:2
	v_mfma_f32_16x16x128_f8f6f4 v[204:207], v[128:133], v[44:49], v[204:207] cbsz:2 blgp:2
	v_mfma_f32_16x16x128_f8f6f4 v[138:141], v[128:133], v[20:25], v[138:141] cbsz:2 blgp:2
	v_mfma_f32_16x16x128_f8f6f4 v[208:211], v[128:133], v[56:61], v[208:211] cbsz:2 blgp:2
	v_mfma_f32_16x16x128_f8f6f4 v[142:145], v[128:133], v[32:37], v[142:145] cbsz:2 blgp:2
	v_mfma_f32_16x16x128_f8f6f4 v[212:215], v[128:133], v[68:73], v[212:215] cbsz:2 blgp:2
	v_cndmask_b32_e64 v158, v134, v204, s[0:1]
	v_cndmask_b32_e64 v159, v138, v208, s[0:1]
	v_fma_mix_f32 v158, v158, v100, v85 op_sel:[0,0,1] op_sel_hi:[0,0,1]
	v_fma_mix_f32 v159, v159, v101, v77 op_sel:[0,0,1] op_sel_hi:[0,0,1]
	v_exp_f32_e32 v158, v158
	v_exp_f32_e32 v159, v159
	v_fma_f32 v158, v158, v186, v186
	v_add_f32_e32 v159, 1.0, v159
	v_rcp_f32_e32 v158, v158
	v_rcp_f32_e32 v159, v159
	v_cndmask_b32_e64 v160, v142, v212, s[0:1]
	v_fma_mix_f32 v161, v158, v160, v81 op_sel:[0,0,1] op_sel_hi:[0,0,1]
	v_exp_f32_e32 v161, v161
	s_add_u32 s48, s48, s40
	v_add_f32_e32 v161, 1.0, v161
	v_rcp_f32_e32 v161, v161
	s_addc_u32 s49, s49, s41
	v_fma_f32 v162, v161, -2.0, 1.0
	v_sub_f32_e32 v163, v176, v162
	v_fma_f32 v176, v159, v163, v162
	v_fma_f32 v164, |v176|, s17, v113
	v_fma_f32 v165, |v176|, s18, v114
	v_fma_f32 v166, |v176|, s19, v115
	v_lshrrev_b32_e32 v167, 26, v176
	v_min3_u32 v164, v164, v165, v166
	v_bfi_b32 v168, 31, v164, v167
	s_nop 1
	v_mul_u32_u24_dpp v170, v168, v180 quad_perm:[1,2,3,3] row_mask:0xf bank_mask:0xf bound_ctrl:1
	v_mad_u32_u24 v171, v168, v181, v170
	ds_write_b8_d16_hi v184, v171
	global_store_short_d16_hi v185, v176, s[48:49]
	s_waitcnt lgkmcnt(0)
	s_barrier
	ds_read_b128 v[122:125], v192 offset:0
	ds_read_b64 v[126:127], v192 offset:16
	s_barrier
	ds_read_b128 v[128:131], v192 offset:128
	ds_read_b64 v[132:133], v192 offset:144
	s_waitcnt vmcnt(8)
	global_load_dwordx4 v[82:85], v[196:197], off
	global_load_dwordx4 v[74:77], v[196:197], off offset:512
	global_load_dwordx4 v[78:81], v[196:197], off offset:1024
	v_lshl_add_u64 v[196:197], v[196:197], 0, s[42:43]
	s_waitcnt lgkmcnt(2)
	v_mfma_f32_16x16x128_f8f6f4 v[134:137], v[122:127], v[2:7], 0 cbsz:2 blgp:2
	v_mfma_f32_16x16x128_f8f6f4 v[138:141], v[122:127], v[14:19], 0 cbsz:2 blgp:2
	v_mfma_f32_16x16x128_f8f6f4 v[142:145], v[122:127], v[26:31], v[188:191] cbsz:2 blgp:2
	v_mfma_f32_16x16x128_f8f6f4 v[204:207], v[122:127], v[38:43], 0 cbsz:2 blgp:2
	v_mfma_f32_16x16x128_f8f6f4 v[208:211], v[122:127], v[50:55], 0 cbsz:2 blgp:2
	v_mfma_f32_16x16x128_f8f6f4 v[212:215], v[122:127], v[62:67], v[188:191] cbsz:2 blgp:2
	s_waitcnt lgkmcnt(0)
	v_mfma_f32_16x16x128_f8f6f4 v[134:137], v[128:133], v[8:13], v[134:137] cbsz:2 blgp:2
	v_mfma_f32_16x16x128_f8f6f4 v[204:207], v[128:133], v[44:49], v[204:207] cbsz:2 blgp:2
	v_mfma_f32_16x16x128_f8f6f4 v[138:141], v[128:133], v[20:25], v[138:141] cbsz:2 blgp:2
	v_mfma_f32_16x16x128_f8f6f4 v[208:211], v[128:133], v[56:61], v[208:211] cbsz:2 blgp:2
	v_mfma_f32_16x16x128_f8f6f4 v[142:145], v[128:133], v[32:37], v[142:145] cbsz:2 blgp:2
	v_mfma_f32_16x16x128_f8f6f4 v[212:215], v[128:133], v[68:73], v[212:215] cbsz:2 blgp:2
	v_cndmask_b32_e64 v158, v134, v204, s[0:1]
	v_cndmask_b32_e64 v159, v138, v208, s[0:1]
	v_fma_mix_f32 v158, v158, v100, v146 op_sel_hi:[0,0,1]
	v_fma_mix_f32 v159, v159, v101, v150 op_sel_hi:[0,0,1]
	v_exp_f32_e32 v158, v158
	v_exp_f32_e32 v159, v159
	v_fma_f32 v158, v158, v186, v186
	v_add_f32_e32 v159, 1.0, v159
	v_rcp_f32_e32 v158, v158
	v_rcp_f32_e32 v159, v159
	v_cndmask_b32_e64 v160, v142, v212, s[0:1]
	v_fma_mix_f32 v161, v158, v160, v154 op_sel_hi:[0,0,1]
	v_exp_f32_e32 v161, v161
	s_add_u32 s48, s48, s40
	v_add_f32_e32 v161, 1.0, v161
	v_rcp_f32_e32 v161, v161
	s_addc_u32 s49, s49, s41
	v_fma_f32 v162, v161, -2.0, 1.0
	v_sub_f32_e32 v163, v176, v162
	v_fma_f32 v176, v159, v163, v162
	v_fma_f32 v164, |v176|, s17, v113
	v_fma_f32 v165, |v176|, s18, v114
	v_fma_f32 v166, |v176|, s19, v115
	v_lshrrev_b32_e32 v167, 26, v176
	v_min3_u32 v164, v164, v165, v166
	v_bfi_b32 v168, 31, v164, v167
	s_nop 1
	v_mul_u32_u24_dpp v170, v168, v180 quad_perm:[1,2,3,3] row_mask:0xf bank_mask:0xf bound_ctrl:1
	v_mad_u32_u24 v171, v168, v181, v170
	ds_write_b8_d16_hi v184, v171 offset:544
	global_store_short_d16_hi v185, v176, s[48:49]
	s_waitcnt lgkmcnt(0)
	s_barrier
	ds_read_b128 v[122:125], v192 offset:544
	ds_read_b64 v[126:127], v192 offset:560
	s_barrier
	ds_read_b128 v[128:131], v192 offset:672
	ds_read_b64 v[132:133], v192 offset:688
	s_waitcnt lgkmcnt(2)
	v_mfma_f32_16x16x128_f8f6f4 v[134:137], v[122:127], v[2:7], 0 cbsz:2 blgp:2
	v_mfma_f32_16x16x128_f8f6f4 v[138:141], v[122:127], v[14:19], 0 cbsz:2 blgp:2
	v_mfma_f32_16x16x128_f8f6f4 v[142:145], v[122:127], v[26:31], v[188:191] cbsz:2 blgp:2
	v_mfma_f32_16x16x128_f8f6f4 v[204:207], v[122:127], v[38:43], 0 cbsz:2 blgp:2
	v_mfma_f32_16x16x128_f8f6f4 v[208:211], v[122:127], v[50:55], 0 cbsz:2 blgp:2
	v_mfma_f32_16x16x128_f8f6f4 v[212:215], v[122:127], v[62:67], v[188:191] cbsz:2 blgp:2
	s_waitcnt lgkmcnt(0)
	v_mfma_f32_16x16x128_f8f6f4 v[134:137], v[128:133], v[8:13], v[134:137] cbsz:2 blgp:2
	v_mfma_f32_16x16x128_f8f6f4 v[204:207], v[128:133], v[44:49], v[204:207] cbsz:2 blgp:2
	v_mfma_f32_16x16x128_f8f6f4 v[138:141], v[128:133], v[20:25], v[138:141] cbsz:2 blgp:2
	v_mfma_f32_16x16x128_f8f6f4 v[208:211], v[128:133], v[56:61], v[208:211] cbsz:2 blgp:2
	v_mfma_f32_16x16x128_f8f6f4 v[142:145], v[128:133], v[32:37], v[142:145] cbsz:2 blgp:2
	v_mfma_f32_16x16x128_f8f6f4 v[212:215], v[128:133], v[68:73], v[212:215] cbsz:2 blgp:2
	v_cndmask_b32_e64 v158, v134, v204, s[0:1]
	v_cndmask_b32_e64 v159, v138, v208, s[0:1]
	v_fma_mix_f32 v158, v158, v100, v146 op_sel:[0,0,1] op_sel_hi:[0,0,1]
	v_fma_mix_f32 v159, v159, v101, v150 op_sel:[0,0,1] op_sel_hi:[0,0,1]
	v_exp_f32_e32 v158, v158
	v_exp_f32_e32 v159, v159
	v_fma_f32 v158, v158, v186, v186
	v_add_f32_e32 v159, 1.0, v159
	v_rcp_f32_e32 v158, v158
	v_rcp_f32_e32 v159, v159
	v_cndmask_b32_e64 v160, v142, v212, s[0:1]
	v_fma_mix_f32 v161, v158, v160, v154 op_sel:[0,0,1] op_sel_hi:[0,0,1]
	v_exp_f32_e32 v161, v161
	s_add_u32 s48, s48, s40
	v_add_f32_e32 v161, 1.0, v161
	v_rcp_f32_e32 v161, v161
	s_addc_u32 s49, s49, s41
	v_fma_f32 v162, v161, -2.0, 1.0
	v_sub_f32_e32 v163, v176, v162
	v_fma_f32 v176, v159, v163, v162
	v_fma_f32 v164, |v176|, s17, v113
	v_fma_f32 v165, |v176|, s18, v114
	v_fma_f32 v166, |v176|, s19, v115
	v_lshrrev_b32_e32 v167, 26, v176
	v_min3_u32 v164, v164, v165, v166
	v_bfi_b32 v168, 31, v164, v167
	s_nop 1
	v_mul_u32_u24_dpp v170, v168, v180 quad_perm:[1,2,3,3] row_mask:0xf bank_mask:0xf bound_ctrl:1
	v_mad_u32_u24 v171, v168, v181, v170
	ds_write_b8_d16_hi v184, v171
	global_store_short_d16_hi v185, v176, s[48:49]
	s_waitcnt lgkmcnt(0)
	s_barrier
	ds_read_b128 v[122:125], v192 offset:0
	ds_read_b64 v[126:127], v192 offset:16
	s_barrier
	ds_read_b128 v[128:131], v192 offset:128
	ds_read_b64 v[132:133], v192 offset:144
	s_waitcnt lgkmcnt(2)
	v_mfma_f32_16x16x128_f8f6f4 v[134:137], v[122:127], v[2:7], 0 cbsz:2 blgp:2
	v_mfma_f32_16x16x128_f8f6f4 v[138:141], v[122:127], v[14:19], 0 cbsz:2 blgp:2
	v_mfma_f32_16x16x128_f8f6f4 v[142:145], v[122:127], v[26:31], v[188:191] cbsz:2 blgp:2
	v_mfma_f32_16x16x128_f8f6f4 v[204:207], v[122:127], v[38:43], 0 cbsz:2 blgp:2
	v_mfma_f32_16x16x128_f8f6f4 v[208:211], v[122:127], v[50:55], 0 cbsz:2 blgp:2
	v_mfma_f32_16x16x128_f8f6f4 v[212:215], v[122:127], v[62:67], v[188:191] cbsz:2 blgp:2
	s_waitcnt lgkmcnt(0)
	v_mfma_f32_16x16x128_f8f6f4 v[134:137], v[128:133], v[8:13], v[134:137] cbsz:2 blgp:2
	v_mfma_f32_16x16x128_f8f6f4 v[204:207], v[128:133], v[44:49], v[204:207] cbsz:2 blgp:2
	v_mfma_f32_16x16x128_f8f6f4 v[138:141], v[128:133], v[20:25], v[138:141] cbsz:2 blgp:2
	v_mfma_f32_16x16x128_f8f6f4 v[208:211], v[128:133], v[56:61], v[208:211] cbsz:2 blgp:2
	v_mfma_f32_16x16x128_f8f6f4 v[142:145], v[128:133], v[32:37], v[142:145] cbsz:2 blgp:2
	v_mfma_f32_16x16x128_f8f6f4 v[212:215], v[128:133], v[68:73], v[212:215] cbsz:2 blgp:2
	v_cndmask_b32_e64 v158, v134, v204, s[0:1]
	v_cndmask_b32_e64 v159, v138, v208, s[0:1]
	v_fma_mix_f32 v158, v158, v100, v147 op_sel_hi:[0,0,1]
	v_fma_mix_f32 v159, v159, v101, v151 op_sel_hi:[0,0,1]
	v_exp_f32_e32 v158, v158
	v_exp_f32_e32 v159, v159
	v_fma_f32 v158, v158, v186, v186
	v_add_f32_e32 v159, 1.0, v159
	v_rcp_f32_e32 v158, v158
	v_rcp_f32_e32 v159, v159
	v_cndmask_b32_e64 v160, v142, v212, s[0:1]
	v_fma_mix_f32 v161, v158, v160, v155 op_sel_hi:[0,0,1]
	v_exp_f32_e32 v161, v161
	s_add_u32 s48, s48, s40
	v_add_f32_e32 v161, 1.0, v161
	v_rcp_f32_e32 v161, v161
	s_addc_u32 s49, s49, s41
	v_fma_f32 v162, v161, -2.0, 1.0
	v_sub_f32_e32 v163, v176, v162
	v_fma_f32 v176, v159, v163, v162
	v_fma_f32 v164, |v176|, s17, v113
	v_fma_f32 v165, |v176|, s18, v114
	v_fma_f32 v166, |v176|, s19, v115
	v_lshrrev_b32_e32 v167, 26, v176
	v_min3_u32 v164, v164, v165, v166
	v_bfi_b32 v168, 31, v164, v167
	s_nop 1
	v_mul_u32_u24_dpp v170, v168, v180 quad_perm:[1,2,3,3] row_mask:0xf bank_mask:0xf bound_ctrl:1
	v_mad_u32_u24 v171, v168, v181, v170
	ds_write_b8_d16_hi v184, v171 offset:544
	global_store_short_d16_hi v185, v176, s[48:49]
	s_waitcnt lgkmcnt(0)
	s_barrier
	ds_read_b128 v[122:125], v192 offset:544
	ds_read_b64 v[126:127], v192 offset:560
	s_barrier
	ds_read_b128 v[128:131], v192 offset:672
	ds_read_b64 v[132:133], v192 offset:688
	s_waitcnt lgkmcnt(2)
	v_mfma_f32_16x16x128_f8f6f4 v[134:137], v[122:127], v[2:7], 0 cbsz:2 blgp:2
	v_mfma_f32_16x16x128_f8f6f4 v[138:141], v[122:127], v[14:19], 0 cbsz:2 blgp:2
	v_mfma_f32_16x16x128_f8f6f4 v[142:145], v[122:127], v[26:31], v[188:191] cbsz:2 blgp:2
	v_mfma_f32_16x16x128_f8f6f4 v[204:207], v[122:127], v[38:43], 0 cbsz:2 blgp:2
	v_mfma_f32_16x16x128_f8f6f4 v[208:211], v[122:127], v[50:55], 0 cbsz:2 blgp:2
	v_mfma_f32_16x16x128_f8f6f4 v[212:215], v[122:127], v[62:67], v[188:191] cbsz:2 blgp:2
	s_waitcnt lgkmcnt(0)
	v_mfma_f32_16x16x128_f8f6f4 v[134:137], v[128:133], v[8:13], v[134:137] cbsz:2 blgp:2
	v_mfma_f32_16x16x128_f8f6f4 v[204:207], v[128:133], v[44:49], v[204:207] cbsz:2 blgp:2
	v_mfma_f32_16x16x128_f8f6f4 v[138:141], v[128:133], v[20:25], v[138:141] cbsz:2 blgp:2
	v_mfma_f32_16x16x128_f8f6f4 v[208:211], v[128:133], v[56:61], v[208:211] cbsz:2 blgp:2
	v_mfma_f32_16x16x128_f8f6f4 v[142:145], v[128:133], v[32:37], v[142:145] cbsz:2 blgp:2
	v_mfma_f32_16x16x128_f8f6f4 v[212:215], v[128:133], v[68:73], v[212:215] cbsz:2 blgp:2
	v_cndmask_b32_e64 v158, v134, v204, s[0:1]
	v_cndmask_b32_e64 v159, v138, v208, s[0:1]
	v_fma_mix_f32 v158, v158, v100, v147 op_sel:[0,0,1] op_sel_hi:[0,0,1]
	v_fma_mix_f32 v159, v159, v101, v151 op_sel:[0,0,1] op_sel_hi:[0,0,1]
	v_exp_f32_e32 v158, v158
	v_exp_f32_e32 v159, v159
	v_fma_f32 v158, v158, v186, v186
	v_add_f32_e32 v159, 1.0, v159
	v_rcp_f32_e32 v158, v158
	v_rcp_f32_e32 v159, v159
	v_cndmask_b32_e64 v160, v142, v212, s[0:1]
	v_fma_mix_f32 v161, v158, v160, v155 op_sel:[0,0,1] op_sel_hi:[0,0,1]
	v_exp_f32_e32 v161, v161
	s_add_u32 s48, s48, s40
	v_add_f32_e32 v161, 1.0, v161
	v_rcp_f32_e32 v161, v161
	s_addc_u32 s49, s49, s41
	v_fma_f32 v162, v161, -2.0, 1.0
	v_sub_f32_e32 v163, v176, v162
	v_fma_f32 v176, v159, v163, v162
	v_fma_f32 v164, |v176|, s17, v113
	v_fma_f32 v165, |v176|, s18, v114
	v_fma_f32 v166, |v176|, s19, v115
	v_lshrrev_b32_e32 v167, 26, v176
	v_min3_u32 v164, v164, v165, v166
	v_bfi_b32 v168, 31, v164, v167
	s_nop 1
	v_mul_u32_u24_dpp v170, v168, v180 quad_perm:[1,2,3,3] row_mask:0xf bank_mask:0xf bound_ctrl:1
	v_mad_u32_u24 v171, v168, v181, v170
	ds_write_b8_d16_hi v184, v171
	global_store_short_d16_hi v185, v176, s[48:49]
	s_waitcnt lgkmcnt(0)
	s_barrier
	ds_read_b128 v[122:125], v192 offset:0
	ds_read_b64 v[126:127], v192 offset:16
	s_barrier
	ds_read_b128 v[128:131], v192 offset:128
	ds_read_b64 v[132:133], v192 offset:144
	s_waitcnt lgkmcnt(2)
	v_mfma_f32_16x16x128_f8f6f4 v[134:137], v[122:127], v[2:7], 0 cbsz:2 blgp:2
	v_mfma_f32_16x16x128_f8f6f4 v[138:141], v[122:127], v[14:19], 0 cbsz:2 blgp:2
	v_mfma_f32_16x16x128_f8f6f4 v[142:145], v[122:127], v[26:31], v[188:191] cbsz:2 blgp:2
	v_mfma_f32_16x16x128_f8f6f4 v[204:207], v[122:127], v[38:43], 0 cbsz:2 blgp:2
	v_mfma_f32_16x16x128_f8f6f4 v[208:211], v[122:127], v[50:55], 0 cbsz:2 blgp:2
	v_mfma_f32_16x16x128_f8f6f4 v[212:215], v[122:127], v[62:67], v[188:191] cbsz:2 blgp:2
	s_waitcnt lgkmcnt(0)
	v_mfma_f32_16x16x128_f8f6f4 v[134:137], v[128:133], v[8:13], v[134:137] cbsz:2 blgp:2
	v_mfma_f32_16x16x128_f8f6f4 v[204:207], v[128:133], v[44:49], v[204:207] cbsz:2 blgp:2
	v_mfma_f32_16x16x128_f8f6f4 v[138:141], v[128:133], v[20:25], v[138:141] cbsz:2 blgp:2
	v_mfma_f32_16x16x128_f8f6f4 v[208:211], v[128:133], v[56:61], v[208:211] cbsz:2 blgp:2
	v_mfma_f32_16x16x128_f8f6f4 v[142:145], v[128:133], v[32:37], v[142:145] cbsz:2 blgp:2
	v_mfma_f32_16x16x128_f8f6f4 v[212:215], v[128:133], v[68:73], v[212:215] cbsz:2 blgp:2
	v_cndmask_b32_e64 v158, v134, v204, s[0:1]
	v_cndmask_b32_e64 v159, v138, v208, s[0:1]
	v_fma_mix_f32 v158, v158, v100, v148 op_sel_hi:[0,0,1]
	v_fma_mix_f32 v159, v159, v101, v152 op_sel_hi:[0,0,1]
	v_exp_f32_e32 v158, v158
	v_exp_f32_e32 v159, v159
	v_fma_f32 v158, v158, v186, v186
	v_add_f32_e32 v159, 1.0, v159
	v_rcp_f32_e32 v158, v158
	v_rcp_f32_e32 v159, v159
	v_cndmask_b32_e64 v160, v142, v212, s[0:1]
	v_fma_mix_f32 v161, v158, v160, v156 op_sel_hi:[0,0,1]
	v_exp_f32_e32 v161, v161
	s_add_u32 s48, s48, s40
	v_add_f32_e32 v161, 1.0, v161
	v_rcp_f32_e32 v161, v161
	s_addc_u32 s49, s49, s41
	v_fma_f32 v162, v161, -2.0, 1.0
	v_sub_f32_e32 v163, v176, v162
	v_fma_f32 v176, v159, v163, v162
	v_fma_f32 v164, |v176|, s17, v113
	v_fma_f32 v165, |v176|, s18, v114
	v_fma_f32 v166, |v176|, s19, v115
	v_lshrrev_b32_e32 v167, 26, v176
	v_min3_u32 v164, v164, v165, v166
	v_bfi_b32 v168, 31, v164, v167
	s_nop 1
	v_mul_u32_u24_dpp v170, v168, v180 quad_perm:[1,2,3,3] row_mask:0xf bank_mask:0xf bound_ctrl:1
	v_mad_u32_u24 v171, v168, v181, v170
	ds_write_b8_d16_hi v184, v171 offset:544
	global_store_short_d16_hi v185, v176, s[48:49]
	s_waitcnt lgkmcnt(0)
	s_barrier
	ds_read_b128 v[122:125], v192 offset:544
	ds_read_b64 v[126:127], v192 offset:560
	s_barrier
	ds_read_b128 v[128:131], v192 offset:672
	ds_read_b64 v[132:133], v192 offset:688
	s_waitcnt lgkmcnt(2)
	v_mfma_f32_16x16x128_f8f6f4 v[134:137], v[122:127], v[2:7], 0 cbsz:2 blgp:2
	v_mfma_f32_16x16x128_f8f6f4 v[138:141], v[122:127], v[14:19], 0 cbsz:2 blgp:2
	v_mfma_f32_16x16x128_f8f6f4 v[142:145], v[122:127], v[26:31], v[188:191] cbsz:2 blgp:2
	v_mfma_f32_16x16x128_f8f6f4 v[204:207], v[122:127], v[38:43], 0 cbsz:2 blgp:2
	v_mfma_f32_16x16x128_f8f6f4 v[208:211], v[122:127], v[50:55], 0 cbsz:2 blgp:2
	v_mfma_f32_16x16x128_f8f6f4 v[212:215], v[122:127], v[62:67], v[188:191] cbsz:2 blgp:2
	s_waitcnt lgkmcnt(0)
	v_mfma_f32_16x16x128_f8f6f4 v[134:137], v[128:133], v[8:13], v[134:137] cbsz:2 blgp:2
	v_mfma_f32_16x16x128_f8f6f4 v[204:207], v[128:133], v[44:49], v[204:207] cbsz:2 blgp:2
	v_mfma_f32_16x16x128_f8f6f4 v[138:141], v[128:133], v[20:25], v[138:141] cbsz:2 blgp:2
	v_mfma_f32_16x16x128_f8f6f4 v[208:211], v[128:133], v[56:61], v[208:211] cbsz:2 blgp:2
	v_mfma_f32_16x16x128_f8f6f4 v[142:145], v[128:133], v[32:37], v[142:145] cbsz:2 blgp:2
	v_mfma_f32_16x16x128_f8f6f4 v[212:215], v[128:133], v[68:73], v[212:215] cbsz:2 blgp:2
	v_cndmask_b32_e64 v158, v134, v204, s[0:1]
	v_cndmask_b32_e64 v159, v138, v208, s[0:1]
	v_fma_mix_f32 v158, v158, v100, v148 op_sel:[0,0,1] op_sel_hi:[0,0,1]
	v_fma_mix_f32 v159, v159, v101, v152 op_sel:[0,0,1] op_sel_hi:[0,0,1]
	v_exp_f32_e32 v158, v158
	v_exp_f32_e32 v159, v159
	v_fma_f32 v158, v158, v186, v186
	v_add_f32_e32 v159, 1.0, v159
	v_rcp_f32_e32 v158, v158
	v_rcp_f32_e32 v159, v159
	v_cndmask_b32_e64 v160, v142, v212, s[0:1]
	v_fma_mix_f32 v161, v158, v160, v156 op_sel:[0,0,1] op_sel_hi:[0,0,1]
	v_exp_f32_e32 v161, v161
	s_add_u32 s48, s48, s40
	v_add_f32_e32 v161, 1.0, v161
	v_rcp_f32_e32 v161, v161
	s_addc_u32 s49, s49, s41
	v_fma_f32 v162, v161, -2.0, 1.0
	v_sub_f32_e32 v163, v176, v162
	v_fma_f32 v176, v159, v163, v162
	v_fma_f32 v164, |v176|, s17, v113
	v_fma_f32 v165, |v176|, s18, v114
	v_fma_f32 v166, |v176|, s19, v115
	v_lshrrev_b32_e32 v167, 26, v176
	v_min3_u32 v164, v164, v165, v166
	v_bfi_b32 v168, 31, v164, v167
	s_nop 1
	v_mul_u32_u24_dpp v170, v168, v180 quad_perm:[1,2,3,3] row_mask:0xf bank_mask:0xf bound_ctrl:1
	v_mad_u32_u24 v171, v168, v181, v170
	ds_write_b8_d16_hi v184, v171
	global_store_short_d16_hi v185, v176, s[48:49]
	s_waitcnt lgkmcnt(0)
	s_barrier
	ds_read_b128 v[122:125], v192 offset:0
	ds_read_b64 v[126:127], v192 offset:16
	s_barrier
	ds_read_b128 v[128:131], v192 offset:128
	ds_read_b64 v[132:133], v192 offset:144
	s_waitcnt lgkmcnt(2)
	v_mfma_f32_16x16x128_f8f6f4 v[134:137], v[122:127], v[2:7], 0 cbsz:2 blgp:2
	v_mfma_f32_16x16x128_f8f6f4 v[138:141], v[122:127], v[14:19], 0 cbsz:2 blgp:2
	v_mfma_f32_16x16x128_f8f6f4 v[142:145], v[122:127], v[26:31], v[188:191] cbsz:2 blgp:2
	v_mfma_f32_16x16x128_f8f6f4 v[204:207], v[122:127], v[38:43], 0 cbsz:2 blgp:2
	v_mfma_f32_16x16x128_f8f6f4 v[208:211], v[122:127], v[50:55], 0 cbsz:2 blgp:2
	v_mfma_f32_16x16x128_f8f6f4 v[212:215], v[122:127], v[62:67], v[188:191] cbsz:2 blgp:2
	s_waitcnt lgkmcnt(0)
	v_mfma_f32_16x16x128_f8f6f4 v[134:137], v[128:133], v[8:13], v[134:137] cbsz:2 blgp:2
	v_mfma_f32_16x16x128_f8f6f4 v[204:207], v[128:133], v[44:49], v[204:207] cbsz:2 blgp:2
	v_mfma_f32_16x16x128_f8f6f4 v[138:141], v[128:133], v[20:25], v[138:141] cbsz:2 blgp:2
	v_mfma_f32_16x16x128_f8f6f4 v[208:211], v[128:133], v[56:61], v[208:211] cbsz:2 blgp:2
	v_mfma_f32_16x16x128_f8f6f4 v[142:145], v[128:133], v[32:37], v[142:145] cbsz:2 blgp:2
	v_mfma_f32_16x16x128_f8f6f4 v[212:215], v[128:133], v[68:73], v[212:215] cbsz:2 blgp:2
	v_cndmask_b32_e64 v158, v134, v204, s[0:1]
	v_cndmask_b32_e64 v159, v138, v208, s[0:1]
	v_fma_mix_f32 v158, v158, v100, v149 op_sel_hi:[0,0,1]
	v_fma_mix_f32 v159, v159, v101, v153 op_sel_hi:[0,0,1]
	v_exp_f32_e32 v158, v158
	v_exp_f32_e32 v159, v159
	v_fma_f32 v158, v158, v186, v186
	v_add_f32_e32 v159, 1.0, v159
	v_rcp_f32_e32 v158, v158
	v_rcp_f32_e32 v159, v159
	v_cndmask_b32_e64 v160, v142, v212, s[0:1]
	v_fma_mix_f32 v161, v158, v160, v157 op_sel_hi:[0,0,1]
	v_exp_f32_e32 v161, v161
	s_add_u32 s48, s48, s40
	v_add_f32_e32 v161, 1.0, v161
	v_rcp_f32_e32 v161, v161
	s_addc_u32 s49, s49, s41
	v_fma_f32 v162, v161, -2.0, 1.0
	v_sub_f32_e32 v163, v176, v162
	v_fma_f32 v176, v159, v163, v162
	v_fma_f32 v164, |v176|, s17, v113
	v_fma_f32 v165, |v176|, s18, v114
	v_fma_f32 v166, |v176|, s19, v115
	v_lshrrev_b32_e32 v167, 26, v176
	v_min3_u32 v164, v164, v165, v166
	v_bfi_b32 v168, 31, v164, v167
	s_nop 1
	v_mul_u32_u24_dpp v170, v168, v180 quad_perm:[1,2,3,3] row_mask:0xf bank_mask:0xf bound_ctrl:1
	v_mad_u32_u24 v171, v168, v181, v170
	ds_write_b8_d16_hi v184, v171 offset:544
	global_store_short_d16_hi v185, v176, s[48:49]
	s_waitcnt lgkmcnt(0)
	s_barrier
	ds_read_b128 v[122:125], v192 offset:544
	ds_read_b64 v[126:127], v192 offset:560
	s_barrier
	ds_read_b128 v[128:131], v192 offset:672
	ds_read_b64 v[132:133], v192 offset:688
	s_add_i32 s44, s44, 16
	s_waitcnt lgkmcnt(2)
	v_mfma_f32_16x16x128_f8f6f4 v[134:137], v[122:127], v[2:7], 0 cbsz:2 blgp:2
	v_mfma_f32_16x16x128_f8f6f4 v[138:141], v[122:127], v[14:19], 0 cbsz:2 blgp:2
	v_mfma_f32_16x16x128_f8f6f4 v[142:145], v[122:127], v[26:31], v[188:191] cbsz:2 blgp:2
	v_mfma_f32_16x16x128_f8f6f4 v[204:207], v[122:127], v[38:43], 0 cbsz:2 blgp:2
	v_mfma_f32_16x16x128_f8f6f4 v[208:211], v[122:127], v[50:55], 0 cbsz:2 blgp:2
	v_mfma_f32_16x16x128_f8f6f4 v[212:215], v[122:127], v[62:67], v[188:191] cbsz:2 blgp:2
	s_waitcnt lgkmcnt(0)
	v_mfma_f32_16x16x128_f8f6f4 v[134:137], v[128:133], v[8:13], v[134:137] cbsz:2 blgp:2
	v_mfma_f32_16x16x128_f8f6f4 v[204:207], v[128:133], v[44:49], v[204:207] cbsz:2 blgp:2
	v_mfma_f32_16x16x128_f8f6f4 v[138:141], v[128:133], v[20:25], v[138:141] cbsz:2 blgp:2
	v_mfma_f32_16x16x128_f8f6f4 v[208:211], v[128:133], v[56:61], v[208:211] cbsz:2 blgp:2
	v_mfma_f32_16x16x128_f8f6f4 v[142:145], v[128:133], v[32:37], v[142:145] cbsz:2 blgp:2
	v_mfma_f32_16x16x128_f8f6f4 v[212:215], v[128:133], v[68:73], v[212:215] cbsz:2 blgp:2
	v_cndmask_b32_e64 v158, v134, v204, s[0:1]
	v_cndmask_b32_e64 v159, v138, v208, s[0:1]
	v_fma_mix_f32 v158, v158, v100, v149 op_sel:[0,0,1] op_sel_hi:[0,0,1]
	v_fma_mix_f32 v159, v159, v101, v153 op_sel:[0,0,1] op_sel_hi:[0,0,1]
	v_exp_f32_e32 v158, v158
	v_exp_f32_e32 v159, v159
	v_fma_f32 v158, v158, v186, v186
	v_add_f32_e32 v159, 1.0, v159
	v_rcp_f32_e32 v158, v158
	v_rcp_f32_e32 v159, v159
	v_cndmask_b32_e64 v160, v142, v212, s[0:1]
	v_fma_mix_f32 v161, v158, v160, v157 op_sel:[0,0,1] op_sel_hi:[0,0,1]
	v_exp_f32_e32 v161, v161
	s_add_u32 s48, s48, s40
	v_add_f32_e32 v161, 1.0, v161
	v_rcp_f32_e32 v161, v161
	s_addc_u32 s49, s49, s41
	v_fma_f32 v162, v161, -2.0, 1.0
	v_sub_f32_e32 v163, v176, v162
	v_fma_f32 v176, v159, v163, v162
	v_fma_f32 v164, |v176|, s17, v113
	v_fma_f32 v165, |v176|, s18, v114
	v_fma_f32 v166, |v176|, s19, v115
	v_lshrrev_b32_e32 v167, 26, v176
	v_min3_u32 v164, v164, v165, v166
	v_bfi_b32 v168, 31, v164, v167
	s_nop 1
	v_mul_u32_u24_dpp v170, v168, v180 quad_perm:[1,2,3,3] row_mask:0xf bank_mask:0xf bound_ctrl:1
	v_mad_u32_u24 v171, v168, v181, v170
	ds_write_b8_d16_hi v184, v171
	global_store_short_d16_hi v185, v176, s[48:49]
	s_waitcnt lgkmcnt(0)
	s_barrier
	ds_read_b128 v[122:125], v192 offset:0
	ds_read_b64 v[126:127], v192 offset:16
	s_cmp_lt_i32 s44, s45
	s_cbranch_scc1 .Lscan_loop_a_f2
	s_barrier
	s_branch .Lscan_exit_f2

.Lscan_enter_b_f2:
	ds_read_b128 v[122:125], v192 offset:0
	ds_read_b64 v[126:127], v192 offset:16
	ds_read_b128 v[128:131], v192 offset:128
	ds_read_b64 v[132:133], v192 offset:144
	s_waitcnt vmcnt(8)
	global_load_dwordx4 v[146:149], v[196:197], off
	global_load_dwordx4 v[150:153], v[196:197], off offset:512
	global_load_dwordx4 v[154:157], v[196:197], off offset:1024
	v_lshl_add_u64 v[196:197], v[196:197], 0, s[42:43]
	s_waitcnt lgkmcnt(2)
	v_mfma_f32_16x16x128_f8f6f4 v[134:137], v[122:127], v[2:7], 0 cbsz:2 blgp:2
	v_mfma_f32_16x16x128_f8f6f4 v[138:141], v[122:127], v[14:19], 0 cbsz:2 blgp:2
	v_mfma_f32_16x16x128_f8f6f4 v[142:145], v[122:127], v[26:31], v[188:191] cbsz:2 blgp:2
	v_mfma_f32_16x16x128_f8f6f4 v[204:207], v[122:127], v[38:43], 0 cbsz:2 blgp:2
	v_mfma_f32_16x16x128_f8f6f4 v[208:211], v[122:127], v[50:55], 0 cbsz:2 blgp:2
	v_mfma_f32_16x16x128_f8f6f4 v[212:215], v[122:127], v[62:67], v[188:191] cbsz:2 blgp:2
	s_waitcnt lgkmcnt(0)
	v_mfma_f32_16x16x128_f8f6f4 v[134:137], v[128:133], v[8:13], v[134:137] cbsz:2 blgp:2
	v_mfma_f32_16x16x128_f8f6f4 v[204:207], v[128:133], v[44:49], v[204:207] cbsz:2 blgp:2
	v_mfma_f32_16x16x128_f8f6f4 v[138:141], v[128:133], v[20:25], v[138:141] cbsz:2 blgp:2
	v_mfma_f32_16x16x128_f8f6f4 v[208:211], v[128:133], v[56:61], v[208:211] cbsz:2 blgp:2
	v_mfma_f32_16x16x128_f8f6f4 v[142:145], v[128:133], v[32:37], v[142:145] cbsz:2 blgp:2
	v_mfma_f32_16x16x128_f8f6f4 v[212:215], v[128:133], v[68:73], v[212:215] cbsz:2 blgp:2
	v_cndmask_b32_e64 v158, v134, v204, s[0:1]
	v_cndmask_b32_e64 v159, v138, v208, s[0:1]
	v_fma_mix_f32 v158, v158, v100, v82 op_sel_hi:[0,0,1]
	v_fma_mix_f32 v159, v159, v101, v74 op_sel_hi:[0,0,1]
	v_exp_f32_e32 v158, v158
	v_exp_f32_e32 v159, v159
	v_fma_f32 v158, v158, v186, v186
	v_add_f32_e32 v159, 1.0, v159
	v_rcp_f32_e32 v158, v158
	v_rcp_f32_e32 v159, v159
	v_cndmask_b32_e64 v160, v142, v212, s[0:1]
	v_fma_mix_f32 v161, v158, v160, v78 op_sel_hi:[0,0,1]
	v_exp_f32_e32 v161, v161
	s_add_u32 s48, s48, s40
	v_add_f32_e32 v161, 1.0, v161
	v_rcp_f32_e32 v161, v161
	s_addc_u32 s49, s49, s41
	v_fma_f32 v162, v161, -2.0, 1.0
	v_sub_f32_e32 v163, v176, v162
	v_fma_f32 v176, v159, v163, v162
	v_fma_f32 v164, |v176|, s17, v113
	v_fma_f32 v165, |v176|, s18, v114
	v_fma_f32 v166, |v176|, s19, v115
	v_lshrrev_b32_e32 v167, 26, v176
	v_min3_u32 v164, v164, v165, v166
	v_bfi_b32 v168, 31, v164, v167
	s_nop 1
	v_mul_u32_u24_dpp v170, v168, v180 quad_perm:[1,2,3,3] row_mask:0xf bank_mask:0xf bound_ctrl:1
	v_mad_u32_u24 v171, v168, v181, v170
	ds_write_b8_d16_hi v184, v171 offset:544
	s_barrier
	global_store_short_d16_hi v185, v176, s[48:49]
	s_waitcnt lgkmcnt(0)
	s_barrier
	ds_read_b128 v[122:125], v192 offset:544
	ds_read_b64 v[126:127], v192 offset:560
	ds_read_b128 v[128:131], v192 offset:672
	ds_read_b64 v[132:133], v192 offset:688
	s_waitcnt lgkmcnt(2)
	v_mfma_f32_16x16x128_f8f6f4 v[134:137], v[122:127], v[2:7], 0 cbsz:2 blgp:2
	v_mfma_f32_16x16x128_f8f6f4 v[138:141], v[122:127], v[14:19], 0 cbsz:2 blgp:2
	v_mfma_f32_16x16x128_f8f6f4 v[142:145], v[122:127], v[26:31], v[188:191] cbsz:2 blgp:2
	v_mfma_f32_16x16x128_f8f6f4 v[204:207], v[122:127], v[38:43], 0 cbsz:2 blgp:2
	v_mfma_f32_16x16x128_f8f6f4 v[208:211], v[122:127], v[50:55], 0 cbsz:2 blgp:2
	v_mfma_f32_16x16x128_f8f6f4 v[212:215], v[122:127], v[62:67], v[188:191] cbsz:2 blgp:2
	s_waitcnt lgkmcnt(0)
	v_mfma_f32_16x16x128_f8f6f4 v[134:137], v[128:133], v[8:13], v[134:137] cbsz:2 blgp:2
	v_mfma_f32_16x16x128_f8f6f4 v[204:207], v[128:133], v[44:49], v[204:207] cbsz:2 blgp:2
	v_mfma_f32_16x16x128_f8f6f4 v[138:141], v[128:133], v[20:25], v[138:141] cbsz:2 blgp:2
	v_mfma_f32_16x16x128_f8f6f4 v[208:211], v[128:133], v[56:61], v[208:211] cbsz:2 blgp:2
	v_mfma_f32_16x16x128_f8f6f4 v[142:145], v[128:133], v[32:37], v[142:145] cbsz:2 blgp:2
	v_mfma_f32_16x16x128_f8f6f4 v[212:215], v[128:133], v[68:73], v[212:215] cbsz:2 blgp:2
	v_cndmask_b32_e64 v158, v134, v204, s[0:1]
	v_cndmask_b32_e64 v159, v138, v208, s[0:1]
	v_fma_mix_f32 v158, v158, v100, v82 op_sel:[0,0,1] op_sel_hi:[0,0,1]
	v_fma_mix_f32 v159, v159, v101, v74 op_sel:[0,0,1] op_sel_hi:[0,0,1]
	v_exp_f32_e32 v158, v158
	v_exp_f32_e32 v159, v159
	v_fma_f32 v158, v158, v186, v186
	v_add_f32_e32 v159, 1.0, v159
	v_rcp_f32_e32 v158, v158
	v_rcp_f32_e32 v159, v159
	v_cndmask_b32_e64 v160, v142, v212, s[0:1]
	v_fma_mix_f32 v161, v158, v160, v78 op_sel:[0,0,1] op_sel_hi:[0,0,1]
	v_exp_f32_e32 v161, v161
	s_add_u32 s48, s48, s40
	v_add_f32_e32 v161, 1.0, v161
	v_rcp_f32_e32 v161, v161
	s_addc_u32 s49, s49, s41
	v_fma_f32 v162, v161, -2.0, 1.0
	v_sub_f32_e32 v163, v176, v162
	v_fma_f32 v176, v159, v163, v162
	v_fma_f32 v164, |v176|, s17, v113
	v_fma_f32 v165, |v176|, s18, v114
	v_fma_f32 v166, |v176|, s19, v115
	v_lshrrev_b32_e32 v167, 26, v176
	v_min3_u32 v164, v164, v165, v166
	v_bfi_b32 v168, 31, v164, v167
	s_nop 1
	v_mul_u32_u24_dpp v170, v168, v180 quad_perm:[1,2,3,3] row_mask:0xf bank_mask:0xf bound_ctrl:1
	v_mad_u32_u24 v171, v168, v181, v170
	ds_write_b8_d16_hi v184, v171
	s_barrier
	global_store_short_d16_hi v185, v176, s[48:49]
	s_waitcnt lgkmcnt(0)
	s_barrier
	ds_read_b128 v[122:125], v192 offset:0
	ds_read_b64 v[126:127], v192 offset:16
	ds_read_b128 v[128:131], v192 offset:128
	ds_read_b64 v[132:133], v192 offset:144
	s_waitcnt lgkmcnt(2)
	v_mfma_f32_16x16x128_f8f6f4 v[134:137], v[122:127], v[2:7], 0 cbsz:2 blgp:2
	v_mfma_f32_16x16x128_f8f6f4 v[138:141], v[122:127], v[14:19], 0 cbsz:2 blgp:2
	v_mfma_f32_16x16x128_f8f6f4 v[142:145], v[122:127], v[26:31], v[188:191] cbsz:2 blgp:2
	v_mfma_f32_16x16x128_f8f6f4 v[204:207], v[122:127], v[38:43], 0 cbsz:2 blgp:2
	v_mfma_f32_16x16x128_f8f6f4 v[208:211], v[122:127], v[50:55], 0 cbsz:2 blgp:2
	v_mfma_f32_16x16x128_f8f6f4 v[212:215], v[122:127], v[62:67], v[188:191] cbsz:2 blgp:2
	s_waitcnt lgkmcnt(0)
	v_mfma_f32_16x16x128_f8f6f4 v[134:137], v[128:133], v[8:13], v[134:137] cbsz:2 blgp:2
	v_mfma_f32_16x16x128_f8f6f4 v[204:207], v[128:133], v[44:49], v[204:207] cbsz:2 blgp:2
	v_mfma_f32_16x16x128_f8f6f4 v[138:141], v[128:133], v[20:25], v[138:141] cbsz:2 blgp:2
	v_mfma_f32_16x16x128_f8f6f4 v[208:211], v[128:133], v[56:61], v[208:211] cbsz:2 blgp:2
	v_mfma_f32_16x16x128_f8f6f4 v[142:145], v[128:133], v[32:37], v[142:145] cbsz:2 blgp:2
	v_mfma_f32_16x16x128_f8f6f4 v[212:215], v[128:133], v[68:73], v[212:215] cbsz:2 blgp:2
	v_cndmask_b32_e64 v158, v134, v204, s[0:1]
	v_cndmask_b32_e64 v159, v138, v208, s[0:1]
	v_fma_mix_f32 v158, v158, v100, v83 op_sel_hi:[0,0,1]
	v_fma_mix_f32 v159, v159, v101, v75 op_sel_hi:[0,0,1]
	v_exp_f32_e32 v158, v158
	v_exp_f32_e32 v159, v159
	v_fma_f32 v158, v158, v186, v186
	v_add_f32_e32 v159, 1.0, v159
	v_rcp_f32_e32 v158, v158
	v_rcp_f32_e32 v159, v159
	v_cndmask_b32_e64 v160, v142, v212, s[0:1]
	v_fma_mix_f32 v161, v158, v160, v79 op_sel_hi:[0,0,1]
	v_exp_f32_e32 v161, v161
	s_add_u32 s48, s48, s40
	v_add_f32_e32 v161, 1.0, v161
	v_rcp_f32_e32 v161, v161
	s_addc_u32 s49, s49, s41
	v_fma_f32 v162, v161, -2.0, 1.0
	v_sub_f32_e32 v163, v176, v162
	v_fma_f32 v176, v159, v163, v162
	v_fma_f32 v164, |v176|, s17, v113
	v_fma_f32 v165, |v176|, s18, v114
	v_fma_f32 v166, |v176|, s19, v115
	v_lshrrev_b32_e32 v167, 26, v176
	v_min3_u32 v164, v164, v165, v166
	v_bfi_b32 v168, 31, v164, v167
	s_nop 1
	v_mul_u32_u24_dpp v170, v168, v180 quad_perm:[1,2,3,3] row_mask:0xf bank_mask:0xf bound_ctrl:1
	v_mad_u32_u24 v171, v168, v181, v170
	ds_write_b8_d16_hi v184, v171 offset:544
	s_barrier
	global_store_short_d16_hi v185, v176, s[48:49]
	s_waitcnt lgkmcnt(0)
	s_barrier
	ds_read_b128 v[122:125], v192 offset:544
	ds_read_b64 v[126:127], v192 offset:560
	ds_read_b128 v[128:131], v192 offset:672
	ds_read_b64 v[132:133], v192 offset:688
	s_waitcnt lgkmcnt(2)
	v_mfma_f32_16x16x128_f8f6f4 v[134:137], v[122:127], v[2:7], 0 cbsz:2 blgp:2
	v_mfma_f32_16x16x128_f8f6f4 v[138:141], v[122:127], v[14:19], 0 cbsz:2 blgp:2
	v_mfma_f32_16x16x128_f8f6f4 v[142:145], v[122:127], v[26:31], v[188:191] cbsz:2 blgp:2
	v_mfma_f32_16x16x128_f8f6f4 v[204:207], v[122:127], v[38:43], 0 cbsz:2 blgp:2
	v_mfma_f32_16x16x128_f8f6f4 v[208:211], v[122:127], v[50:55], 0 cbsz:2 blgp:2
	v_mfma_f32_16x16x128_f8f6f4 v[212:215], v[122:127], v[62:67], v[188:191] cbsz:2 blgp:2
	s_waitcnt lgkmcnt(0)
	v_mfma_f32_16x16x128_f8f6f4 v[134:137], v[128:133], v[8:13], v[134:137] cbsz:2 blgp:2
	v_mfma_f32_16x16x128_f8f6f4 v[204:207], v[128:133], v[44:49], v[204:207] cbsz:2 blgp:2
	v_mfma_f32_16x16x128_f8f6f4 v[138:141], v[128:133], v[20:25], v[138:141] cbsz:2 blgp:2
	v_mfma_f32_16x16x128_f8f6f4 v[208:211], v[128:133], v[56:61], v[208:211] cbsz:2 blgp:2
	v_mfma_f32_16x16x128_f8f6f4 v[142:145], v[128:133], v[32:37], v[142:145] cbsz:2 blgp:2
	v_mfma_f32_16x16x128_f8f6f4 v[212:215], v[128:133], v[68:73], v[212:215] cbsz:2 blgp:2
	v_cndmask_b32_e64 v158, v134, v204, s[0:1]
	v_cndmask_b32_e64 v159, v138, v208, s[0:1]
	v_fma_mix_f32 v158, v158, v100, v83 op_sel:[0,0,1] op_sel_hi:[0,0,1]
	v_fma_mix_f32 v159, v159, v101, v75 op_sel:[0,0,1] op_sel_hi:[0,0,1]
	v_exp_f32_e32 v158, v158
	v_exp_f32_e32 v159, v159
	v_fma_f32 v158, v158, v186, v186
	v_add_f32_e32 v159, 1.0, v159
	v_rcp_f32_e32 v158, v158
	v_rcp_f32_e32 v159, v159
	v_cndmask_b32_e64 v160, v142, v212, s[0:1]
	v_fma_mix_f32 v161, v158, v160, v79 op_sel:[0,0,1] op_sel_hi:[0,0,1]
	v_exp_f32_e32 v161, v161
	s_add_u32 s48, s48, s40
	v_add_f32_e32 v161, 1.0, v161
	v_rcp_f32_e32 v161, v161
	s_addc_u32 s49, s49, s41
	v_fma_f32 v162, v161, -2.0, 1.0
	v_sub_f32_e32 v163, v176, v162
	v_fma_f32 v176, v159, v163, v162
	v_fma_f32 v164, |v176|, s17, v113
	v_fma_f32 v165, |v176|, s18, v114
	v_fma_f32 v166, |v176|, s19, v115
	v_lshrrev_b32_e32 v167, 26, v176
	v_min3_u32 v164, v164, v165, v166
	v_bfi_b32 v168, 31, v164, v167
	s_nop 1
	v_mul_u32_u24_dpp v170, v168, v180 quad_perm:[1,2,3,3] row_mask:0xf bank_mask:0xf bound_ctrl:1
	v_mad_u32_u24 v171, v168, v181, v170
	ds_write_b8_d16_hi v184, v171
	s_barrier
	global_store_short_d16_hi v185, v176, s[48:49]
	s_waitcnt lgkmcnt(0)
	s_barrier
	ds_read_b128 v[122:125], v192 offset:0
	ds_read_b64 v[126:127], v192 offset:16
	ds_read_b128 v[128:131], v192 offset:128
	ds_read_b64 v[132:133], v192 offset:144
	s_waitcnt lgkmcnt(2)
	v_mfma_f32_16x16x128_f8f6f4 v[134:137], v[122:127], v[2:7], 0 cbsz:2 blgp:2
	v_mfma_f32_16x16x128_f8f6f4 v[138:141], v[122:127], v[14:19], 0 cbsz:2 blgp:2
	v_mfma_f32_16x16x128_f8f6f4 v[142:145], v[122:127], v[26:31], v[188:191] cbsz:2 blgp:2
	v_mfma_f32_16x16x128_f8f6f4 v[204:207], v[122:127], v[38:43], 0 cbsz:2 blgp:2
	v_mfma_f32_16x16x128_f8f6f4 v[208:211], v[122:127], v[50:55], 0 cbsz:2 blgp:2
	v_mfma_f32_16x16x128_f8f6f4 v[212:215], v[122:127], v[62:67], v[188:191] cbsz:2 blgp:2
	s_waitcnt lgkmcnt(0)
	v_mfma_f32_16x16x128_f8f6f4 v[134:137], v[128:133], v[8:13], v[134:137] cbsz:2 blgp:2
	v_mfma_f32_16x16x128_f8f6f4 v[204:207], v[128:133], v[44:49], v[204:207] cbsz:2 blgp:2
	v_mfma_f32_16x16x128_f8f6f4 v[138:141], v[128:133], v[20:25], v[138:141] cbsz:2 blgp:2
	v_mfma_f32_16x16x128_f8f6f4 v[208:211], v[128:133], v[56:61], v[208:211] cbsz:2 blgp:2
	v_mfma_f32_16x16x128_f8f6f4 v[142:145], v[128:133], v[32:37], v[142:145] cbsz:2 blgp:2
	v_mfma_f32_16x16x128_f8f6f4 v[212:215], v[128:133], v[68:73], v[212:215] cbsz:2 blgp:2
	v_cndmask_b32_e64 v158, v134, v204, s[0:1]
	v_cndmask_b32_e64 v159, v138, v208, s[0:1]
	v_fma_mix_f32 v158, v158, v100, v84 op_sel_hi:[0,0,1]
	v_fma_mix_f32 v159, v159, v101, v76 op_sel_hi:[0,0,1]
	v_exp_f32_e32 v158, v158
	v_exp_f32_e32 v159, v159
	v_fma_f32 v158, v158, v186, v186
	v_add_f32_e32 v159, 1.0, v159
	v_rcp_f32_e32 v158, v158
	v_rcp_f32_e32 v159, v159
	v_cndmask_b32_e64 v160, v142, v212, s[0:1]
	v_fma_mix_f32 v161, v158, v160, v80 op_sel_hi:[0,0,1]
	v_exp_f32_e32 v161, v161
	s_add_u32 s48, s48, s40
	v_add_f32_e32 v161, 1.0, v161
	v_rcp_f32_e32 v161, v161
	s_addc_u32 s49, s49, s41
	v_fma_f32 v162, v161, -2.0, 1.0
	v_sub_f32_e32 v163, v176, v162
	v_fma_f32 v176, v159, v163, v162
	v_fma_f32 v164, |v176|, s17, v113
	v_fma_f32 v165, |v176|, s18, v114
	v_fma_f32 v166, |v176|, s19, v115
	v_lshrrev_b32_e32 v167, 26, v176
	v_min3_u32 v164, v164, v165, v166
	v_bfi_b32 v168, 31, v164, v167
	s_nop 1
	v_mul_u32_u24_dpp v170, v168, v180 quad_perm:[1,2,3,3] row_mask:0xf bank_mask:0xf bound_ctrl:1
	v_mad_u32_u24 v171, v168, v181, v170
	ds_write_b8_d16_hi v184, v171 offset:544
	s_barrier
	global_store_short_d16_hi v185, v176, s[48:49]
	s_waitcnt lgkmcnt(0)
	s_barrier
	ds_read_b128 v[122:125], v192 offset:544
	ds_read_b64 v[126:127], v192 offset:560
	ds_read_b128 v[128:131], v192 offset:672
	ds_read_b64 v[132:133], v192 offset:688
	s_waitcnt lgkmcnt(2)
	v_mfma_f32_16x16x128_f8f6f4 v[134:137], v[122:127], v[2:7], 0 cbsz:2 blgp:2
	v_mfma_f32_16x16x128_f8f6f4 v[138:141], v[122:127], v[14:19], 0 cbsz:2 blgp:2
	v_mfma_f32_16x16x128_f8f6f4 v[142:145], v[122:127], v[26:31], v[188:191] cbsz:2 blgp:2
	v_mfma_f32_16x16x128_f8f6f4 v[204:207], v[122:127], v[38:43], 0 cbsz:2 blgp:2
	v_mfma_f32_16x16x128_f8f6f4 v[208:211], v[122:127], v[50:55], 0 cbsz:2 blgp:2
	v_mfma_f32_16x16x128_f8f6f4 v[212:215], v[122:127], v[62:67], v[188:191] cbsz:2 blgp:2
	s_waitcnt lgkmcnt(0)
	v_mfma_f32_16x16x128_f8f6f4 v[134:137], v[128:133], v[8:13], v[134:137] cbsz:2 blgp:2
	v_mfma_f32_16x16x128_f8f6f4 v[204:207], v[128:133], v[44:49], v[204:207] cbsz:2 blgp:2
	v_mfma_f32_16x16x128_f8f6f4 v[138:141], v[128:133], v[20:25], v[138:141] cbsz:2 blgp:2
	v_mfma_f32_16x16x128_f8f6f4 v[208:211], v[128:133], v[56:61], v[208:211] cbsz:2 blgp:2
	v_mfma_f32_16x16x128_f8f6f4 v[142:145], v[128:133], v[32:37], v[142:145] cbsz:2 blgp:2
	v_mfma_f32_16x16x128_f8f6f4 v[212:215], v[128:133], v[68:73], v[212:215] cbsz:2 blgp:2
	v_cndmask_b32_e64 v158, v134, v204, s[0:1]
	v_cndmask_b32_e64 v159, v138, v208, s[0:1]
	v_fma_mix_f32 v158, v158, v100, v84 op_sel:[0,0,1] op_sel_hi:[0,0,1]
	v_fma_mix_f32 v159, v159, v101, v76 op_sel:[0,0,1] op_sel_hi:[0,0,1]
	v_exp_f32_e32 v158, v158
	v_exp_f32_e32 v159, v159
	v_fma_f32 v158, v158, v186, v186
	v_add_f32_e32 v159, 1.0, v159
	v_rcp_f32_e32 v158, v158
	v_rcp_f32_e32 v159, v159
	v_cndmask_b32_e64 v160, v142, v212, s[0:1]
	v_fma_mix_f32 v161, v158, v160, v80 op_sel:[0,0,1] op_sel_hi:[0,0,1]
	v_exp_f32_e32 v161, v161
	s_add_u32 s48, s48, s40
	v_add_f32_e32 v161, 1.0, v161
	v_rcp_f32_e32 v161, v161
	s_addc_u32 s49, s49, s41
	v_fma_f32 v162, v161, -2.0, 1.0
	v_sub_f32_e32 v163, v176, v162
	v_fma_f32 v176, v159, v163, v162
	v_fma_f32 v164, |v176|, s17, v113
	v_fma_f32 v165, |v176|, s18, v114
	v_fma_f32 v166, |v176|, s19, v115
	v_lshrrev_b32_e32 v167, 26, v176
	v_min3_u32 v164, v164, v165, v166
	v_bfi_b32 v168, 31, v164, v167
	s_nop 1
	v_mul_u32_u24_dpp v170, v168, v180 quad_perm:[1,2,3,3] row_mask:0xf bank_mask:0xf bound_ctrl:1
	v_mad_u32_u24 v171, v168, v181, v170
	ds_write_b8_d16_hi v184, v171
	s_barrier
	global_store_short_d16_hi v185, v176, s[48:49]
	s_waitcnt lgkmcnt(0)
	s_barrier
	ds_read_b128 v[122:125], v192 offset:0
	ds_read_b64 v[126:127], v192 offset:16
	ds_read_b128 v[128:131], v192 offset:128
	ds_read_b64 v[132:133], v192 offset:144
	s_waitcnt lgkmcnt(2)
	v_mfma_f32_16x16x128_f8f6f4 v[134:137], v[122:127], v[2:7], 0 cbsz:2 blgp:2
	v_mfma_f32_16x16x128_f8f6f4 v[138:141], v[122:127], v[14:19], 0 cbsz:2 blgp:2
	v_mfma_f32_16x16x128_f8f6f4 v[142:145], v[122:127], v[26:31], v[188:191] cbsz:2 blgp:2
	v_mfma_f32_16x16x128_f8f6f4 v[204:207], v[122:127], v[38:43], 0 cbsz:2 blgp:2
	v_mfma_f32_16x16x128_f8f6f4 v[208:211], v[122:127], v[50:55], 0 cbsz:2 blgp:2
	v_mfma_f32_16x16x128_f8f6f4 v[212:215], v[122:127], v[62:67], v[188:191] cbsz:2 blgp:2
	s_waitcnt lgkmcnt(0)
	v_mfma_f32_16x16x128_f8f6f4 v[134:137], v[128:133], v[8:13], v[134:137] cbsz:2 blgp:2
	v_mfma_f32_16x16x128_f8f6f4 v[204:207], v[128:133], v[44:49], v[204:207] cbsz:2 blgp:2
	v_mfma_f32_16x16x128_f8f6f4 v[138:141], v[128:133], v[20:25], v[138:141] cbsz:2 blgp:2
	v_mfma_f32_16x16x128_f8f6f4 v[208:211], v[128:133], v[56:61], v[208:211] cbsz:2 blgp:2
	v_mfma_f32_16x16x128_f8f6f4 v[142:145], v[128:133], v[32:37], v[142:145] cbsz:2 blgp:2
	v_mfma_f32_16x16x128_f8f6f4 v[212:215], v[128:133], v[68:73], v[212:215] cbsz:2 blgp:2
	v_cndmask_b32_e64 v158, v134, v204, s[0:1]
	v_cndmask_b32_e64 v159, v138, v208, s[0:1]
	v_fma_mix_f32 v158, v158, v100, v85 op_sel_hi:[0,0,1]
	v_fma_mix_f32 v159, v159, v101, v77 op_sel_hi:[0,0,1]
	v_exp_f32_e32 v158, v158
	v_exp_f32_e32 v159, v159
	v_fma_f32 v158, v158, v186, v186
	v_add_f32_e32 v159, 1.0, v159
	v_rcp_f32_e32 v158, v158
	v_rcp_f32_e32 v159, v159
	v_cndmask_b32_e64 v160, v142, v212, s[0:1]
	v_fma_mix_f32 v161, v158, v160, v81 op_sel_hi:[0,0,1]
	v_exp_f32_e32 v161, v161
	s_add_u32 s48, s48, s40
	v_add_f32_e32 v161, 1.0, v161
	v_rcp_f32_e32 v161, v161
	s_addc_u32 s49, s49, s41
	v_fma_f32 v162, v161, -2.0, 1.0
	v_sub_f32_e32 v163, v176, v162
	v_fma_f32 v176, v159, v163, v162
	v_fma_f32 v164, |v176|, s17, v113
	v_fma_f32 v165, |v176|, s18, v114
	v_fma_f32 v166, |v176|, s19, v115
	v_lshrrev_b32_e32 v167, 26, v176
	v_min3_u32 v164, v164, v165, v166
	v_bfi_b32 v168, 31, v164, v167
	s_nop 1
	v_mul_u32_u24_dpp v170, v168, v180 quad_perm:[1,2,3,3] row_mask:0xf bank_mask:0xf bound_ctrl:1
	v_mad_u32_u24 v171, v168, v181, v170
	ds_write_b8_d16_hi v184, v171 offset:544
	s_barrier
	global_store_short_d16_hi v185, v176, s[48:49]
	s_waitcnt lgkmcnt(0)
	s_barrier
	ds_read_b128 v[122:125], v192 offset:544
	ds_read_b64 v[126:127], v192 offset:560
	ds_read_b128 v[128:131], v192 offset:672
	ds_read_b64 v[132:133], v192 offset:688
	s_waitcnt lgkmcnt(2)
	v_mfma_f32_16x16x128_f8f6f4 v[134:137], v[122:127], v[2:7], 0 cbsz:2 blgp:2
	v_mfma_f32_16x16x128_f8f6f4 v[138:141], v[122:127], v[14:19], 0 cbsz:2 blgp:2
	v_mfma_f32_16x16x128_f8f6f4 v[142:145], v[122:127], v[26:31], v[188:191] cbsz:2 blgp:2
	v_mfma_f32_16x16x128_f8f6f4 v[204:207], v[122:127], v[38:43], 0 cbsz:2 blgp:2
	v_mfma_f32_16x16x128_f8f6f4 v[208:211], v[122:127], v[50:55], 0 cbsz:2 blgp:2
	v_mfma_f32_16x16x128_f8f6f4 v[212:215], v[122:127], v[62:67], v[188:191] cbsz:2 blgp:2
	s_waitcnt lgkmcnt(0)
	v_mfma_f32_16x16x128_f8f6f4 v[134:137], v[128:133], v[8:13], v[134:137] cbsz:2 blgp:2
	v_mfma_f32_16x16x128_f8f6f4 v[204:207], v[128:133], v[44:49], v[204:207] cbsz:2 blgp:2
	v_mfma_f32_16x16x128_f8f6f4 v[138:141], v[128:133], v[20:25], v[138:141] cbsz:2 blgp:2
	v_mfma_f32_16x16x128_f8f6f4 v[208:211], v[128:133], v[56:61], v[208:211] cbsz:2 blgp:2
	v_mfma_f32_16x16x128_f8f6f4 v[142:145], v[128:133], v[32:37], v[142:145] cbsz:2 blgp:2
	v_mfma_f32_16x16x128_f8f6f4 v[212:215], v[128:133], v[68:73], v[212:215] cbsz:2 blgp:2
	v_cndmask_b32_e64 v158, v134, v204, s[0:1]
	v_cndmask_b32_e64 v159, v138, v208, s[0:1]
	v_fma_mix_f32 v158, v158, v100, v85 op_sel:[0,0,1] op_sel_hi:[0,0,1]
	v_fma_mix_f32 v159, v159, v101, v77 op_sel:[0,0,1] op_sel_hi:[0,0,1]
	v_exp_f32_e32 v158, v158
	v_exp_f32_e32 v159, v159
	v_fma_f32 v158, v158, v186, v186
	v_add_f32_e32 v159, 1.0, v159
	v_rcp_f32_e32 v158, v158
	v_rcp_f32_e32 v159, v159
	v_cndmask_b32_e64 v160, v142, v212, s[0:1]
	v_fma_mix_f32 v161, v158, v160, v81 op_sel:[0,0,1] op_sel_hi:[0,0,1]
	v_exp_f32_e32 v161, v161
	s_add_u32 s48, s48, s40
	v_add_f32_e32 v161, 1.0, v161
	v_rcp_f32_e32 v161, v161
	s_addc_u32 s49, s49, s41
	v_fma_f32 v162, v161, -2.0, 1.0
	v_sub_f32_e32 v163, v176, v162
	v_fma_f32 v176, v159, v163, v162
	v_fma_f32 v164, |v176|, s17, v113
	v_fma_f32 v165, |v176|, s18, v114
	v_fma_f32 v166, |v176|, s19, v115
	v_lshrrev_b32_e32 v167, 26, v176
	v_min3_u32 v164, v164, v165, v166
	v_bfi_b32 v168, 31, v164, v167
	s_nop 1
	v_mul_u32_u24_dpp v170, v168, v180 quad_perm:[1,2,3,3] row_mask:0xf bank_mask:0xf bound_ctrl:1
	v_mad_u32_u24 v171, v168, v181, v170
	ds_write_b8_d16_hi v184, v171
	s_barrier
	global_store_short_d16_hi v185, v176, s[48:49]
	s_waitcnt lgkmcnt(0)
	s_barrier
	ds_read_b128 v[122:125], v192 offset:0
	ds_read_b64 v[126:127], v192 offset:16
	ds_read_b128 v[128:131], v192 offset:128
	ds_read_b64 v[132:133], v192 offset:144
	s_waitcnt vmcnt(8)
	global_load_dwordx4 v[82:85], v[196:197], off
	global_load_dwordx4 v[74:77], v[196:197], off offset:512
	global_load_dwordx4 v[78:81], v[196:197], off offset:1024
	v_lshl_add_u64 v[196:197], v[196:197], 0, s[42:43]
	s_waitcnt lgkmcnt(2)
	v_mfma_f32_16x16x128_f8f6f4 v[134:137], v[122:127], v[2:7], 0 cbsz:2 blgp:2
	v_mfma_f32_16x16x128_f8f6f4 v[138:141], v[122:127], v[14:19], 0 cbsz:2 blgp:2
	v_mfma_f32_16x16x128_f8f6f4 v[142:145], v[122:127], v[26:31], v[188:191] cbsz:2 blgp:2
	v_mfma_f32_16x16x128_f8f6f4 v[204:207], v[122:127], v[38:43], 0 cbsz:2 blgp:2
	v_mfma_f32_16x16x128_f8f6f4 v[208:211], v[122:127], v[50:55], 0 cbsz:2 blgp:2
	v_mfma_f32_16x16x128_f8f6f4 v[212:215], v[122:127], v[62:67], v[188:191] cbsz:2 blgp:2
	s_waitcnt lgkmcnt(0)
	v_mfma_f32_16x16x128_f8f6f4 v[134:137], v[128:133], v[8:13], v[134:137] cbsz:2 blgp:2
	v_mfma_f32_16x16x128_f8f6f4 v[204:207], v[128:133], v[44:49], v[204:207] cbsz:2 blgp:2
	v_mfma_f32_16x16x128_f8f6f4 v[138:141], v[128:133], v[20:25], v[138:141] cbsz:2 blgp:2
	v_mfma_f32_16x16x128_f8f6f4 v[208:211], v[128:133], v[56:61], v[208:211] cbsz:2 blgp:2
	v_mfma_f32_16x16x128_f8f6f4 v[142:145], v[128:133], v[32:37], v[142:145] cbsz:2 blgp:2
	v_mfma_f32_16x16x128_f8f6f4 v[212:215], v[128:133], v[68:73], v[212:215] cbsz:2 blgp:2
	v_cndmask_b32_e64 v158, v134, v204, s[0:1]
	v_cndmask_b32_e64 v159, v138, v208, s[0:1]
	v_fma_mix_f32 v158, v158, v100, v146 op_sel_hi:[0,0,1]
	v_fma_mix_f32 v159, v159, v101, v150 op_sel_hi:[0,0,1]
	v_exp_f32_e32 v158, v158
	v_exp_f32_e32 v159, v159
	v_fma_f32 v158, v158, v186, v186
	v_add_f32_e32 v159, 1.0, v159
	v_rcp_f32_e32 v158, v158
	v_rcp_f32_e32 v159, v159
	v_cndmask_b32_e64 v160, v142, v212, s[0:1]
	v_fma_mix_f32 v161, v158, v160, v154 op_sel_hi:[0,0,1]
	v_exp_f32_e32 v161, v161
	s_add_u32 s48, s48, s40
	v_add_f32_e32 v161, 1.0, v161
	v_rcp_f32_e32 v161, v161
	s_addc_u32 s49, s49, s41
	v_fma_f32 v162, v161, -2.0, 1.0
	v_sub_f32_e32 v163, v176, v162
	v_fma_f32 v176, v159, v163, v162
	v_fma_f32 v164, |v176|, s17, v113
	v_fma_f32 v165, |v176|, s18, v114
	v_fma_f32 v166, |v176|, s19, v115
	v_lshrrev_b32_e32 v167, 26, v176
	v_min3_u32 v164, v164, v165, v166
	v_bfi_b32 v168, 31, v164, v167
	s_nop 1
	v_mul_u32_u24_dpp v170, v168, v180 quad_perm:[1,2,3,3] row_mask:0xf bank_mask:0xf bound_ctrl:1
	v_mad_u32_u24 v171, v168, v181, v170
	ds_write_b8_d16_hi v184, v171 offset:544
	s_barrier
	global_store_short_d16_hi v185, v176, s[48:49]
	s_waitcnt lgkmcnt(0)
	s_barrier
	ds_read_b128 v[122:125], v192 offset:544
	ds_read_b64 v[126:127], v192 offset:560
	ds_read_b128 v[128:131], v192 offset:672
	ds_read_b64 v[132:133], v192 offset:688
	s_waitcnt lgkmcnt(2)
	v_mfma_f32_16x16x128_f8f6f4 v[134:137], v[122:127], v[2:7], 0 cbsz:2 blgp:2
	v_mfma_f32_16x16x128_f8f6f4 v[138:141], v[122:127], v[14:19], 0 cbsz:2 blgp:2
	v_mfma_f32_16x16x128_f8f6f4 v[142:145], v[122:127], v[26:31], v[188:191] cbsz:2 blgp:2
	v_mfma_f32_16x16x128_f8f6f4 v[204:207], v[122:127], v[38:43], 0 cbsz:2 blgp:2
	v_mfma_f32_16x16x128_f8f6f4 v[208:211], v[122:127], v[50:55], 0 cbsz:2 blgp:2
	v_mfma_f32_16x16x128_f8f6f4 v[212:215], v[122:127], v[62:67], v[188:191] cbsz:2 blgp:2
	s_waitcnt lgkmcnt(0)
	v_mfma_f32_16x16x128_f8f6f4 v[134:137], v[128:133], v[8:13], v[134:137] cbsz:2 blgp:2
	v_mfma_f32_16x16x128_f8f6f4 v[204:207], v[128:133], v[44:49], v[204:207] cbsz:2 blgp:2
	v_mfma_f32_16x16x128_f8f6f4 v[138:141], v[128:133], v[20:25], v[138:141] cbsz:2 blgp:2
	v_mfma_f32_16x16x128_f8f6f4 v[208:211], v[128:133], v[56:61], v[208:211] cbsz:2 blgp:2
	v_mfma_f32_16x16x128_f8f6f4 v[142:145], v[128:133], v[32:37], v[142:145] cbsz:2 blgp:2
	v_mfma_f32_16x16x128_f8f6f4 v[212:215], v[128:133], v[68:73], v[212:215] cbsz:2 blgp:2
	v_cndmask_b32_e64 v158, v134, v204, s[0:1]
	v_cndmask_b32_e64 v159, v138, v208, s[0:1]
	v_fma_mix_f32 v158, v158, v100, v146 op_sel:[0,0,1] op_sel_hi:[0,0,1]
	v_fma_mix_f32 v159, v159, v101, v150 op_sel:[0,0,1] op_sel_hi:[0,0,1]
	v_exp_f32_e32 v158, v158
	v_exp_f32_e32 v159, v159
	v_fma_f32 v158, v158, v186, v186
	v_add_f32_e32 v159, 1.0, v159
	v_rcp_f32_e32 v158, v158
	v_rcp_f32_e32 v159, v159
	v_cndmask_b32_e64 v160, v142, v212, s[0:1]
	v_fma_mix_f32 v161, v158, v160, v154 op_sel:[0,0,1] op_sel_hi:[0,0,1]
	v_exp_f32_e32 v161, v161
	s_add_u32 s48, s48, s40
	v_add_f32_e32 v161, 1.0, v161
	v_rcp_f32_e32 v161, v161
	s_addc_u32 s49, s49, s41
	v_fma_f32 v162, v161, -2.0, 1.0
	v_sub_f32_e32 v163, v176, v162
	v_fma_f32 v176, v159, v163, v162
	v_fma_f32 v164, |v176|, s17, v113
	v_fma_f32 v165, |v176|, s18, v114
	v_fma_f32 v166, |v176|, s19, v115
	v_lshrrev_b32_e32 v167, 26, v176
	v_min3_u32 v164, v164, v165, v166
	v_bfi_b32 v168, 31, v164, v167
	s_nop 1
	v_mul_u32_u24_dpp v170, v168, v180 quad_perm:[1,2,3,3] row_mask:0xf bank_mask:0xf bound_ctrl:1
	v_mad_u32_u24 v171, v168, v181, v170
	ds_write_b8_d16_hi v184, v171
	s_barrier
	global_store_short_d16_hi v185, v176, s[48:49]
	s_waitcnt lgkmcnt(0)
	s_barrier
	ds_read_b128 v[122:125], v192 offset:0
	ds_read_b64 v[126:127], v192 offset:16
	ds_read_b128 v[128:131], v192 offset:128
	ds_read_b64 v[132:133], v192 offset:144
	s_waitcnt lgkmcnt(2)
	v_mfma_f32_16x16x128_f8f6f4 v[134:137], v[122:127], v[2:7], 0 cbsz:2 blgp:2
	v_mfma_f32_16x16x128_f8f6f4 v[138:141], v[122:127], v[14:19], 0 cbsz:2 blgp:2
	v_mfma_f32_16x16x128_f8f6f4 v[142:145], v[122:127], v[26:31], v[188:191] cbsz:2 blgp:2
	v_mfma_f32_16x16x128_f8f6f4 v[204:207], v[122:127], v[38:43], 0 cbsz:2 blgp:2
	v_mfma_f32_16x16x128_f8f6f4 v[208:211], v[122:127], v[50:55], 0 cbsz:2 blgp:2
	v_mfma_f32_16x16x128_f8f6f4 v[212:215], v[122:127], v[62:67], v[188:191] cbsz:2 blgp:2
	s_waitcnt lgkmcnt(0)
	v_mfma_f32_16x16x128_f8f6f4 v[134:137], v[128:133], v[8:13], v[134:137] cbsz:2 blgp:2
	v_mfma_f32_16x16x128_f8f6f4 v[204:207], v[128:133], v[44:49], v[204:207] cbsz:2 blgp:2
	v_mfma_f32_16x16x128_f8f6f4 v[138:141], v[128:133], v[20:25], v[138:141] cbsz:2 blgp:2
	v_mfma_f32_16x16x128_f8f6f4 v[208:211], v[128:133], v[56:61], v[208:211] cbsz:2 blgp:2
	v_mfma_f32_16x16x128_f8f6f4 v[142:145], v[128:133], v[32:37], v[142:145] cbsz:2 blgp:2
	v_mfma_f32_16x16x128_f8f6f4 v[212:215], v[128:133], v[68:73], v[212:215] cbsz:2 blgp:2
	v_cndmask_b32_e64 v158, v134, v204, s[0:1]
	v_cndmask_b32_e64 v159, v138, v208, s[0:1]
	v_fma_mix_f32 v158, v158, v100, v147 op_sel_hi:[0,0,1]
	v_fma_mix_f32 v159, v159, v101, v151 op_sel_hi:[0,0,1]
	v_exp_f32_e32 v158, v158
	v_exp_f32_e32 v159, v159
	v_fma_f32 v158, v158, v186, v186
	v_add_f32_e32 v159, 1.0, v159
	v_rcp_f32_e32 v158, v158
	v_rcp_f32_e32 v159, v159
	v_cndmask_b32_e64 v160, v142, v212, s[0:1]
	v_fma_mix_f32 v161, v158, v160, v155 op_sel_hi:[0,0,1]
	v_exp_f32_e32 v161, v161
	s_add_u32 s48, s48, s40
	v_add_f32_e32 v161, 1.0, v161
	v_rcp_f32_e32 v161, v161
	s_addc_u32 s49, s49, s41
	v_fma_f32 v162, v161, -2.0, 1.0
	v_sub_f32_e32 v163, v176, v162
	v_fma_f32 v176, v159, v163, v162
	v_fma_f32 v164, |v176|, s17, v113
	v_fma_f32 v165, |v176|, s18, v114
	v_fma_f32 v166, |v176|, s19, v115
	v_lshrrev_b32_e32 v167, 26, v176
	v_min3_u32 v164, v164, v165, v166
	v_bfi_b32 v168, 31, v164, v167
	s_nop 1
	v_mul_u32_u24_dpp v170, v168, v180 quad_perm:[1,2,3,3] row_mask:0xf bank_mask:0xf bound_ctrl:1
	v_mad_u32_u24 v171, v168, v181, v170
	ds_write_b8_d16_hi v184, v171 offset:544
	s_barrier
	global_store_short_d16_hi v185, v176, s[48:49]
	s_waitcnt lgkmcnt(0)
	s_barrier
	ds_read_b128 v[122:125], v192 offset:544
	ds_read_b64 v[126:127], v192 offset:560
	ds_read_b128 v[128:131], v192 offset:672
	ds_read_b64 v[132:133], v192 offset:688
	s_waitcnt lgkmcnt(2)
	v_mfma_f32_16x16x128_f8f6f4 v[134:137], v[122:127], v[2:7], 0 cbsz:2 blgp:2
	v_mfma_f32_16x16x128_f8f6f4 v[138:141], v[122:127], v[14:19], 0 cbsz:2 blgp:2
	v_mfma_f32_16x16x128_f8f6f4 v[142:145], v[122:127], v[26:31], v[188:191] cbsz:2 blgp:2
	v_mfma_f32_16x16x128_f8f6f4 v[204:207], v[122:127], v[38:43], 0 cbsz:2 blgp:2
	v_mfma_f32_16x16x128_f8f6f4 v[208:211], v[122:127], v[50:55], 0 cbsz:2 blgp:2
	v_mfma_f32_16x16x128_f8f6f4 v[212:215], v[122:127], v[62:67], v[188:191] cbsz:2 blgp:2
	s_waitcnt lgkmcnt(0)
	v_mfma_f32_16x16x128_f8f6f4 v[134:137], v[128:133], v[8:13], v[134:137] cbsz:2 blgp:2
	v_mfma_f32_16x16x128_f8f6f4 v[204:207], v[128:133], v[44:49], v[204:207] cbsz:2 blgp:2
	v_mfma_f32_16x16x128_f8f6f4 v[138:141], v[128:133], v[20:25], v[138:141] cbsz:2 blgp:2
	v_mfma_f32_16x16x128_f8f6f4 v[208:211], v[128:133], v[56:61], v[208:211] cbsz:2 blgp:2
	v_mfma_f32_16x16x128_f8f6f4 v[142:145], v[128:133], v[32:37], v[142:145] cbsz:2 blgp:2
	v_mfma_f32_16x16x128_f8f6f4 v[212:215], v[128:133], v[68:73], v[212:215] cbsz:2 blgp:2
	v_cndmask_b32_e64 v158, v134, v204, s[0:1]
	v_cndmask_b32_e64 v159, v138, v208, s[0:1]
	v_fma_mix_f32 v158, v158, v100, v147 op_sel:[0,0,1] op_sel_hi:[0,0,1]
	v_fma_mix_f32 v159, v159, v101, v151 op_sel:[0,0,1] op_sel_hi:[0,0,1]
	v_exp_f32_e32 v158, v158
	v_exp_f32_e32 v159, v159
	v_fma_f32 v158, v158, v186, v186
	v_add_f32_e32 v159, 1.0, v159
	v_rcp_f32_e32 v158, v158
	v_rcp_f32_e32 v159, v159
	v_cndmask_b32_e64 v160, v142, v212, s[0:1]
	v_fma_mix_f32 v161, v158, v160, v155 op_sel:[0,0,1] op_sel_hi:[0,0,1]
	v_exp_f32_e32 v161, v161
	s_add_u32 s48, s48, s40
	v_add_f32_e32 v161, 1.0, v161
	v_rcp_f32_e32 v161, v161
	s_addc_u32 s49, s49, s41
	v_fma_f32 v162, v161, -2.0, 1.0
	v_sub_f32_e32 v163, v176, v162
	v_fma_f32 v176, v159, v163, v162
	v_fma_f32 v164, |v176|, s17, v113
	v_fma_f32 v165, |v176|, s18, v114
	v_fma_f32 v166, |v176|, s19, v115
	v_lshrrev_b32_e32 v167, 26, v176
	v_min3_u32 v164, v164, v165, v166
	v_bfi_b32 v168, 31, v164, v167
	s_nop 1
	v_mul_u32_u24_dpp v170, v168, v180 quad_perm:[1,2,3,3] row_mask:0xf bank_mask:0xf bound_ctrl:1
	v_mad_u32_u24 v171, v168, v181, v170
	ds_write_b8_d16_hi v184, v171
	s_barrier
	global_store_short_d16_hi v185, v176, s[48:49]
	s_waitcnt lgkmcnt(0)
	s_barrier
	ds_read_b128 v[122:125], v192 offset:0
	ds_read_b64 v[126:127], v192 offset:16
	ds_read_b128 v[128:131], v192 offset:128
	ds_read_b64 v[132:133], v192 offset:144
	s_waitcnt lgkmcnt(2)
	v_mfma_f32_16x16x128_f8f6f4 v[134:137], v[122:127], v[2:7], 0 cbsz:2 blgp:2
	v_mfma_f32_16x16x128_f8f6f4 v[138:141], v[122:127], v[14:19], 0 cbsz:2 blgp:2
	v_mfma_f32_16x16x128_f8f6f4 v[142:145], v[122:127], v[26:31], v[188:191] cbsz:2 blgp:2
	v_mfma_f32_16x16x128_f8f6f4 v[204:207], v[122:127], v[38:43], 0 cbsz:2 blgp:2
	v_mfma_f32_16x16x128_f8f6f4 v[208:211], v[122:127], v[50:55], 0 cbsz:2 blgp:2
	v_mfma_f32_16x16x128_f8f6f4 v[212:215], v[122:127], v[62:67], v[188:191] cbsz:2 blgp:2
	s_waitcnt lgkmcnt(0)
	v_mfma_f32_16x16x128_f8f6f4 v[134:137], v[128:133], v[8:13], v[134:137] cbsz:2 blgp:2
	v_mfma_f32_16x16x128_f8f6f4 v[204:207], v[128:133], v[44:49], v[204:207] cbsz:2 blgp:2
	v_mfma_f32_16x16x128_f8f6f4 v[138:141], v[128:133], v[20:25], v[138:141] cbsz:2 blgp:2
	v_mfma_f32_16x16x128_f8f6f4 v[208:211], v[128:133], v[56:61], v[208:211] cbsz:2 blgp:2
	v_mfma_f32_16x16x128_f8f6f4 v[142:145], v[128:133], v[32:37], v[142:145] cbsz:2 blgp:2
	v_mfma_f32_16x16x128_f8f6f4 v[212:215], v[128:133], v[68:73], v[212:215] cbsz:2 blgp:2
	v_cndmask_b32_e64 v158, v134, v204, s[0:1]
	v_cndmask_b32_e64 v159, v138, v208, s[0:1]
	v_fma_mix_f32 v158, v158, v100, v148 op_sel_hi:[0,0,1]
	v_fma_mix_f32 v159, v159, v101, v152 op_sel_hi:[0,0,1]
	v_exp_f32_e32 v158, v158
	v_exp_f32_e32 v159, v159
	v_fma_f32 v158, v158, v186, v186
	v_add_f32_e32 v159, 1.0, v159
	v_rcp_f32_e32 v158, v158
	v_rcp_f32_e32 v159, v159
	v_cndmask_b32_e64 v160, v142, v212, s[0:1]
	v_fma_mix_f32 v161, v158, v160, v156 op_sel_hi:[0,0,1]
	v_exp_f32_e32 v161, v161
	s_add_u32 s48, s48, s40
	v_add_f32_e32 v161, 1.0, v161
	v_rcp_f32_e32 v161, v161
	s_addc_u32 s49, s49, s41
	v_fma_f32 v162, v161, -2.0, 1.0
	v_sub_f32_e32 v163, v176, v162
	v_fma_f32 v176, v159, v163, v162
	v_fma_f32 v164, |v176|, s17, v113
	v_fma_f32 v165, |v176|, s18, v114
	v_fma_f32 v166, |v176|, s19, v115
	v_lshrrev_b32_e32 v167, 26, v176
	v_min3_u32 v164, v164, v165, v166
	v_bfi_b32 v168, 31, v164, v167
	s_nop 1
	v_mul_u32_u24_dpp v170, v168, v180 quad_perm:[1,2,3,3] row_mask:0xf bank_mask:0xf bound_ctrl:1
	v_mad_u32_u24 v171, v168, v181, v170
	ds_write_b8_d16_hi v184, v171 offset:544
	s_barrier
	global_store_short_d16_hi v185, v176, s[48:49]
	s_waitcnt lgkmcnt(0)
	s_barrier
	ds_read_b128 v[122:125], v192 offset:544
	ds_read_b64 v[126:127], v192 offset:560
	ds_read_b128 v[128:131], v192 offset:672
	ds_read_b64 v[132:133], v192 offset:688
	s_waitcnt lgkmcnt(2)
	v_mfma_f32_16x16x128_f8f6f4 v[134:137], v[122:127], v[2:7], 0 cbsz:2 blgp:2
	v_mfma_f32_16x16x128_f8f6f4 v[138:141], v[122:127], v[14:19], 0 cbsz:2 blgp:2
	v_mfma_f32_16x16x128_f8f6f4 v[142:145], v[122:127], v[26:31], v[188:191] cbsz:2 blgp:2
	v_mfma_f32_16x16x128_f8f6f4 v[204:207], v[122:127], v[38:43], 0 cbsz:2 blgp:2
	v_mfma_f32_16x16x128_f8f6f4 v[208:211], v[122:127], v[50:55], 0 cbsz:2 blgp:2
	v_mfma_f32_16x16x128_f8f6f4 v[212:215], v[122:127], v[62:67], v[188:191] cbsz:2 blgp:2
	s_waitcnt lgkmcnt(0)
	v_mfma_f32_16x16x128_f8f6f4 v[134:137], v[128:133], v[8:13], v[134:137] cbsz:2 blgp:2
	v_mfma_f32_16x16x128_f8f6f4 v[204:207], v[128:133], v[44:49], v[204:207] cbsz:2 blgp:2
	v_mfma_f32_16x16x128_f8f6f4 v[138:141], v[128:133], v[20:25], v[138:141] cbsz:2 blgp:2
	v_mfma_f32_16x16x128_f8f6f4 v[208:211], v[128:133], v[56:61], v[208:211] cbsz:2 blgp:2
	v_mfma_f32_16x16x128_f8f6f4 v[142:145], v[128:133], v[32:37], v[142:145] cbsz:2 blgp:2
	v_mfma_f32_16x16x128_f8f6f4 v[212:215], v[128:133], v[68:73], v[212:215] cbsz:2 blgp:2
	v_cndmask_b32_e64 v158, v134, v204, s[0:1]
	v_cndmask_b32_e64 v159, v138, v208, s[0:1]
	v_fma_mix_f32 v158, v158, v100, v148 op_sel:[0,0,1] op_sel_hi:[0,0,1]
	v_fma_mix_f32 v159, v159, v101, v152 op_sel:[0,0,1] op_sel_hi:[0,0,1]
	v_exp_f32_e32 v158, v158
	v_exp_f32_e32 v159, v159
	v_fma_f32 v158, v158, v186, v186
	v_add_f32_e32 v159, 1.0, v159
	v_rcp_f32_e32 v158, v158
	v_rcp_f32_e32 v159, v159
	v_cndmask_b32_e64 v160, v142, v212, s[0:1]
	v_fma_mix_f32 v161, v158, v160, v156 op_sel:[0,0,1] op_sel_hi:[0,0,1]
	v_exp_f32_e32 v161, v161
	s_add_u32 s48, s48, s40
	v_add_f32_e32 v161, 1.0, v161
	v_rcp_f32_e32 v161, v161
	s_addc_u32 s49, s49, s41
	v_fma_f32 v162, v161, -2.0, 1.0
	v_sub_f32_e32 v163, v176, v162
	v_fma_f32 v176, v159, v163, v162
	v_fma_f32 v164, |v176|, s17, v113
	v_fma_f32 v165, |v176|, s18, v114
	v_fma_f32 v166, |v176|, s19, v115
	v_lshrrev_b32_e32 v167, 26, v176
	v_min3_u32 v164, v164, v165, v166
	v_bfi_b32 v168, 31, v164, v167
	s_nop 1
	v_mul_u32_u24_dpp v170, v168, v180 quad_perm:[1,2,3,3] row_mask:0xf bank_mask:0xf bound_ctrl:1
	v_mad_u32_u24 v171, v168, v181, v170
	ds_write_b8_d16_hi v184, v171
	s_barrier
	global_store_short_d16_hi v185, v176, s[48:49]
	s_waitcnt lgkmcnt(0)
	s_barrier
	ds_read_b128 v[122:125], v192 offset:0
	ds_read_b64 v[126:127], v192 offset:16
	ds_read_b128 v[128:131], v192 offset:128
	ds_read_b64 v[132:133], v192 offset:144
	s_waitcnt lgkmcnt(2)
	v_mfma_f32_16x16x128_f8f6f4 v[134:137], v[122:127], v[2:7], 0 cbsz:2 blgp:2
	v_mfma_f32_16x16x128_f8f6f4 v[138:141], v[122:127], v[14:19], 0 cbsz:2 blgp:2
	v_mfma_f32_16x16x128_f8f6f4 v[142:145], v[122:127], v[26:31], v[188:191] cbsz:2 blgp:2
	v_mfma_f32_16x16x128_f8f6f4 v[204:207], v[122:127], v[38:43], 0 cbsz:2 blgp:2
	v_mfma_f32_16x16x128_f8f6f4 v[208:211], v[122:127], v[50:55], 0 cbsz:2 blgp:2
	v_mfma_f32_16x16x128_f8f6f4 v[212:215], v[122:127], v[62:67], v[188:191] cbsz:2 blgp:2
	s_waitcnt lgkmcnt(0)
	v_mfma_f32_16x16x128_f8f6f4 v[134:137], v[128:133], v[8:13], v[134:137] cbsz:2 blgp:2
	v_mfma_f32_16x16x128_f8f6f4 v[204:207], v[128:133], v[44:49], v[204:207] cbsz:2 blgp:2
	v_mfma_f32_16x16x128_f8f6f4 v[138:141], v[128:133], v[20:25], v[138:141] cbsz:2 blgp:2
	v_mfma_f32_16x16x128_f8f6f4 v[208:211], v[128:133], v[56:61], v[208:211] cbsz:2 blgp:2
	v_mfma_f32_16x16x128_f8f6f4 v[142:145], v[128:133], v[32:37], v[142:145] cbsz:2 blgp:2
	v_mfma_f32_16x16x128_f8f6f4 v[212:215], v[128:133], v[68:73], v[212:215] cbsz:2 blgp:2
	v_cndmask_b32_e64 v158, v134, v204, s[0:1]
	v_cndmask_b32_e64 v159, v138, v208, s[0:1]
	v_fma_mix_f32 v158, v158, v100, v149 op_sel_hi:[0,0,1]
	v_fma_mix_f32 v159, v159, v101, v153 op_sel_hi:[0,0,1]
	v_exp_f32_e32 v158, v158
	v_exp_f32_e32 v159, v159
	v_fma_f32 v158, v158, v186, v186
	v_add_f32_e32 v159, 1.0, v159
	v_rcp_f32_e32 v158, v158
	v_rcp_f32_e32 v159, v159
	v_cndmask_b32_e64 v160, v142, v212, s[0:1]
	v_fma_mix_f32 v161, v158, v160, v157 op_sel_hi:[0,0,1]
	v_exp_f32_e32 v161, v161
	s_add_u32 s48, s48, s40
	v_add_f32_e32 v161, 1.0, v161
	v_rcp_f32_e32 v161, v161
	s_addc_u32 s49, s49, s41
	v_fma_f32 v162, v161, -2.0, 1.0
	v_sub_f32_e32 v163, v176, v162
	v_fma_f32 v176, v159, v163, v162
	v_fma_f32 v164, |v176|, s17, v113
	v_fma_f32 v165, |v176|, s18, v114
	v_fma_f32 v166, |v176|, s19, v115
	v_lshrrev_b32_e32 v167, 26, v176
	v_min3_u32 v164, v164, v165, v166
	v_bfi_b32 v168, 31, v164, v167
	s_nop 1
	v_mul_u32_u24_dpp v170, v168, v180 quad_perm:[1,2,3,3] row_mask:0xf bank_mask:0xf bound_ctrl:1
	v_mad_u32_u24 v171, v168, v181, v170
	ds_write_b8_d16_hi v184, v171 offset:544
	s_barrier
	global_store_short_d16_hi v185, v176, s[48:49]
	s_waitcnt lgkmcnt(0)
	s_barrier
	ds_read_b128 v[122:125], v192 offset:544
	ds_read_b64 v[126:127], v192 offset:560
	ds_read_b128 v[128:131], v192 offset:672
	ds_read_b64 v[132:133], v192 offset:688
	s_add_i32 s44, s44, 16
	s_waitcnt lgkmcnt(2)
	v_mfma_f32_16x16x128_f8f6f4 v[134:137], v[122:127], v[2:7], 0 cbsz:2 blgp:2
	v_mfma_f32_16x16x128_f8f6f4 v[138:141], v[122:127], v[14:19], 0 cbsz:2 blgp:2
	v_mfma_f32_16x16x128_f8f6f4 v[142:145], v[122:127], v[26:31], v[188:191] cbsz:2 blgp:2
	v_mfma_f32_16x16x128_f8f6f4 v[204:207], v[122:127], v[38:43], 0 cbsz:2 blgp:2
	v_mfma_f32_16x16x128_f8f6f4 v[208:211], v[122:127], v[50:55], 0 cbsz:2 blgp:2
	v_mfma_f32_16x16x128_f8f6f4 v[212:215], v[122:127], v[62:67], v[188:191] cbsz:2 blgp:2
	s_waitcnt lgkmcnt(0)
	v_mfma_f32_16x16x128_f8f6f4 v[134:137], v[128:133], v[8:13], v[134:137] cbsz:2 blgp:2
	v_mfma_f32_16x16x128_f8f6f4 v[204:207], v[128:133], v[44:49], v[204:207] cbsz:2 blgp:2
	v_mfma_f32_16x16x128_f8f6f4 v[138:141], v[128:133], v[20:25], v[138:141] cbsz:2 blgp:2
	v_mfma_f32_16x16x128_f8f6f4 v[208:211], v[128:133], v[56:61], v[208:211] cbsz:2 blgp:2
	v_mfma_f32_16x16x128_f8f6f4 v[142:145], v[128:133], v[32:37], v[142:145] cbsz:2 blgp:2
	v_mfma_f32_16x16x128_f8f6f4 v[212:215], v[128:133], v[68:73], v[212:215] cbsz:2 blgp:2
	v_cndmask_b32_e64 v158, v134, v204, s[0:1]
	v_cndmask_b32_e64 v159, v138, v208, s[0:1]
	v_fma_mix_f32 v158, v158, v100, v149 op_sel:[0,0,1] op_sel_hi:[0,0,1]
	v_fma_mix_f32 v159, v159, v101, v153 op_sel:[0,0,1] op_sel_hi:[0,0,1]
	v_exp_f32_e32 v158, v158
	v_exp_f32_e32 v159, v159
	v_fma_f32 v158, v158, v186, v186
	v_add_f32_e32 v159, 1.0, v159
	v_rcp_f32_e32 v158, v158
	v_rcp_f32_e32 v159, v159
	v_cndmask_b32_e64 v160, v142, v212, s[0:1]
	v_fma_mix_f32 v161, v158, v160, v157 op_sel:[0,0,1] op_sel_hi:[0,0,1]
	v_exp_f32_e32 v161, v161
	s_add_u32 s48, s48, s40
	v_add_f32_e32 v161, 1.0, v161
	v_rcp_f32_e32 v161, v161
	s_addc_u32 s49, s49, s41
	v_fma_f32 v162, v161, -2.0, 1.0
	v_sub_f32_e32 v163, v176, v162
	v_fma_f32 v176, v159, v163, v162
	v_fma_f32 v164, |v176|, s17, v113
	v_fma_f32 v165, |v176|, s18, v114
	v_fma_f32 v166, |v176|, s19, v115
	v_lshrrev_b32_e32 v167, 26, v176
	v_min3_u32 v164, v164, v165, v166
	v_bfi_b32 v168, 31, v164, v167
	s_nop 1
	v_mul_u32_u24_dpp v170, v168, v180 quad_perm:[1,2,3,3] row_mask:0xf bank_mask:0xf bound_ctrl:1
	v_mad_u32_u24 v171, v168, v181, v170
	ds_write_b8_d16_hi v184, v171
	s_barrier
	global_store_short_d16_hi v185, v176, s[48:49]
	s_cmp_lt_i32 s44, s45
	s_cbranch_scc1 .Lscan_loop_b_f2
	s_waitcnt lgkmcnt(0)
	s_barrier

	.amdhsa_kernel _Z13fused2_kernelPKfPKtS0_S2_S0_PfPKjPKhS0_S0_S0_S3_Pj
		.amdhsa_group_segment_fixed_size 116864
		.amdhsa_private_segment_fixed_size 0
		.amdhsa_kernarg_size 104
		.amdhsa_user_sgpr_count 2
		.amdhsa_user_sgpr_dispatch_ptr 0
		.amdhsa_user_sgpr_queue_ptr 0
		.amdhsa_user_sgpr_kernarg_segment_ptr 1
		.amdhsa_user_sgpr_dispatch_id 0
		.amdhsa_user_sgpr_kernarg_preload_length 0
		.amdhsa_user_sgpr_kernarg_preload_offset 0
		.amdhsa_user_sgpr_private_segment_size 0
		.amdhsa_uses_dynamic_stack 0
		.amdhsa_enable_private_segment 0
		.amdhsa_system_sgpr_workgroup_id_x 1
		.amdhsa_system_sgpr_workgroup_id_y 0
		.amdhsa_system_sgpr_workgroup_id_z 0
		.amdhsa_system_sgpr_workgroup_info 0
		.amdhsa_system_vgpr_workitem_id 0
		.amdhsa_next_free_vgpr 238
		.amdhsa_next_free_sgpr 96
		.amdhsa_accum_offset 240
		.amdhsa_reserve_vcc 1
		.amdhsa_float_round_mode_32 0
		.amdhsa_float_round_mode_16_64 0
		.amdhsa_float_denorm_mode_32 3
		.amdhsa_float_denorm_mode_16_64 3
		.amdhsa_dx10_clamp 1
		.amdhsa_ieee_mode 1
		.amdhsa_fp16_overflow 0
		.amdhsa_tg_split 0
		.amdhsa_exception_fp_ieee_invalid_op 0
		.amdhsa_exception_fp_denorm_src 0
		.amdhsa_exception_fp_ieee_div_zero 0
		.amdhsa_exception_fp_ieee_overflow 0
		.amdhsa_exception_fp_ieee_underflow 0
		.amdhsa_exception_fp_ieee_inexact 0
		.amdhsa_exception_int_div_zero 0
	.end_amdhsa_kernel

amdhsa.kernels:
  - .agpr_count:     0
    .args:
      - .actual_access:  read_only
        .address_space:  global
        .offset:         0
        .size:           8
        .value_kind:     global_buffer
      - .actual_access:  read_only
        .address_space:  global
        .offset:         8
        .size:           8
        .value_kind:     global_buffer
      - .actual_access:  read_only
        .address_space:  global
        .offset:         16
        .size:           8
        .value_kind:     global_buffer
      - .actual_access:  read_only
        .address_space:  global
        .offset:         24
        .size:           8
        .value_kind:     global_buffer
      - .actual_access:  read_only
        .address_space:  global
        .offset:         32
        .size:           8
        .value_kind:     global_buffer
      - .actual_access:  read_only
        .address_space:  global
        .offset:         40
        .size:           8
        .value_kind:     global_buffer
      - .actual_access:  read_only
        .address_space:  global
        .offset:         48
        .size:           8
        .value_kind:     global_buffer
      - .actual_access:  read_only
        .address_space:  global
        .offset:         56
        .size:           8
        .value_kind:     global_buffer
      - .actual_access:  read_only
        .address_space:  global
        .offset:         64
        .size:           8
        .value_kind:     global_buffer
      - .actual_access:  read_only
        .address_space:  global
        .offset:         72
        .size:           8
        .value_kind:     global_buffer
      - .actual_access:  write_only
        .address_space:  global
        .offset:         80
        .size:           8
        .value_kind:     global_buffer
      - .actual_access:  write_only
        .address_space:  global
        .offset:         88
        .size:           8
        .value_kind:     global_buffer
      - .actual_access:  read_only
        .address_space:  global
        .offset:         96
        .size:           8
        .value_kind:     global_buffer
      - .actual_access:  read_only
        .address_space:  global
        .offset:         104
        .size:           8
        .value_kind:     global_buffer
      - .actual_access:  write_only
        .address_space:  global
        .offset:         112
        .size:           8
        .value_kind:     global_buffer
      - .actual_access:  write_only
        .address_space:  global
        .offset:         120
        .size:           8
        .value_kind:     global_buffer
      - .actual_access:  read_only
        .address_space:  global
        .offset:         128
        .size:           8
        .value_kind:     global_buffer
      - .actual_access:  read_only
        .address_space:  global
        .offset:         136
        .size:           8
        .value_kind:     global_buffer
      - .actual_access:  write_only
        .address_space:  global
        .offset:         144
        .size:           8
        .value_kind:     global_buffer
      - .actual_access:  write_only
        .address_space:  global
        .offset:         152
        .size:           8
        .value_kind:     global_buffer
    .group_segment_fixed_size: 0
    .kernarg_segment_align: 8
    .kernarg_segment_size: 160
    .language:       OpenCL C
    .language_version:
      - 2
      - 0
    .max_flat_workgroup_size: 256
    .name:           _Z10pre_kernelPKfS0_S0_PtS0_S0_S0_S0_S0_S0_S1_PfS0_S0_PhS2_S0_S0_S1_S1_
    .private_segment_fixed_size: 0
    .sgpr_count:     18
    .sgpr_spill_count: 0
    .symbol:         _Z10pre_kernelPKfS0_S0_PtS0_S0_S0_S0_S0_S0_S1_PfS0_S0_PhS2_S0_S0_S1_S1_.kd
    .uniform_work_group_size: 1
    .uses_dynamic_stack: false
    .vgpr_count:     24
    .vgpr_spill_count: 0
    .wavefront_size: 64
  - .agpr_count:     0
    .args:
      - .offset:         0
        .size:           4
        .value_kind:     by_value
      - .offset:         4
        .size:           4
        .value_kind:     by_value
      - .offset:         8
        .size:           4
        .value_kind:     by_value
      - .offset:         12
        .size:           4
        .value_kind:     by_value
      - .offset:         16
        .size:           4
        .value_kind:     by_value
      - .offset:         20
        .size:           4
        .value_kind:     by_value
      - .actual_access:  read_only
        .address_space:  global
        .offset:         24
        .size:           8
        .value_kind:     global_buffer
      - .actual_access:  read_only
        .address_space:  global
        .offset:         32
        .size:           8
        .value_kind:     global_buffer
      - .actual_access:  read_only
        .address_space:  global
        .offset:         40
        .size:           8
        .value_kind:     global_buffer
      - .actual_access:  read_only
        .address_space:  global
        .offset:         48
        .size:           8
        .value_kind:     global_buffer
      - .actual_access:  read_only
        .address_space:  global
        .offset:         56
        .size:           8
        .value_kind:     global_buffer
      - .address_space:  global
        .offset:         64
        .size:           8
        .value_kind:     global_buffer
      - .actual_access:  read_only
        .address_space:  global
        .offset:         72
        .size:           8
        .value_kind:     global_buffer
      - .actual_access:  read_only
        .address_space:  global
        .offset:         80
        .size:           8
        .value_kind:     global_buffer
      - .actual_access:  read_only
        .address_space:  global
        .offset:         88
        .size:           8
        .value_kind:     global_buffer
      - .actual_access:  read_only
        .address_space:  global
        .offset:         96
        .size:           8
        .value_kind:     global_buffer
      - .actual_access:  write_only
        .address_space:  global
        .offset:         104
        .size:           8
        .value_kind:     global_buffer
      - .address_space:  global
        .offset:         112
        .size:           8
        .value_kind:     global_buffer
      - .address_space:  global
        .offset:         120
        .size:           8
        .value_kind:     global_buffer
      - .offset:         128
        .size:           4
        .value_kind:     hidden_block_count_x
      - .offset:         132
        .size:           4
        .value_kind:     hidden_block_count_y
      - .offset:         136
        .size:           4
        .value_kind:     hidden_block_count_z
      - .offset:         140
        .size:           2
        .value_kind:     hidden_group_size_x
      - .offset:         142
        .size:           2
        .value_kind:     hidden_group_size_y
      - .offset:         144
        .size:           2
        .value_kind:     hidden_group_size_z
      - .offset:         146
        .size:           2
        .value_kind:     hidden_remainder_x
      - .offset:         148
        .size:           2
        .value_kind:     hidden_remainder_y
      - .offset:         150
        .size:           2
        .value_kind:     hidden_remainder_z
      - .offset:         168
        .size:           8
        .value_kind:     hidden_global_offset_x
      - .offset:         176
        .size:           8
        .value_kind:     hidden_global_offset_y
      - .offset:         184
        .size:           8
        .value_kind:     hidden_global_offset_z
      - .offset:         192
        .size:           2
        .value_kind:     hidden_grid_dims
    .group_segment_fixed_size: 29184
    .kernarg_segment_align: 8
    .kernarg_segment_size: 384
    .language:       OpenCL C
    .language_version:
      - 2
      - 0
    .max_flat_workgroup_size: 512
    .name:           _Z12stage_kerneliiiiiiPKfS0_S0_PKtS0_PjPKhS0_S0_S0_PtPfS3_
    .private_segment_fixed_size: 0
    .sgpr_count:     60
    .sgpr_spill_count: 0
    .symbol:         _Z12stage_kerneliiiiiiPKfS0_S0_PKtS0_PjPKhS0_S0_S0_PtPfS3_.kd
    .uniform_work_group_size: 1
    .uses_dynamic_stack: false
    .vgpr_count:     228
    .vgpr_spill_count: 0
    .wavefront_size: 64
  - .agpr_count:     0
    .args:
      - .actual_access:  read_only
        .address_space:  global
        .offset:         0
        .size:           8
        .value_kind:     global_buffer
      - .actual_access:  read_only
        .address_space:  global
        .offset:         8
        .size:           8
        .value_kind:     global_buffer
      - .actual_access:  read_only
        .address_space:  global
        .offset:         16
        .size:           8
        .value_kind:     global_buffer
      - .actual_access:  read_only
        .address_space:  global
        .offset:         24
        .size:           8
        .value_kind:     global_buffer
      - .actual_access:  read_only
        .address_space:  global
        .offset:         32
        .size:           8
        .value_kind:     global_buffer
      - .address_space:  global
        .offset:         40
        .size:           8
        .value_kind:     global_buffer
      - .address_space:  global
        .offset:         48
        .size:           8
        .value_kind:     global_buffer
      - .actual_access:  read_only
        .address_space:  global
        .offset:         56
        .size:           8
        .value_kind:     global_buffer
      - .actual_access:  read_only
        .address_space:  global
        .offset:         64
        .size:           8
        .value_kind:     global_buffer
      - .actual_access:  read_only
        .address_space:  global
        .offset:         72
        .size:           8
        .value_kind:     global_buffer
      - .actual_access:  read_only
        .address_space:  global
        .offset:         80
        .size:           8
        .value_kind:     global_buffer
      - .address_space:  global
        .offset:         88
        .size:           8
        .value_kind:     global_buffer
      - .address_space:  global
        .offset:         96
        .size:           8
        .value_kind:     global_buffer
    .group_segment_fixed_size: 116864
    .kernarg_segment_align: 8
    .kernarg_segment_size: 104
    .language:       OpenCL C
    .language_version:
      - 2
      - 0
    .max_flat_workgroup_size: 512
    .name:           _Z13fused2_kernelPKfPKtS0_S2_S0_PfPKjPKhS0_S0_S0_S3_Pj
    .private_segment_fixed_size: 0
    .sgpr_count:     30
    .sgpr_spill_count: 0
    .symbol:         _Z13fused2_kernelPKfPKtS0_S2_S0_PfPKjPKhS0_S0_S0_S3_Pj.kd
    .uniform_work_group_size: 1
    .uses_dynamic_stack: false
    .vgpr_count:     238
    .vgpr_spill_count: 0
    .wavefront_size: 64
  - .agpr_count:     0
    .args:
      - .actual_access:  read_only
        .address_space:  global
        .offset:         0
        .size:           8
        .value_kind:     global_buffer
      - .actual_access:  read_only
        .address_space:  global
        .offset:         8
        .size:           8
        .value_kind:     global_buffer
      - .actual_access:  read_only
        .address_space:  global
        .offset:         16
        .size:           8
        .value_kind:     global_buffer
      - .actual_access:  read_only
        .address_space:  global
        .offset:         24
        .size:           8
        .value_kind:     global_buffer
      - .actual_access:  read_only
        .address_space:  global
        .offset:         32
        .size:           8
        .value_kind:     global_buffer
      - .address_space:  global
        .offset:         40
        .size:           8
        .value_kind:     global_buffer
    .group_segment_fixed_size: 115712
    .kernarg_segment_align: 8
    .kernarg_segment_size: 48
    .language:       OpenCL C
    .language_version:
      - 2
      - 0
    .max_flat_workgroup_size: 512
    .name:           _Z17final_rest_kernelPKfPKtS0_S2_S0_Pf
    .private_segment_fixed_size: 0
    .sgpr_count:     22
    .sgpr_spill_count: 0
    .symbol:         _Z17final_rest_kernelPKfPKtS0_S2_S0_Pf.kd
    .uniform_work_group_size: 1
    .uses_dynamic_stack: false
    .vgpr_count:     226
    .vgpr_spill_count: 0
    .wavefront_size: 64
